# heads of all MFMA loops aligned to 64 bytes (padding executes once per loop entry), otherwise the 115-converter version
# speedup vs baseline: 1.0018x; 1.0015x over previous
.LBB0_335:
	s_add_u32 s4, s56, 0x20000
	s_addc_u32 s5, s57, 0
	s_lshl_b32 s2, s2, 1
	s_or_b32 s60, s2, s6
	s_lshl_b32 s2, s3, 5
	s_and_b32 s15, s2, 0x60
	s_lshl_b32 s14, s9, 13
	s_lshl_b32 s28, s15, 7
	s_add_u32 s6, s56, 0x4fb00000
	s_addc_u32 s7, s57, 0
	s_add_u32 s2, s44, 0x80
	s_addc_u32 s3, s45, 0
	v_mov_b32_e32 v2, v137
	s_waitcnt vmcnt(2)
	s_barrier
	s_add_i32 m0, s17, 0x18000
	v_bfe_u32 v3, v0, 4, 2
	global_load_lds_dwordx4 v2, s[2:3]
	v_mov_b32_e32 v2, v139
	s_add_i32 m0, s17, 0x1a000
	v_lshlrev_b32_e32 v4, 4, v3
	global_load_lds_dwordx4 v2, s[2:3]
	s_add_u32 s2, s44, 0x20080
	s_addc_u32 s3, s45, 0
	v_mov_b32_e32 v2, v137
	s_add_i32 m0, s17, 0x1c000
	v_lshlrev_b32_e32 v5, 6, v0
	global_load_lds_dwordx4 v2, s[2:3]
	v_mov_b32_e32 v2, v139
	s_add_i32 m0, s17, 0x1e000
	v_and_b32_e32 v6, 32, v200
	global_load_lds_dwordx4 v2, s[2:3]
	v_and_b32_e32 v2, 15, v0
	s_movk_i32 s2, 0x3c0
	v_and_or_b32 v5, v5, s2, v4
	v_lshl_or_b32 v141, s9, 6, v2
	v_lshl_or_b32 v2, v2, 6, v4
	v_bitop3_b32 v2, v2, s14, v6 bitop3:0xde
	v_bitop3_b32 v142, s28, v5, v6 bitop3:0xf6
	s_waitcnt vmcnt(6)
	v_cmp_eq_u32_e64 s[2:3], 0, v3
	s_cmpk_lt_u32 s8, 0x100
	v_lshl_or_b32 v143, v3, 3, s15
	v_add_u32_e32 v3, 0, v142
	v_add_u32_e32 v146, 0, v2
	v_mbcnt_lo_u32_b32 v2, -1, 0
	s_cselect_b64 s[8:9], -1, 0
	v_add_u32_e32 v144, 0x10000, v3
	v_add_u32_e32 v145, 0x14000, v3
	s_add_i32 s28, s17, 0x8000
	s_add_i32 s29, s17, 0xa000
	s_add_i32 s30, s17, 0xc000
	s_add_i32 s31, s17, 0xe000
	v_mbcnt_hi_u32_b32 v147, -1, v2
	s_mov_b64 s[14:15], s[42:43]
	s_mov_b64 s[36:37], s[44:45]
	s_barrier
	s_waitcnt vmcnt(0)
	s_branch .LBB0_338
	.p2align	6
.LBB0_336:
	s_mov_b64 s[40:41], 0
	.p2align	6

.LBB0_340:
	s_add_u32 s48, s42, 0x100
	s_addc_u32 s49, s43, 0
	s_add_u32 s62, s44, 0x100
	s_waitcnt vmcnt(8)
	s_addc_u32 s63, s45, 0
	s_waitcnt lgkmcnt(0)
	s_add_u32 s46, s44, 0x180
	s_addc_u32 s47, s45, 0
	s_barrier
	s_setprio 1
	s_waitcnt lgkmcnt(0)
	v_mfma_f32_16x16x32_bf16 v[66:69], v[2:5], v[58:61], 0
	v_mfma_f32_16x16x32_bf16 v[70:73], v[10:13], v[58:61], 0
	v_mfma_f32_16x16x32_bf16 v[74:77], v[18:21], v[58:61], 0
	v_mfma_f32_16x16x32_bf16 v[58:61], v[26:29], v[58:61], 0
	v_mfma_f32_16x16x32_bf16 v[66:69], v[6:9], v[62:65], v[66:69]
	v_mfma_f32_16x16x32_bf16 v[70:73], v[14:17], v[62:65], v[70:73]
	v_mfma_f32_16x16x32_bf16 v[74:77], v[22:25], v[62:65], v[74:77]
	v_mfma_f32_16x16x32_bf16 v[58:61], v[30:33], v[62:65], v[58:61]
	v_mfma_f32_16x16x32_bf16 v[62:65], v[2:5], v[50:53], 0
	v_mfma_f32_16x16x32_bf16 v[78:81], v[10:13], v[50:53], 0
	v_mfma_f32_16x16x32_bf16 v[82:85], v[18:21], v[50:53], 0
	v_mfma_f32_16x16x32_bf16 v[50:53], v[26:29], v[50:53], 0
	v_mfma_f32_16x16x32_bf16 v[90:93], v[18:21], v[42:45], 0
	v_mfma_f32_16x16x32_bf16 v[62:65], v[6:9], v[54:57], v[62:65]
	v_mfma_f32_16x16x32_bf16 v[78:81], v[14:17], v[54:57], v[78:81]
	v_mfma_f32_16x16x32_bf16 v[82:85], v[22:25], v[54:57], v[82:85]
	v_mfma_f32_16x16x32_bf16 v[50:53], v[30:33], v[54:57], v[50:53]
	v_mfma_f32_16x16x32_bf16 v[54:57], v[2:5], v[42:45], 0
	v_mfma_f32_16x16x32_bf16 v[86:89], v[10:13], v[42:45], 0
	v_mfma_f32_16x16x32_bf16 v[132:135], v[22:25], v[46:49], v[90:93]
	v_mfma_f32_16x16x32_bf16 v[42:45], v[26:29], v[42:45], 0
	v_mfma_f32_16x16x32_bf16 v[90:93], v[10:13], v[34:37], 0
	v_mfma_f32_16x16x32_bf16 v[54:57], v[6:9], v[46:49], v[54:57]
	v_mfma_f32_16x16x32_bf16 v[86:89], v[14:17], v[46:49], v[86:89]
	v_mfma_f32_16x16x32_bf16 v[42:45], v[30:33], v[46:49], v[42:45]
	v_mfma_f32_16x16x32_bf16 v[46:49], v[2:5], v[34:37], 0
	v_mfma_f32_16x16x32_bf16 v[148:151], v[14:17], v[38:41], v[90:93]
	v_mfma_f32_16x16x32_bf16 v[90:93], v[18:21], v[34:37], 0
	v_mfma_f32_16x16x32_bf16 v[34:37], v[26:29], v[34:37], 0
	v_mfma_f32_16x16x32_bf16 v[46:49], v[6:9], v[38:41], v[46:49]
	v_mfma_f32_16x16x32_bf16 v[34:37], v[30:33], v[38:41], v[34:37]
	v_mfma_f32_16x16x32_bf16 v[152:155], v[22:25], v[38:41], v[90:93]
	s_setprio 0
	s_barrier
	v_mov_b32_e32 v118, v137
	s_mov_b32 m0, s18
	ds_read_b128 v[38:41], v146 offset:16384
	ds_read_b128 v[90:93], v146 offset:17408
	ds_read_b128 v[94:97], v146 offset:18432
	ds_read_b128 v[98:101], v146 offset:19456
	ds_read_b128 v[102:105], v146 offset:20480
	ds_read_b128 v[106:109], v146 offset:21504
	ds_read_b128 v[110:113], v146 offset:22528
	ds_read_b128 v[114:117], v146 offset:23552
	s_nop 0
	global_load_lds_dwordx4 v118, s[62:63]
	v_mov_b32_e32 v118, v139
	s_mov_b32 m0, s19
	s_nop 0
	global_load_lds_dwordx4 v118, s[62:63]
	s_add_u32 s62, s44, 0x20100
	s_addc_u32 s63, s45, 0
	v_mov_b32_e32 v118, v137
	s_mov_b32 m0, s20
	s_nop 0
	global_load_lds_dwordx4 v118, s[62:63]
	v_mov_b32_e32 v118, v139
	s_mov_b32 m0, s21
	s_nop 0
	global_load_lds_dwordx4 v118, s[62:63]
	s_waitcnt vmcnt(6)
	s_waitcnt lgkmcnt(0)
	s_barrier
	s_setprio 1
	s_waitcnt lgkmcnt(0)
	v_mfma_f32_16x16x32_bf16 v[118:121], v[2:5], v[38:41], 0
	v_mfma_f32_16x16x32_bf16 v[156:159], v[6:9], v[90:93], v[118:121]
	v_mfma_f32_16x16x32_bf16 v[118:121], v[10:13], v[38:41], 0
	v_mfma_f32_16x16x32_bf16 v[160:163], v[14:17], v[90:93], v[118:121]
	v_mfma_f32_16x16x32_bf16 v[118:121], v[18:21], v[38:41], 0
	v_mfma_f32_16x16x32_bf16 v[38:41], v[26:29], v[38:41], 0
	v_mfma_f32_16x16x32_bf16 v[164:167], v[22:25], v[90:93], v[118:121]
	v_mfma_f32_16x16x32_bf16 v[38:41], v[30:33], v[90:93], v[38:41]
	v_mfma_f32_16x16x32_bf16 v[90:93], v[2:5], v[94:97], 0
	v_mfma_f32_16x16x32_bf16 v[168:171], v[6:9], v[98:101], v[90:93]
	v_mfma_f32_16x16x32_bf16 v[90:93], v[10:13], v[94:97], 0
	v_mfma_f32_16x16x32_bf16 v[172:175], v[14:17], v[98:101], v[90:93]
	v_mfma_f32_16x16x32_bf16 v[90:93], v[18:21], v[94:97], 0
	v_mfma_f32_16x16x32_bf16 v[176:179], v[22:25], v[98:101], v[90:93]
	v_mfma_f32_16x16x32_bf16 v[90:93], v[26:29], v[94:97], 0
	v_mfma_f32_16x16x32_bf16 v[180:183], v[30:33], v[98:101], v[90:93]
	v_mfma_f32_16x16x32_bf16 v[90:93], v[2:5], v[102:105], 0
	v_mfma_f32_16x16x32_bf16 v[184:187], v[6:9], v[106:109], v[90:93]
	v_mfma_f32_16x16x32_bf16 v[90:93], v[10:13], v[102:105], 0
	v_mfma_f32_16x16x32_bf16 v[2:5], v[2:5], v[110:113], 0
	v_mfma_f32_16x16x32_bf16 v[188:191], v[14:17], v[106:109], v[90:93]
	v_mfma_f32_16x16x32_bf16 v[90:93], v[18:21], v[102:105], 0
	v_mfma_f32_16x16x32_bf16 v[2:5], v[6:9], v[114:117], v[2:5]
	v_mfma_f32_16x16x32_bf16 v[6:9], v[10:13], v[110:113], 0
	v_mfma_f32_16x16x32_bf16 v[10:13], v[18:21], v[110:113], 0
	v_mfma_f32_16x16x32_bf16 v[192:195], v[22:25], v[106:109], v[90:93]
	v_mfma_f32_16x16x32_bf16 v[90:93], v[26:29], v[102:105], 0
	v_mfma_f32_16x16x32_bf16 v[6:9], v[14:17], v[114:117], v[6:9]
	v_mfma_f32_16x16x32_bf16 v[202:205], v[22:25], v[114:117], v[10:13]
	v_mfma_f32_16x16x32_bf16 v[10:13], v[26:29], v[110:113], 0
	v_mfma_f32_16x16x32_bf16 v[196:199], v[30:33], v[106:109], v[90:93]
	v_mfma_f32_16x16x32_bf16 v[206:209], v[30:33], v[114:117], v[10:13]
	s_setprio 0
	s_barrier
	s_add_i32 s61, 0, 0x18000
	s_add_i32 s63, 0, 0x1c000
	v_add_u32_e32 v130, s61, v142
	v_add_u32_e32 v131, s63, v142
	ds_read_b128 v[10:13], v130
	ds_read_b128 v[14:17], v130 offset:1024
	ds_read_b128 v[210:213], v130 offset:2048
	ds_read_b128 v[214:217], v130 offset:3072
	ds_read_b128 v[218:221], v131
	ds_read_b128 v[222:225], v131 offset:1024
	ds_read_b128 v[226:229], v131 offset:2048
	ds_read_b128 v[230:233], v131 offset:3072
	v_mov_b32_e32 v90, v136
	s_mov_b32 m0, s17
	ds_read_b128 v[18:21], v146 offset:32768
	ds_read_b128 v[22:25], v146 offset:33792
	ds_read_b128 v[26:29], v146 offset:34816
	ds_read_b128 v[30:33], v146 offset:35840
	ds_read_b128 v[234:237], v146 offset:36864
	ds_read_b128 v[238:241], v146 offset:37888
	ds_read_b128 v[242:245], v146 offset:38912
	ds_read_b128 v[246:249], v146 offset:39936
	s_nop 0
	global_load_lds_dwordx4 v90, s[48:49]
	v_mov_b32_e32 v90, v138
	s_mov_b32 m0, s22
	s_nop 0
	global_load_lds_dwordx4 v90, s[48:49]
	s_add_u32 s48, s42, 0x80100
	s_addc_u32 s49, s43, 0
	v_mov_b32_e32 v90, v136
	s_mov_b32 m0, s23
	s_nop 0
	global_load_lds_dwordx4 v90, s[48:49]
	v_mov_b32_e32 v90, v138
	s_mov_b32 m0, s26
	s_nop 0
	global_load_lds_dwordx4 v90, s[48:49]
	s_waitcnt vmcnt(8)
	s_waitcnt lgkmcnt(0)
	s_barrier
	s_setprio 1
	s_waitcnt lgkmcnt(0)
	v_mfma_f32_16x16x32_bf16 v[66:69], v[10:13], v[18:21], v[66:69]
	v_mfma_f32_16x16x32_bf16 v[126:129], v[14:17], v[22:25], v[66:69]
	v_mfma_f32_16x16x32_bf16 v[66:69], v[210:213], v[18:21], v[70:73]
	v_mfma_f32_16x16x32_bf16 v[122:125], v[214:217], v[22:25], v[66:69]
	v_mfma_f32_16x16x32_bf16 v[66:69], v[218:221], v[18:21], v[74:77]
	v_mfma_f32_16x16x32_bf16 v[18:21], v[226:229], v[18:21], v[58:61]
	v_mfma_f32_16x16x32_bf16 v[114:117], v[230:233], v[22:25], v[18:21]
	v_mfma_f32_16x16x32_bf16 v[18:21], v[10:13], v[26:29], v[62:65]
	v_mfma_f32_16x16x32_bf16 v[110:113], v[14:17], v[30:33], v[18:21]
	v_mfma_f32_16x16x32_bf16 v[18:21], v[210:213], v[26:29], v[78:81]
	v_mfma_f32_16x16x32_bf16 v[106:109], v[214:217], v[30:33], v[18:21]
	v_mfma_f32_16x16x32_bf16 v[18:21], v[218:221], v[26:29], v[82:85]
	v_mfma_f32_16x16x32_bf16 v[102:105], v[222:225], v[30:33], v[18:21]
	v_mfma_f32_16x16x32_bf16 v[18:21], v[226:229], v[26:29], v[50:53]
	v_mfma_f32_16x16x32_bf16 v[98:101], v[230:233], v[30:33], v[18:21]
	v_mfma_f32_16x16x32_bf16 v[18:21], v[10:13], v[234:237], v[54:57]
	v_mfma_f32_16x16x32_bf16 v[94:97], v[14:17], v[238:241], v[18:21]
	v_mfma_f32_16x16x32_bf16 v[18:21], v[210:213], v[234:237], v[86:89]
	v_mfma_f32_16x16x32_bf16 v[90:93], v[214:217], v[238:241], v[18:21]
	v_mfma_f32_16x16x32_bf16 v[18:21], v[218:221], v[234:237], v[132:135]
	v_mfma_f32_16x16x32_bf16 v[86:89], v[222:225], v[238:241], v[18:21]
	v_mfma_f32_16x16x32_bf16 v[18:21], v[226:229], v[234:237], v[42:45]
	v_mfma_f32_16x16x32_bf16 v[82:85], v[230:233], v[238:241], v[18:21]
	v_mfma_f32_16x16x32_bf16 v[18:21], v[10:13], v[242:245], v[46:49]
	v_mfma_f32_16x16x32_bf16 v[78:81], v[14:17], v[246:249], v[18:21]
	v_mfma_f32_16x16x32_bf16 v[18:21], v[210:213], v[242:245], v[148:151]
	v_mfma_f32_16x16x32_bf16 v[74:77], v[214:217], v[246:249], v[18:21]
	v_mfma_f32_16x16x32_bf16 v[18:21], v[218:221], v[242:245], v[152:155]
	v_mfma_f32_16x16x32_bf16 v[70:73], v[222:225], v[246:249], v[18:21]
	v_mfma_f32_16x16x32_bf16 v[18:21], v[226:229], v[242:245], v[34:37]
	v_mfma_f32_16x16x32_bf16 v[118:121], v[222:225], v[22:25], v[66:69]
	v_mfma_f32_16x16x32_bf16 v[66:69], v[230:233], v[246:249], v[18:21]
	s_setprio 0
	s_barrier
	v_mov_b32_e32 v34, v137
	s_add_i32 s61, s61, s16
	s_nop 1
	ds_read_b128 v[18:21], v146 offset:49152
	ds_read_b128 v[22:25], v146 offset:50176
	ds_read_b128 v[26:29], v146 offset:51200
	ds_read_b128 v[30:33], v146 offset:52224
	ds_read_b128 v[132:135], v146 offset:53248
	ds_read_b128 v[148:151], v146 offset:54272
	ds_read_b128 v[152:155], v146 offset:55296
	ds_read_b128 v[234:237], v146 offset:56320
	s_mov_b32 m0, s61
	s_add_i32 s62, s61, 0x2000
	global_load_lds_dwordx4 v34, s[46:47]
	v_mov_b32_e32 v34, v139
	s_mov_b32 m0, s62
	s_nop 0
	global_load_lds_dwordx4 v34, s[46:47]
	s_add_u32 s46, s44, 0x20180
	s_addc_u32 s47, s45, 0
	v_mov_b32_e32 v34, v137
	s_add_i32 s63, s63, s16
	s_mov_b32 m0, s63
	s_add_i32 s64, s63, 0x2000
	global_load_lds_dwordx4 v34, s[46:47]
	v_mov_b32_e32 v34, v139
	s_mov_b32 m0, s64
	s_nop 0
	global_load_lds_dwordx4 v34, s[46:47]
	s_waitcnt vmcnt(6)
	s_waitcnt lgkmcnt(0)
	s_barrier
	s_setprio 1
	s_waitcnt lgkmcnt(0)
	v_mfma_f32_16x16x32_bf16 v[34:37], v[10:13], v[18:21], v[156:159]
	v_mfma_f32_16x16x32_bf16 v[62:65], v[14:17], v[22:25], v[34:37]
	v_mfma_f32_16x16x32_bf16 v[34:37], v[210:213], v[18:21], v[160:163]
	v_mfma_f32_16x16x32_bf16 v[58:61], v[214:217], v[22:25], v[34:37]
	v_mfma_f32_16x16x32_bf16 v[34:37], v[218:221], v[18:21], v[164:167]
	v_mfma_f32_16x16x32_bf16 v[18:21], v[226:229], v[18:21], v[38:41]
	v_mfma_f32_16x16x32_bf16 v[50:53], v[230:233], v[22:25], v[18:21]
	v_mfma_f32_16x16x32_bf16 v[18:21], v[10:13], v[26:29], v[168:171]
	v_mfma_f32_16x16x32_bf16 v[46:49], v[14:17], v[30:33], v[18:21]
	v_mfma_f32_16x16x32_bf16 v[18:21], v[210:213], v[26:29], v[172:175]
	v_mfma_f32_16x16x32_bf16 v[42:45], v[214:217], v[30:33], v[18:21]
	v_mfma_f32_16x16x32_bf16 v[18:21], v[218:221], v[26:29], v[176:179]
	v_mfma_f32_16x16x32_bf16 v[38:41], v[222:225], v[30:33], v[18:21]
	v_mfma_f32_16x16x32_bf16 v[18:21], v[226:229], v[26:29], v[180:183]
	v_mfma_f32_16x16x32_bf16 v[54:57], v[222:225], v[22:25], v[34:37]
	v_mfma_f32_16x16x32_bf16 v[34:37], v[230:233], v[30:33], v[18:21]
	v_mfma_f32_16x16x32_bf16 v[18:21], v[10:13], v[132:135], v[184:187]
	v_mfma_f32_16x16x32_bf16 v[2:5], v[10:13], v[152:155], v[2:5]
	v_mfma_f32_16x16x32_bf16 v[30:33], v[14:17], v[148:151], v[18:21]
	v_mfma_f32_16x16x32_bf16 v[18:21], v[210:213], v[132:135], v[188:191]
	v_mfma_f32_16x16x32_bf16 v[14:17], v[14:17], v[234:237], v[2:5]
	v_mfma_f32_16x16x32_bf16 v[2:5], v[210:213], v[152:155], v[6:9]
	v_mfma_f32_16x16x32_bf16 v[26:29], v[214:217], v[148:151], v[18:21]
	v_mfma_f32_16x16x32_bf16 v[18:21], v[218:221], v[132:135], v[192:195]
	v_mfma_f32_16x16x32_bf16 v[10:13], v[214:217], v[234:237], v[2:5]
	v_mfma_f32_16x16x32_bf16 v[2:5], v[218:221], v[152:155], v[202:205]
	v_mfma_f32_16x16x32_bf16 v[22:25], v[222:225], v[148:151], v[18:21]
	v_mfma_f32_16x16x32_bf16 v[18:21], v[226:229], v[132:135], v[196:199]
	v_mfma_f32_16x16x32_bf16 v[6:9], v[222:225], v[234:237], v[2:5]
	v_mfma_f32_16x16x32_bf16 v[2:5], v[226:229], v[152:155], v[206:209]
	v_mfma_f32_16x16x32_bf16 v[18:21], v[230:233], v[148:151], v[18:21]
	v_mfma_f32_16x16x32_bf16 v[2:5], v[230:233], v[234:237], v[2:5]
	s_setprio 0
	s_barrier
	s_add_u32 s46, s42, 0x100
	s_addc_u32 s47, s43, 0
	s_add_u32 s65, s44, 0x200
	s_addc_u32 s66, s45, 0
	s_mov_b32 s67, 0
	.p2align	6

.LBB0_531:
	s_waitcnt vmcnt(8)
	s_waitcnt lgkmcnt(0)
	s_barrier
	s_setprio 1
	v_mfma_i32_16x16x64_i8 v[18:21], v[158:161], v[190:193], 0
	s_nop 0
	v_mfma_i32_16x16x64_i8 v[18:21], v[154:157], v[186:189], v[18:21]
	v_mfma_i32_16x16x64_i8 v[22:25], v[150:153], v[190:193], 0
	s_nop 0
	v_mfma_i32_16x16x64_i8 v[22:25], v[142:145], v[186:189], v[22:25]
	v_mfma_i32_16x16x64_i8 v[26:29], v[146:149], v[190:193], 0
	s_nop 0
	v_mfma_i32_16x16x64_i8 v[26:29], v[138:141], v[186:189], v[26:29]
	v_mfma_i32_16x16x64_i8 v[34:37], v[134:137], v[190:193], 0
	s_nop 0
	v_mfma_i32_16x16x64_i8 v[34:37], v[130:133], v[186:189], v[34:37]
	v_mfma_i32_16x16x64_i8 v[50:53], v[158:161], v[182:185], 0
	s_nop 0
	v_mfma_i32_16x16x64_i8 v[50:53], v[154:157], v[178:181], v[50:53]
	v_mfma_i32_16x16x64_i8 v[62:65], v[150:153], v[182:185], 0
	s_nop 0
	v_mfma_i32_16x16x64_i8 v[62:65], v[142:145], v[178:181], v[62:65]
	v_mfma_i32_16x16x64_i8 v[54:57], v[146:149], v[182:185], 0
	s_nop 0
	v_mfma_i32_16x16x64_i8 v[54:57], v[138:141], v[178:181], v[54:57]
	v_mfma_i32_16x16x64_i8 v[66:69], v[134:137], v[182:185], 0
	s_nop 0
	v_mfma_i32_16x16x64_i8 v[66:69], v[130:133], v[178:181], v[66:69]
	v_mfma_i32_16x16x64_i8 v[82:85], v[158:161], v[174:177], 0
	s_nop 0
	v_mfma_i32_16x16x64_i8 v[82:85], v[154:157], v[170:173], v[82:85]
	v_mfma_i32_16x16x64_i8 v[94:97], v[150:153], v[174:177], 0
	s_nop 0
	v_mfma_i32_16x16x64_i8 v[94:97], v[142:145], v[170:173], v[94:97]
	v_mfma_i32_16x16x64_i8 v[86:89], v[146:149], v[174:177], 0
	s_nop 0
	v_mfma_i32_16x16x64_i8 v[86:89], v[138:141], v[170:173], v[86:89]
	v_mfma_i32_16x16x64_i8 v[98:101], v[134:137], v[174:177], 0
	s_nop 0
	v_mfma_i32_16x16x64_i8 v[98:101], v[130:133], v[170:173], v[98:101]
	v_mfma_i32_16x16x64_i8 v[114:117], v[158:161], v[166:169], 0
	s_nop 0
	v_mfma_i32_16x16x64_i8 v[114:117], v[154:157], v[162:165], v[114:117]
	v_mfma_i32_16x16x64_i8 v[122:125], v[150:153], v[166:169], 0
	s_nop 0
	v_mfma_i32_16x16x64_i8 v[122:125], v[142:145], v[162:165], v[122:125]
	v_mfma_i32_16x16x64_i8 v[118:121], v[146:149], v[166:169], 0
	s_nop 0
	v_mfma_i32_16x16x64_i8 v[118:121], v[138:141], v[162:165], v[118:121]
	v_mfma_i32_16x16x64_i8 v[126:129], v[134:137], v[166:169], 0
	s_nop 0
	v_mfma_i32_16x16x64_i8 v[126:129], v[130:133], v[162:165], v[126:129]
	s_setprio 0
	s_barrier
	s_add_u32 s63, s35, s66
	s_addc_u32 s69, s60, s67
	s_cmp_eq_u32 s49, 12
	s_cselect_b64 s[82:83], -1, 0
	s_and_b64 s[70:71], s[82:83], exec
	s_cselect_b32 s79, s79, s69
	s_cselect_b32 s78, s78, s63
	s_mov_b64 s[70:71], s[78:79]
	v_mov_b32_e32 v205, v197
	s_mov_b32 m0, s19
	s_waitcnt lgkmcnt(0)
	ds_read_b128 v[190:193], v204 offset:16384
	ds_read_b128 v[186:189], v204 offset:17408
	ds_read_b128 v[182:185], v204 offset:18432
	ds_read_b128 v[178:181], v204 offset:19456
	ds_read_b128 v[174:177], v204 offset:20480
	ds_read_b128 v[170:173], v204 offset:21504
	ds_read_b128 v[166:169], v204 offset:22528
	ds_read_b128 v[162:165], v204 offset:23552
	s_nop 0
	global_load_lds_dwordx4 v205, s[70:71]
	v_mov_b32_e32 v205, v199
	s_mov_b32 m0, s20
	s_nop 0
	global_load_lds_dwordx4 v205, s[70:71]
	s_add_u32 s70, s78, 0x40000
	s_addc_u32 s71, s79, 0
	v_mov_b32_e32 v205, v197
	s_mov_b32 m0, s21
	s_nop 0
	global_load_lds_dwordx4 v205, s[70:71]
	v_mov_b32_e32 v205, v199
	s_mov_b32 m0, s22
	s_nop 0
	global_load_lds_dwordx4 v205, s[70:71]
	s_waitcnt vmcnt(6)
	s_waitcnt lgkmcnt(0)
	s_barrier
	s_setprio 1
	v_mfma_i32_16x16x64_i8 v[2:5], v[158:161], v[190:193], 0
	s_nop 0
	v_mfma_i32_16x16x64_i8 v[2:5], v[154:157], v[186:189], v[2:5]
	v_mfma_i32_16x16x64_i8 v[6:9], v[150:153], v[190:193], 0
	s_nop 0
	v_mfma_i32_16x16x64_i8 v[6:9], v[142:145], v[186:189], v[6:9]
	v_mfma_i32_16x16x64_i8 v[10:13], v[146:149], v[190:193], 0
	s_nop 0
	v_mfma_i32_16x16x64_i8 v[10:13], v[138:141], v[186:189], v[10:13]
	v_mfma_i32_16x16x64_i8 v[14:17], v[134:137], v[190:193], 0
	s_nop 0
	v_mfma_i32_16x16x64_i8 v[14:17], v[130:133], v[186:189], v[14:17]
	v_mfma_i32_16x16x64_i8 v[30:33], v[158:161], v[182:185], 0
	s_nop 0
	v_mfma_i32_16x16x64_i8 v[30:33], v[154:157], v[178:181], v[30:33]
	v_mfma_i32_16x16x64_i8 v[42:45], v[150:153], v[182:185], 0
	s_nop 0
	v_mfma_i32_16x16x64_i8 v[42:45], v[142:145], v[178:181], v[42:45]
	v_mfma_i32_16x16x64_i8 v[38:41], v[146:149], v[182:185], 0
	s_nop 0
	v_mfma_i32_16x16x64_i8 v[38:41], v[138:141], v[178:181], v[38:41]
	v_mfma_i32_16x16x64_i8 v[46:49], v[134:137], v[182:185], 0
	s_nop 0
	v_mfma_i32_16x16x64_i8 v[46:49], v[130:133], v[178:181], v[46:49]
	v_mfma_i32_16x16x64_i8 v[58:61], v[158:161], v[174:177], 0
	s_nop 0
	v_mfma_i32_16x16x64_i8 v[58:61], v[154:157], v[170:173], v[58:61]
	v_mfma_i32_16x16x64_i8 v[74:77], v[150:153], v[174:177], 0
	s_nop 0
	v_mfma_i32_16x16x64_i8 v[74:77], v[142:145], v[170:173], v[74:77]
	v_mfma_i32_16x16x64_i8 v[70:73], v[146:149], v[174:177], 0
	s_nop 0
	v_mfma_i32_16x16x64_i8 v[70:73], v[138:141], v[170:173], v[70:73]
	v_mfma_i32_16x16x64_i8 v[78:81], v[134:137], v[174:177], 0
	s_nop 0
	v_mfma_i32_16x16x64_i8 v[78:81], v[130:133], v[170:173], v[78:81]
	v_mfma_i32_16x16x64_i8 v[90:93], v[158:161], v[166:169], 0
	s_nop 0
	v_mfma_i32_16x16x64_i8 v[90:93], v[154:157], v[162:165], v[90:93]
	v_mfma_i32_16x16x64_i8 v[106:109], v[150:153], v[166:169], 0
	s_nop 0
	v_mfma_i32_16x16x64_i8 v[106:109], v[142:145], v[162:165], v[106:109]
	v_mfma_i32_16x16x64_i8 v[102:105], v[146:149], v[166:169], 0
	s_nop 0
	v_mfma_i32_16x16x64_i8 v[102:105], v[138:141], v[162:165], v[102:105]
	v_mfma_i32_16x16x64_i8 v[110:113], v[134:137], v[166:169], 0
	s_nop 0
	v_mfma_i32_16x16x64_i8 v[110:113], v[130:133], v[162:165], v[110:113]
	s_setprio 0
	s_barrier
	s_add_u32 s51, s51, 0x100
	s_addc_u32 s69, s62, 0
	s_and_b64 s[62:63], s[82:83], exec
	s_cselect_b32 s63, s77, s69
	s_cselect_b32 s62, s76, s51
	s_add_u32 s76, s78, 0x80
	s_addc_u32 s77, s79, 0
	s_add_i32 s51, 0, 0x18000
	s_add_i32 s69, 0, 0x1c000
	v_add_u32_e32 v130, s51, v202
	v_add_u32_e32 v131, s69, v202
	ds_read_b128 v[158:161], v130
	ds_read_b128 v[154:157], v130 offset:1024
	ds_read_b128 v[150:153], v130 offset:2048
	ds_read_b128 v[146:149], v130 offset:3072
	ds_read_b128 v[142:145], v131
	ds_read_b128 v[138:141], v131 offset:1024
	ds_read_b128 v[134:137], v131 offset:2048
	ds_read_b128 v[130:133], v131 offset:3072
	s_mov_b64 s[70:71], s[62:63]
	v_mov_b32_e32 v205, v196
	s_mov_b32 m0, s1
	s_waitcnt lgkmcnt(0)
	ds_read_b128 v[162:165], v204 offset:32768
	ds_read_b128 v[166:169], v204 offset:33792
	ds_read_b128 v[170:173], v204 offset:34816
	ds_read_b128 v[174:177], v204 offset:35840
	ds_read_b128 v[178:181], v204 offset:36864
	ds_read_b128 v[182:185], v204 offset:37888
	ds_read_b128 v[186:189], v204 offset:38912
	ds_read_b128 v[190:193], v204 offset:39936
	s_add_u32 s62, s62, 0x40000
	global_load_lds_dwordx4 v205, s[70:71]
	v_mov_b32_e32 v205, v198
	s_mov_b32 m0, s23
	s_addc_u32 s63, s63, 0
	global_load_lds_dwordx4 v205, s[70:71]
	v_mov_b32_e32 v205, v196
	s_mov_b32 m0, s26
	s_nop 0
	global_load_lds_dwordx4 v205, s[62:63]
	v_mov_b32_e32 v205, v198
	s_mov_b32 m0, s27
	s_nop 0
	global_load_lds_dwordx4 v205, s[62:63]
	s_waitcnt vmcnt(8)
	s_waitcnt lgkmcnt(0)
	s_barrier
	s_setprio 1
	s_waitcnt lgkmcnt(0)
	v_mfma_i32_16x16x64_i8 v[18:21], v[158:161], v[162:165], v[18:21]
	s_nop 0
	v_mfma_i32_16x16x64_i8 v[18:21], v[154:157], v[166:169], v[18:21]
	v_mfma_i32_16x16x64_i8 v[22:25], v[150:153], v[162:165], v[22:25]
	s_nop 0
	v_mfma_i32_16x16x64_i8 v[22:25], v[146:149], v[166:169], v[22:25]
	v_mfma_i32_16x16x64_i8 v[26:29], v[142:145], v[162:165], v[26:29]
	s_nop 0
	v_mfma_i32_16x16x64_i8 v[26:29], v[138:141], v[166:169], v[26:29]
	v_mfma_i32_16x16x64_i8 v[34:37], v[134:137], v[162:165], v[34:37]
	s_nop 0
	v_mfma_i32_16x16x64_i8 v[34:37], v[130:133], v[166:169], v[34:37]
	v_mfma_i32_16x16x64_i8 v[50:53], v[158:161], v[170:173], v[50:53]
	s_nop 0
	v_mfma_i32_16x16x64_i8 v[50:53], v[154:157], v[174:177], v[50:53]
	v_mfma_i32_16x16x64_i8 v[62:65], v[150:153], v[170:173], v[62:65]
	s_nop 0
	v_mfma_i32_16x16x64_i8 v[62:65], v[146:149], v[174:177], v[62:65]
	v_mfma_i32_16x16x64_i8 v[54:57], v[142:145], v[170:173], v[54:57]
	s_nop 0
	v_mfma_i32_16x16x64_i8 v[54:57], v[138:141], v[174:177], v[54:57]
	v_mfma_i32_16x16x64_i8 v[66:69], v[134:137], v[170:173], v[66:69]
	s_nop 0
	v_mfma_i32_16x16x64_i8 v[66:69], v[130:133], v[174:177], v[66:69]
	v_mfma_i32_16x16x64_i8 v[82:85], v[158:161], v[178:181], v[82:85]
	s_nop 0
	v_mfma_i32_16x16x64_i8 v[82:85], v[154:157], v[182:185], v[82:85]
	v_mfma_i32_16x16x64_i8 v[94:97], v[150:153], v[178:181], v[94:97]
	s_nop 0
	v_mfma_i32_16x16x64_i8 v[94:97], v[146:149], v[182:185], v[94:97]
	v_mfma_i32_16x16x64_i8 v[86:89], v[142:145], v[178:181], v[86:89]
	s_nop 0
	v_mfma_i32_16x16x64_i8 v[86:89], v[138:141], v[182:185], v[86:89]
	v_mfma_i32_16x16x64_i8 v[98:101], v[134:137], v[178:181], v[98:101]
	s_nop 0
	v_mfma_i32_16x16x64_i8 v[98:101], v[130:133], v[182:185], v[98:101]
	v_mfma_i32_16x16x64_i8 v[114:117], v[158:161], v[186:189], v[114:117]
	s_nop 0
	v_mfma_i32_16x16x64_i8 v[114:117], v[154:157], v[190:193], v[114:117]
	v_mfma_i32_16x16x64_i8 v[122:125], v[150:153], v[186:189], v[122:125]
	s_nop 0
	v_mfma_i32_16x16x64_i8 v[122:125], v[146:149], v[190:193], v[122:125]
	v_mfma_i32_16x16x64_i8 v[118:121], v[142:145], v[186:189], v[118:121]
	s_nop 0
	v_mfma_i32_16x16x64_i8 v[118:121], v[138:141], v[190:193], v[118:121]
	v_mfma_i32_16x16x64_i8 v[126:129], v[134:137], v[186:189], v[126:129]
	s_nop 0
	v_mfma_i32_16x16x64_i8 v[126:129], v[130:133], v[190:193], v[126:129]
	s_setprio 0
	s_barrier
	v_mov_b32_e32 v205, v197
	s_add_i32 s51, s51, s10
	ds_read_b128 v[162:165], v204 offset:49152
	ds_read_b128 v[166:169], v204 offset:50176
	ds_read_b128 v[170:173], v204 offset:51200
	ds_read_b128 v[174:177], v204 offset:52224
	ds_read_b128 v[178:181], v204 offset:53248
	ds_read_b128 v[182:185], v204 offset:54272
	ds_read_b128 v[186:189], v204 offset:55296
	ds_read_b128 v[190:193], v204 offset:56320
	s_mov_b32 m0, s51
	s_nop 0
	global_load_lds_dwordx4 v205, s[76:77]
	v_mov_b32_e32 v205, v199
	s_add_i32 m0, s51, 0x2000
	s_add_u32 s62, s78, 0x40080
	global_load_lds_dwordx4 v205, s[76:77]
	s_addc_u32 s63, s79, 0
	v_mov_b32_e32 v205, v197
	s_add_i32 s51, s69, s10
	s_mov_b32 m0, s51
	s_nop 0
	global_load_lds_dwordx4 v205, s[62:63]
	v_mov_b32_e32 v205, v199
	s_add_i32 m0, s51, 0x2000
	s_nop 0
	global_load_lds_dwordx4 v205, s[62:63]
	s_waitcnt vmcnt(6)
	s_waitcnt lgkmcnt(0)
	s_barrier
	s_setprio 1
	s_waitcnt lgkmcnt(0)
	v_mfma_i32_16x16x64_i8 v[2:5], v[158:161], v[162:165], v[2:5]
	s_nop 0
	v_mfma_i32_16x16x64_i8 v[2:5], v[154:157], v[166:169], v[2:5]
	v_mfma_i32_16x16x64_i8 v[6:9], v[150:153], v[162:165], v[6:9]
	s_nop 0
	v_mfma_i32_16x16x64_i8 v[6:9], v[146:149], v[166:169], v[6:9]
	v_mfma_i32_16x16x64_i8 v[10:13], v[142:145], v[162:165], v[10:13]
	s_nop 0
	v_mfma_i32_16x16x64_i8 v[10:13], v[138:141], v[166:169], v[10:13]
	v_mfma_i32_16x16x64_i8 v[14:17], v[134:137], v[162:165], v[14:17]
	s_nop 0
	v_mfma_i32_16x16x64_i8 v[14:17], v[130:133], v[166:169], v[14:17]
	v_mfma_i32_16x16x64_i8 v[30:33], v[158:161], v[170:173], v[30:33]
	s_nop 0
	v_mfma_i32_16x16x64_i8 v[30:33], v[154:157], v[174:177], v[30:33]
	v_mfma_i32_16x16x64_i8 v[42:45], v[150:153], v[170:173], v[42:45]
	s_nop 0
	v_mfma_i32_16x16x64_i8 v[42:45], v[146:149], v[174:177], v[42:45]
	v_mfma_i32_16x16x64_i8 v[38:41], v[142:145], v[170:173], v[38:41]
	s_nop 0
	v_mfma_i32_16x16x64_i8 v[38:41], v[138:141], v[174:177], v[38:41]
	v_mfma_i32_16x16x64_i8 v[46:49], v[134:137], v[170:173], v[46:49]
	s_nop 0
	v_mfma_i32_16x16x64_i8 v[46:49], v[130:133], v[174:177], v[46:49]
	v_mfma_i32_16x16x64_i8 v[58:61], v[158:161], v[178:181], v[58:61]
	s_nop 0
	v_mfma_i32_16x16x64_i8 v[58:61], v[154:157], v[182:185], v[58:61]
	v_mfma_i32_16x16x64_i8 v[74:77], v[150:153], v[178:181], v[74:77]
	s_nop 0
	v_mfma_i32_16x16x64_i8 v[74:77], v[146:149], v[182:185], v[74:77]
	v_mfma_i32_16x16x64_i8 v[70:73], v[142:145], v[178:181], v[70:73]
	s_nop 0
	v_mfma_i32_16x16x64_i8 v[70:73], v[138:141], v[182:185], v[70:73]
	v_mfma_i32_16x16x64_i8 v[78:81], v[134:137], v[178:181], v[78:81]
	s_nop 0
	v_mfma_i32_16x16x64_i8 v[78:81], v[130:133], v[182:185], v[78:81]
	v_mfma_i32_16x16x64_i8 v[90:93], v[158:161], v[186:189], v[90:93]
	s_nop 0
	v_mfma_i32_16x16x64_i8 v[90:93], v[154:157], v[190:193], v[90:93]
	v_mfma_i32_16x16x64_i8 v[106:109], v[150:153], v[186:189], v[106:109]
	s_nop 0
	v_mfma_i32_16x16x64_i8 v[106:109], v[146:149], v[190:193], v[106:109]
	v_mfma_i32_16x16x64_i8 v[102:105], v[142:145], v[186:189], v[102:105]
	s_nop 0
	v_mfma_i32_16x16x64_i8 v[102:105], v[138:141], v[190:193], v[102:105]
	v_mfma_i32_16x16x64_i8 v[110:113], v[134:137], v[186:189], v[110:113]
	s_nop 0
	v_mfma_i32_16x16x64_i8 v[110:113], v[130:133], v[190:193], v[110:113]
	s_setprio 0
	s_barrier
	s_add_i32 s49, s49, 2
	s_add_u32 s66, s66, 0x100
	s_addc_u32 s67, s67, 0
	s_cmp_gt_u32 s49, 13
	s_cbranch_scc1 .LBB0_541
	s_mov_b64 s[78:79], s[8:9]
	s_mov_b64 s[76:77], s[40:41]
	.p2align	6

.LBB0_614:
	s_lshl_b32 s8, s30, 6
	s_and_b32 s33, s8, 0x1fc0
	s_bfe_u32 s23, s30, 0x20007
	s_sub_i32 s8, 0x80, s33
	s_lshl_b32 s0, s23, 8
	s_and_b32 s22, s18, 0x1fc0
	s_ashr_i32 s14, s30, 9
	s_waitcnt vmcnt(4)
	v_sub_co_u32_e32 v54, vcc, s33, v184
	s_ashr_i32 s15, s8, 6
	s_and_b64 s[8:9], vcc, exec
	s_cselect_b32 s31, s15, 0
	s_ashr_i32 s15, s14, 31
	s_lshl_b64 s[8:9], s[14:15], 13
	v_or_b32_e32 v2, s33, v155
	s_lshl_b32 s35, s23, 2
	v_mov_b64_e32 v[50:51], s[36:37]
	v_or_b32_e32 v144, s8, v2
	s_add_i32 s35, s35, s16
	v_mad_u64_u32 v[2:3], s[42:43], v144, s20, v[50:51]
	v_mad_i32_i24 v3, s9, v185, v3
	s_lshl_b32 s42, s35, 8
	s_mov_b32 s43, s1
	v_lshl_add_u64 v[2:3], v[2:3], 0, s[42:43]
	v_mov_b32_e32 v143, v131
	v_lshl_add_u64 v[52:53], v[2:3], 0, v[142:143]
	global_load_dwordx4 v[58:61], v[52:53], off offset:224
	global_load_dwordx4 v[66:69], v[52:53], off offset:192
	global_load_dwordx4 v[74:77], v[52:53], off offset:160
	global_load_dwordx4 v[98:101], v[52:53], off offset:128
	global_load_dwordx4 v[42:45], v[134:135], off offset:16
	global_load_dwordx4 v[46:49], v[134:135], off
	global_load_dwordx4 v[34:37], v[134:135], off offset:80
	global_load_dwordx4 v[38:41], v[134:135], off offset:64
	global_load_dwordx4 v[26:29], v[134:135], off offset:144
	global_load_dwordx4 v[30:33], v[134:135], off offset:128
	global_load_dwordx4 v[18:21], v[134:135], off offset:208
	global_load_dwordx4 v[22:25], v[134:135], off offset:192
	global_load_dwordx4 v[10:13], v[134:135], off offset:272
	global_load_dwordx4 v[14:17], v[134:135], off offset:256
	global_load_dwordx4 v[2:5], v[134:135], off offset:336
	global_load_dwordx4 v[6:9], v[134:135], off offset:320
	global_load_dwordx4 v[102:105], v[52:53], off offset:64
	global_load_dwordx4 v[106:109], v[52:53], off offset:96
	global_load_dwordx4 v[110:113], v[52:53], off
	global_load_dwordx4 v[116:119], v[52:53], off offset:32
	s_mul_i32 s15, s23, 0x1800
	s_sub_i32 s23, 0x2040, s33
	s_lshr_b32 s33, s23, 6
	s_lshl_b32 s23, s31, 6
	v_add_u32_e32 v55, s23, v54
	v_or_b32_e32 v54, v55, v154
	v_or_b32_e32 v56, v55, v161
	v_ashrrev_i32_e32 v55, 31, v54
	v_ashrrev_i32_e32 v57, 31, v56
	v_lshl_add_u64 v[54:55], s[8:9], 0, v[54:55]
	v_lshl_add_u64 v[56:57], s[8:9], 0, v[56:57]
	s_waitcnt vmcnt(22)
	v_mad_u64_u32 v[62:63], s[42:43], v54, s20, v[50:51]
	v_mad_u64_u32 v[50:51], s[42:43], v56, s20, v[50:51]
	v_mad_i32_i24 v63, v55, s20, v63
	v_mad_i32_i24 v51, v57, s20, v51
	v_lshl_add_u64 v[52:53], v[62:63], 0, s[0:1]
	v_mov_b32_e32 v141, v131
	v_lshl_add_u64 v[50:51], v[50:51], 0, s[0:1]
	v_lshl_add_u64 v[52:53], v[52:53], 0, s[2:3]
	v_lshl_add_u64 v[50:51], v[50:51], 0, s[2:3]
	v_lshl_add_u64 v[54:55], v[52:53], 0, v[130:131]
	v_lshl_add_u64 v[52:53], v[52:53], 0, v[140:141]
	s_mov_b32 m0, s21
	v_lshl_add_u64 v[56:57], v[50:51], 0, v[130:131]
	v_lshl_add_u64 v[50:51], v[50:51], 0, v[140:141]
	v_lshl_add_u64 v[52:53], v[52:53], 0, s[4:5]
	global_load_dwordx4 v[90:93], v[54:55], off
	global_load_dwordx4 v[94:97], v[56:57], off
	v_lshl_add_u64 v[50:51], v[50:51], 0, s[4:5]
	global_load_lds_dwordx4 v[52:53], off
	s_mov_b32 m0, s26
	s_lshl_b32 s8, s35, 7
	global_load_lds_dwordx4 v[50:51], off
	s_lshl_b32 s35, s35, 2
	v_readlane_b32 s60, v251, 11
	v_readlane_b32 s74, v251, 25
	v_readlane_b32 s75, v251, 26
	s_add_i32 s22, s22, s23
	v_mov_b32_e32 v145, s9
	s_mov_b32 s9, s1
	s_min_u32 s33, s33, 4
	v_mov_b32_e32 v143, v156
	v_readlane_b32 s61, v251, 12
	v_readlane_b32 s62, v251, 13
	v_readlane_b32 s63, v251, 14
	v_readlane_b32 s64, v251, 15
	v_readlane_b32 s65, v251, 16
	v_readlane_b32 s66, v251, 17
	v_readlane_b32 s67, v251, 18
	v_readlane_b32 s68, v251, 19
	v_readlane_b32 s69, v251, 20
	v_readlane_b32 s70, v251, 21
	v_readlane_b32 s71, v251, 22
	v_readlane_b32 s72, v251, 23
	v_readlane_b32 s73, v251, 24
	s_waitcnt vmcnt(0)
	v_lshlrev_b32_e32 v54, 16, v59
	v_and_b32_e32 v63, 0xffff0000, v67
	v_lshlrev_b32_e32 v62, 16, v67
	v_mul_f32_e32 v64, v63, v63
	v_and_b32_e32 v195, 0xffff0000, v105
	v_lshlrev_b32_e32 v114, 16, v109
	v_and_b32_e32 v115, 0xffff0000, v109
	v_and_b32_e32 v109, 0xffff0000, v104
	v_lshlrev_b32_e32 v188, 16, v108
	v_and_b32_e32 v189, 0xffff0000, v108
	v_lshlrev_b32_e32 v194, 16, v105
	v_lshlrev_b32_e32 v108, 16, v104
	v_mov_b32_e32 v148, v195
	v_mov_b32_e32 v149, v109
	v_mov_b32_e32 v104, v194
	v_mov_b32_e32 v105, v108
	v_pk_mul_f32 v[148:149], v[148:149], v[148:149]
	v_and_b32_e32 v197, 0xffff0000, v103
	v_and_b32_e32 v199, 0xffff0000, v102
	v_pk_fma_f32 v[104:105], v[104:105], v[104:105], v[148:149]
	v_lshlrev_b32_e32 v196, 16, v103
	v_lshlrev_b32_e32 v198, 16, v102
	v_mov_b32_e32 v148, v199
	v_mov_b32_e32 v149, v197
	v_pk_fma_f32 v[124:125], v[62:63], v[62:63], v[64:65] op_sel_hi:[1,1,0]
	v_and_b32_e32 v65, 0xffff0000, v66
	v_mov_b32_e32 v102, v198
	v_mov_b32_e32 v103, v196
	v_pk_mul_f32 v[148:149], v[148:149], v[148:149]
	v_lshlrev_b32_e32 v64, 16, v66
	v_mul_f32_e32 v66, v65, v65
	v_pk_fma_f32 v[102:103], v[102:103], v[102:103], v[148:149]
	v_and_b32_e32 v55, 0xffff0000, v59
	v_lshlrev_b32_e32 v56, 16, v58
	v_and_b32_e32 v57, 0xffff0000, v58
	v_lshlrev_b32_e32 v58, 16, v69
	v_and_b32_e32 v59, 0xffff0000, v69
	v_pk_fma_f32 v[126:127], v[64:65], v[64:65], v[66:67] op_sel_hi:[1,1,0]
	v_and_b32_e32 v67, 0xffff0000, v77
	v_and_b32_e32 v69, 0xffff0000, v76
	v_pk_add_f32 v[102:103], v[102:103], v[102:103] op_sel:[0,1] op_sel_hi:[1,0]
	v_lshlrev_b32_e32 v50, 16, v61
	v_and_b32_e32 v51, 0xffff0000, v61
	v_lshlrev_b32_e32 v52, 16, v60
	v_and_b32_e32 v53, 0xffff0000, v60
	v_lshlrev_b32_e32 v60, 16, v68
	v_and_b32_e32 v61, 0xffff0000, v68
	v_lshlrev_b32_e32 v66, 16, v77
	v_lshlrev_b32_e32 v68, 16, v76
	v_mov_b32_e32 v72, v67
	v_mov_b32_e32 v73, v69
	v_pk_add_f32 v[102:103], v[104:105], v[102:103] op_sel:[1,0] op_sel_hi:[0,1]
	v_mov_b32_e32 v70, v66
	v_mov_b32_e32 v71, v68
	v_pk_mul_f32 v[72:73], v[72:73], v[72:73]
	v_pk_add_f32 v[102:103], v[104:105], v[102:103]
	v_lshlrev_b32_e32 v202, 16, v119
	v_and_b32_e32 v203, 0xffff0000, v119
	v_lshlrev_b32_e32 v104, 16, v118
	v_and_b32_e32 v105, 0xffff0000, v118
	v_lshlrev_b32_e32 v118, 16, v117
	v_and_b32_e32 v119, 0xffff0000, v117
	v_and_b32_e32 v117, 0xffff0000, v113
	v_pk_fma_f32 v[76:77], v[70:71], v[70:71], v[72:73]
	v_and_b32_e32 v71, 0xffff0000, v75
	v_and_b32_e32 v73, 0xffff0000, v74
	v_lshlrev_b32_e32 v204, 16, v116
	v_and_b32_e32 v205, 0xffff0000, v116
	v_lshlrev_b32_e32 v116, 16, v113
	v_and_b32_e32 v207, 0xffff0000, v112
	v_mov_b32_e32 v148, v117
	v_mov_b32_e32 v149, v203
	v_lshlrev_b32_e32 v70, 16, v75
	v_lshlrev_b32_e32 v72, 16, v74
	v_mov_b32_e32 v78, v73
	v_mov_b32_e32 v79, v71
	v_lshlrev_b32_e32 v206, 16, v112
	v_lshlrev_b32_e32 v112, 16, v111
	v_and_b32_e32 v113, 0xffff0000, v111
	v_lshlrev_b32_e32 v208, 16, v110
	v_and_b32_e32 v209, 0xffff0000, v110
	v_mov_b32_e32 v110, v116
	v_mov_b32_e32 v111, v202
	v_pk_mul_f32 v[148:149], v[148:149], v[148:149]
	v_mov_b32_e32 v150, v207
	v_mov_b32_e32 v151, v105
	v_mov_b32_e32 v74, v72
	v_mov_b32_e32 v75, v70
	v_pk_mul_f32 v[78:79], v[78:79], v[78:79]
	v_pk_fma_f32 v[110:111], v[110:111], v[110:111], v[148:149]
	v_mov_b32_e32 v148, v206
	v_mov_b32_e32 v149, v104
	v_pk_mul_f32 v[150:151], v[150:151], v[150:151]
	v_mov_b32_e32 v152, v113
	v_mov_b32_e32 v153, v119
	v_pk_fma_f32 v[74:75], v[74:75], v[74:75], v[78:79]
	v_pk_fma_f32 v[148:149], v[148:149], v[148:149], v[150:151]
	v_mov_b32_e32 v150, v112
	v_mov_b32_e32 v151, v118
	v_pk_mul_f32 v[152:153], v[152:153], v[152:153]
	v_mov_b32_e32 v210, v209
	v_mov_b32_e32 v211, v205
	v_pk_add_f32 v[74:75], v[74:75], v[74:75] op_sel:[0,1] op_sel_hi:[1,0]
	v_pk_fma_f32 v[150:151], v[150:151], v[150:151], v[152:153]
	v_mov_b32_e32 v152, v208
	v_mov_b32_e32 v153, v204
	v_pk_mul_f32 v[210:211], v[210:211], v[210:211]
	v_pk_add_f32 v[74:75], v[76:77], v[74:75] op_sel:[1,0] op_sel_hi:[0,1]
	v_pk_fma_f32 v[152:153], v[152:153], v[152:153], v[210:211]
	v_pk_add_f32 v[128:129], v[76:77], v[74:75]
	v_and_b32_e32 v77, 0xffff0000, v100
	v_and_b32_e32 v191, 0xffff0000, v107
	v_and_b32_e32 v193, 0xffff0000, v106
	v_pk_add_f32 v[150:151], v[152:153], v[150:151]
	v_lshlrev_b32_e32 v76, 16, v100
	v_lshlrev_b32_e32 v78, 16, v99
	v_and_b32_e32 v79, 0xffff0000, v99
	v_lshlrev_b32_e32 v80, 16, v98
	v_and_b32_e32 v81, 0xffff0000, v98
	v_lshlrev_b32_e32 v190, 16, v107
	v_mul_f32_e32 v98, v191, v191
	v_lshlrev_b32_e32 v192, 16, v106
	v_mul_f32_e32 v106, v193, v193
	v_pk_add_f32 v[148:149], v[148:149], v[150:151]
	v_mov_b32_e32 v150, v115
	v_mov_b32_e32 v151, v77
	v_lshlrev_b32_e32 v74, 16, v101
	v_and_b32_e32 v75, 0xffff0000, v101
	v_pk_mul_f32 v[100:101], v[78:79], v[78:79]
	v_pk_fma_f32 v[98:99], v[190:191], v[190:191], v[98:99] op_sel_hi:[1,1,0]
	v_pk_fma_f32 v[106:107], v[192:193], v[192:193], v[106:107] op_sel_hi:[1,1,0]
	v_pk_add_f32 v[110:111], v[110:111], v[148:149]
	v_mov_b32_e32 v148, v114
	v_mov_b32_e32 v149, v76
	v_pk_mul_f32 v[150:151], v[150:151], v[150:151]
	v_mov_b32_e32 v152, v189
	v_mov_b32_e32 v153, v81
	v_pk_fma_f32 v[148:149], v[148:149], v[148:149], v[150:151]
	v_mov_b32_e32 v150, v188
	v_mov_b32_e32 v151, v80
	v_pk_mul_f32 v[152:153], v[152:153], v[152:153]
	v_mov_b32_e32 v107, v100
	v_mov_b32_e32 v99, v101
	v_pk_mul_f32 v[146:147], v[74:75], v[74:75]
	v_pk_add_f32 v[110:111], v[110:111], v[110:111] op_sel:[0,1] op_sel_hi:[1,0]
	v_pk_fma_f32 v[150:151], v[150:151], v[150:151], v[152:153]
	v_pk_add_f32 v[98:99], v[106:107], v[98:99]
	v_mov_b32_e32 v111, v146
	v_pk_add_f32 v[98:99], v[150:151], v[98:99]
	v_mov_b32_e32 v103, v147
	v_pk_add_f32 v[98:99], v[148:149], v[98:99]
	v_pk_add_f32 v[100:101], v[110:111], v[102:103]
	v_mov_b32_e32 v102, v59
	v_pk_add_f32 v[98:99], v[100:101], v[98:99]
	v_mov_b32_e32 v103, v53
	v_pk_mul_f32 v[120:121], v[50:51], v[50:51]
	v_pk_mul_f32 v[122:123], v[54:55], v[54:55]
	v_pk_add_f32 v[98:99], v[98:99], v[98:99] op_sel:[0,1] op_sel_hi:[1,0]
	v_mov_b32_e32 v100, v58
	v_mov_b32_e32 v101, v52
	v_pk_mul_f32 v[102:103], v[102:103], v[102:103]
	v_mov_b32_e32 v106, v61
	v_mov_b32_e32 v107, v57
	v_pk_fma_f32 v[100:101], v[100:101], v[100:101], v[102:103]
	v_mov_b32_e32 v102, v60
	v_mov_b32_e32 v103, v56
	v_pk_mul_f32 v[106:107], v[106:107], v[106:107]
	v_mov_b32_e32 v127, v122
	v_mov_b32_e32 v125, v123
	v_mov_b32_e32 v99, v120
	v_mov_b32_e32 v129, v121
	v_pk_fma_f32 v[102:103], v[102:103], v[102:103], v[106:107]
	v_pk_add_f32 v[106:107], v[126:127], v[124:125]
	v_pk_add_f32 v[98:99], v[98:99], v[128:129]
	global_load_dwordx4 v[122:125], v[134:135], off offset:400
	global_load_dwordx4 v[126:129], v[134:135], off offset:384
	global_load_dwordx4 v[146:149], v[134:135], off offset:464
	global_load_dwordx4 v[150:153], v[134:135], off offset:448
	v_pk_add_f32 v[102:103], v[102:103], v[106:107]
	s_nop 0
	v_pk_add_f32 v[100:101], v[100:101], v[102:103]
	s_nop 0
	v_pk_add_f32 v[98:99], v[98:99], v[100:101]
	s_nop 0
	v_add_f32_e32 v98, v98, v99
	ds_bpermute_b32 v99, v160, v98
	s_waitcnt lgkmcnt(0)
	v_add_f32_e32 v98, v98, v99
	v_fmamk_f32 v98, v98, 0x3c000000, v183
	v_rsq_f32_e32 v98, v98
	s_nop 0
	v_mul_f32_e32 v210, 0x3e0293ee, v98
	v_pk_mul_f32 v[2:3], v[210:211], v[2:3] op_sel_hi:[0,1]
	v_pk_mul_f32 v[4:5], v[210:211], v[4:5] op_sel_hi:[0,1]
	v_pk_mul_f32 v[2:3], v[2:3], v[68:69]
	v_pk_mul_f32 v[38:39], v[210:211], v[38:39] op_sel_hi:[0,1]
	v_pk_mul_f32 v[6:7], v[210:211], v[6:7] op_sel_hi:[0,1]
	v_cvt_pk_bf16_f32 v120, v2, v3
	v_pk_mul_f32 v[2:3], v[4:5], v[66:67]
	v_pk_mul_f32 v[40:41], v[210:211], v[40:41] op_sel_hi:[0,1]
	v_pk_mul_f32 v[38:39], v[38:39], v[204:205]
	v_pk_mul_f32 v[8:9], v[210:211], v[8:9] op_sel_hi:[0,1]
	v_pk_mul_f32 v[6:7], v[6:7], v[72:73]
	v_cvt_pk_bf16_f32 v102, v38, v39
	v_pk_mul_f32 v[38:39], v[40:41], v[118:119]
	v_cvt_pk_bf16_f32 v118, v6, v7
	v_pk_mul_f32 v[6:7], v[8:9], v[70:71]
	v_pk_mul_f32 v[22:23], v[210:211], v[22:23] op_sel_hi:[0,1]
	v_pk_mul_f32 v[24:25], v[210:211], v[24:25] op_sel_hi:[0,1]
	v_pk_mul_f32 v[22:23], v[22:23], v[192:193]
	v_cvt_pk_bf16_f32 v121, v2, v3
	v_cvt_pk_bf16_f32 v110, v22, v23
	v_pk_mul_f32 v[22:23], v[24:25], v[190:191]
	v_cvt_pk_bf16_f32 v119, v6, v7
	v_pk_mul_f32 v[42:43], v[210:211], v[42:43] op_sel_hi:[0,1]
	v_pk_mul_f32 v[10:11], v[210:211], v[10:11] op_sel_hi:[0,1]
	v_pk_mul_f32 v[46:47], v[210:211], v[46:47] op_sel_hi:[0,1]
	v_pk_mul_f32 v[44:45], v[210:211], v[44:45] op_sel_hi:[0,1]
	v_pk_mul_f32 v[42:43], v[42:43], v[206:207]
	v_pk_mul_f32 v[18:19], v[210:211], v[18:19] op_sel_hi:[0,1]
	v_pk_mul_f32 v[14:15], v[210:211], v[14:15] op_sel_hi:[0,1]
	v_pk_mul_f32 v[12:13], v[210:211], v[12:13] op_sel_hi:[0,1]
	v_pk_mul_f32 v[10:11], v[10:11], v[76:77]
	v_pk_mul_f32 v[48:49], v[210:211], v[48:49] op_sel_hi:[0,1]
	v_pk_mul_f32 v[46:47], v[46:47], v[208:209]
	v_cvt_pk_bf16_f32 v100, v42, v43
	v_pk_mul_f32 v[42:43], v[44:45], v[116:117]
	v_pk_mul_f32 v[20:21], v[210:211], v[20:21] op_sel_hi:[0,1]
	v_pk_mul_f32 v[18:19], v[18:19], v[188:189]
	v_pk_mul_f32 v[16:17], v[210:211], v[16:17] op_sel_hi:[0,1]
	v_pk_mul_f32 v[14:15], v[14:15], v[80:81]
	v_cvt_pk_bf16_f32 v116, v10, v11
	v_pk_mul_f32 v[10:11], v[12:13], v[74:75]
	v_cvt_pk_bf16_f32 v98, v46, v47
	v_pk_mul_f32 v[46:47], v[48:49], v[112:113]
	v_cvt_pk_bf16_f32 v112, v18, v19
	v_pk_mul_f32 v[18:19], v[20:21], v[114:115]
	v_cvt_pk_bf16_f32 v114, v14, v15
	v_pk_mul_f32 v[14:15], v[16:17], v[78:79]
	v_cvt_pk_bf16_f32 v117, v10, v11
	v_cvt_pk_bf16_f32 v115, v14, v15
	v_and_b32_e32 v15, 0xffff0000, v90
	v_cvt_pk_bf16_f32 v113, v18, v19
	v_lshlrev_b32_e32 v14, 16, v90
	v_mov_b32_e32 v18, v15
	v_mov_b32_e32 v16, v14
	v_cvt_pk_bf16_f32 v111, v22, v23
	v_pk_mul_f32 v[34:35], v[210:211], v[34:35] op_sel_hi:[0,1]
	v_pk_mul_f32 v[30:31], v[210:211], v[30:31] op_sel_hi:[0,1]
	v_pk_mul_f32 v[26:27], v[210:211], v[26:27] op_sel_hi:[0,1]
	s_waitcnt vmcnt(3)
	v_pk_mul_f32 v[8:9], v[210:211], v[122:123] op_sel_hi:[0,1]
	s_waitcnt vmcnt(2)
	v_pk_mul_f32 v[4:5], v[210:211], v[126:127] op_sel_hi:[0,1]
	v_pk_mul_f32 v[4:5], v[4:5], v[64:65]
	v_pk_mul_f32 v[2:3], v[210:211], v[128:129] op_sel_hi:[0,1]
	v_cvt_pk_bf16_f32 v122, v4, v5
	s_waitcnt vmcnt(0)
	v_pk_mul_f32 v[4:5], v[210:211], v[150:151] op_sel_hi:[0,1]
	v_pk_mul_f32 v[4:5], v[4:5], v[56:57]
	v_pk_mul_f32 v[2:3], v[2:3], v[62:63]
	v_cvt_pk_bf16_f32 v126, v4, v5
	v_mov_b32_e32 v4, s35
	global_load_dword v24, v4, s[74:75]
	v_pk_mul_f32 v[6:7], v[210:211], v[124:125] op_sel_hi:[0,1]
	v_cvt_pk_bf16_f32 v123, v2, v3
	v_pk_mul_f32 v[2:3], v[8:9], v[60:61]
	v_pk_mul_f32 v[8:9], v[210:211], v[146:147] op_sel_hi:[0,1]
	v_cvt_pk_bf16_f32 v124, v2, v3
	v_pk_mul_f32 v[2:3], v[6:7], v[58:59]
	v_and_b32_e32 v5, 0xffff0000, v92
	v_cvt_pk_bf16_f32 v125, v2, v3
	v_pk_mul_f32 v[2:3], v[210:211], v[152:153] op_sel_hi:[0,1]
	v_pk_mul_f32 v[2:3], v[2:3], v[54:55]
	v_lshlrev_b32_e32 v4, 16, v92
	v_cvt_pk_bf16_f32 v127, v2, v3
	v_pk_mul_f32 v[2:3], v[8:9], v[52:53]
	v_and_b32_e32 v9, 0xffff0000, v93
	v_lshlrev_b32_e32 v8, 16, v93
	v_mov_b32_e32 v12, v9
	v_mov_b32_e32 v13, v5
	v_mov_b32_e32 v10, v8
	v_mov_b32_e32 v11, v4
	v_pk_mul_f32 v[12:13], v[12:13], v[12:13]
	v_pk_mul_f32 v[6:7], v[210:211], v[148:149] op_sel_hi:[0,1]
	v_pk_fma_f32 v[10:11], v[10:11], v[10:11], v[12:13]
	v_and_b32_e32 v13, 0xffff0000, v91
	v_lshlrev_b32_e32 v12, 16, v91
	v_mov_b32_e32 v19, v13
	v_mov_b32_e32 v17, v12
	v_pk_mul_f32 v[18:19], v[18:19], v[18:19]
	v_cvt_pk_bf16_f32 v128, v2, v3
	v_pk_fma_f32 v[16:17], v[16:17], v[16:17], v[18:19]
	v_pk_mul_f32 v[2:3], v[6:7], v[50:51]
	v_add_f32_e32 v16, v16, v17
	v_add_f32_e32 v11, v11, v16
	v_add_f32_e32 v10, v10, v11
	v_cvt_pk_bf16_f32 v129, v2, v3
	v_and_b32_e32 v19, 0xffff0000, v94
	v_add_f32_dpp v10, v10, v10 quad_perm:[1,0,3,2] row_mask:0xf bank_mask:0xf bound_ctrl:1
	v_lshlrev_b32_e32 v18, 16, v94
	v_mov_b32_e32 v22, v19
	v_add_f32_dpp v10, v10, v10 quad_perm:[2,3,0,1] row_mask:0xf bank_mask:0xf bound_ctrl:1
	v_mov_b32_e32 v20, v18
	v_pk_mul_f32 v[36:37], v[210:211], v[36:37] op_sel_hi:[0,1]
	v_add_f32_dpp v10, v10, v10 row_half_mirror row_mask:0xf bank_mask:0xf bound_ctrl:1
	v_pk_mul_f32 v[34:35], v[34:35], v[104:105]
	v_pk_mul_f32 v[32:33], v[210:211], v[32:33] op_sel_hi:[0,1]
	v_add_f32_dpp v10, v10, v10 row_mirror row_mask:0xf bank_mask:0xf bound_ctrl:1
	v_fmamk_f32 v10, v10, 0x3c000000, v183
	v_rsq_f32_e32 v10, v10
	v_pk_mul_f32 v[28:29], v[210:211], v[28:29] op_sel_hi:[0,1]
	v_pk_mul_f32 v[30:31], v[30:31], v[198:199]
	v_pk_mul_f32 v[26:27], v[26:27], v[108:109]
	v_pk_mul_f32 v[6:7], v[88:89], v[10:11] op_sel_hi:[1,0]
	v_pk_mul_f32 v[2:3], v[86:87], v[10:11] op_sel_hi:[1,0]
	v_pk_mul_f32 v[16:17], v[84:85], v[10:11] op_sel_hi:[1,0]
	v_pk_mul_f32 v[10:11], v[82:83], v[10:11] op_sel_hi:[1,0]
	v_pk_mul_f32 v[2:3], v[2:3], v[14:15]
	v_pk_mul_f32 v[6:7], v[6:7], v[12:13]
	v_cvt_pk_bf16_f32 v2, v2, v3
	v_cvt_pk_bf16_f32 v3, v6, v7
	v_pk_mul_f32 v[4:5], v[10:11], v[4:5]
	v_and_b32_e32 v7, 0xffff0000, v97
	v_and_b32_e32 v11, 0xffff0000, v96
	v_lshlrev_b32_e32 v6, 16, v97
	v_lshlrev_b32_e32 v10, 16, v96
	v_mov_b32_e32 v14, v7
	v_mov_b32_e32 v15, v11
	v_mov_b32_e32 v12, v6
	v_mov_b32_e32 v13, v10
	v_pk_mul_f32 v[14:15], v[14:15], v[14:15]
	v_cvt_pk_bf16_f32 v4, v4, v5
	v_pk_fma_f32 v[12:13], v[12:13], v[12:13], v[14:15]
	v_and_b32_e32 v15, 0xffff0000, v95
	v_lshlrev_b32_e32 v14, 16, v95
	v_mov_b32_e32 v23, v15
	v_mov_b32_e32 v21, v14
	v_pk_mul_f32 v[22:23], v[22:23], v[22:23]
	v_pk_mul_f32 v[8:9], v[16:17], v[8:9]
	v_pk_fma_f32 v[20:21], v[20:21], v[20:21], v[22:23]
	v_cvt_pk_bf16_f32 v104, v34, v35
	v_add_f32_e32 v5, v20, v21
	v_add_f32_e32 v5, v13, v5
	v_add_f32_e32 v5, v12, v5
	v_pk_mul_f32 v[34:35], v[36:37], v[202:203]
	v_cvt_pk_bf16_f32 v106, v30, v31
	v_add_f32_dpp v5, v5, v5 quad_perm:[1,0,3,2] row_mask:0xf bank_mask:0xf bound_ctrl:1
	v_pk_mul_f32 v[30:31], v[32:33], v[196:197]
	v_cvt_pk_bf16_f32 v108, v26, v27
	v_add_f32_dpp v5, v5, v5 quad_perm:[2,3,0,1] row_mask:0xf bank_mask:0xf bound_ctrl:1
	v_pk_mul_f32 v[26:27], v[28:29], v[194:195]
	v_mov_b32_e32 v50, v131
	v_add_f32_dpp v5, v5, v5 row_half_mirror row_mask:0xf bank_mask:0xf bound_ctrl:1
	v_mov_b32_e32 v51, v131
	v_cvt_pk_bf16_f32 v99, v46, v47
	v_add_f32_dpp v5, v5, v5 row_mirror row_mask:0xf bank_mask:0xf bound_ctrl:1
	v_fmamk_f32 v5, v5, 0x3c000000, v183
	v_rsq_f32_e32 v12, v5
	v_cvt_pk_bf16_f32 v5, v8, v9
	ds_write_b128 v157, v[2:5]
	v_cvt_pk_bf16_f32 v101, v42, v43
	v_pk_mul_f32 v[4:5], v[88:89], v[12:13] op_sel_hi:[1,0]
	v_pk_mul_f32 v[2:3], v[86:87], v[12:13] op_sel_hi:[1,0]
	v_pk_mul_f32 v[8:9], v[84:85], v[12:13] op_sel_hi:[1,0]
	v_pk_mul_f32 v[12:13], v[82:83], v[12:13] op_sel_hi:[1,0]
	v_pk_mul_f32 v[2:3], v[2:3], v[18:19]
	v_pk_mul_f32 v[4:5], v[4:5], v[14:15]
	v_cvt_pk_bf16_f32 v2, v2, v3
	v_cvt_pk_bf16_f32 v3, v4, v5
	v_pk_mul_f32 v[4:5], v[12:13], v[10:11]
	v_pk_mul_f32 v[6:7], v[8:9], v[6:7]
	v_cvt_pk_bf16_f32 v4, v4, v5
	v_cvt_pk_bf16_f32 v5, v6, v7
	v_add_u32_e32 v6, 0x2000, v157
	ds_write_b128 v6, v[2:5]
	v_add_u32_e32 v2, s22, v180
	v_mad_i64_i32 v[2:3], s[42:43], v2, s20, 0
	v_mad_i64_i32 v[2:3], s[42:43], s14, v186, v[2:3]
	v_lshl_add_u64 v[146:147], v[136:137], 0, v[2:3]
	v_lshl_add_u64 v[148:149], v[138:139], 0, v[2:3]
	v_add_u32_e32 v2, s22, v181
	v_mad_i64_i32 v[2:3], s[42:43], v2, s20, 0
	v_mad_i64_i32 v[2:3], s[42:43], s14, v186, v[2:3]
	s_lshl_b32 s14, s31, 8
	v_cvt_pk_bf16_f32 v103, v38, v39
	v_cvt_pk_bf16_f32 v105, v34, v35
	v_cvt_pk_bf16_f32 v107, v30, v31
	v_cvt_pk_bf16_f32 v109, v26, v27
	s_waitcnt vmcnt(0)
	v_mul_f32_e32 v188, 0x3fb8aa3b, v24
	v_lshl_add_u64 v[150:151], v[136:137], 0, v[2:3]
	v_lshl_add_u64 v[152:153], v[138:139], 0, v[2:3]
	s_add_i32 s15, s15, s14
	v_mov_b32_e32 v52, v131
	v_mov_b32_e32 v53, v131
	v_mov_b32_e32 v54, v131
	v_mov_b32_e32 v55, v131
	v_mov_b32_e32 v56, v131
	v_mov_b32_e32 v57, v131
	v_mov_b32_e32 v58, v131
	v_mov_b32_e32 v59, v131
	v_mov_b32_e32 v60, v131
	v_mov_b32_e32 v61, v131
	v_mov_b32_e32 v62, v131
	v_mov_b32_e32 v63, v131
	v_mov_b32_e32 v64, v131
	v_mov_b32_e32 v65, v131
	v_mov_b64_e32 v[34:35], v[50:51]
	v_mov_b64_e32 v[18:19], v[50:51]
	v_mov_b64_e32 v[2:3], v[50:51]
	s_or_b32 s35, s23, 63
	v_add_u32_e32 v141, s15, v182
	s_mov_b32 s42, s1
	v_mov_b64_e32 v[36:37], v[52:53]
	v_mov_b64_e32 v[38:39], v[54:55]
	v_mov_b64_e32 v[40:41], v[56:57]
	v_mov_b64_e32 v[42:43], v[58:59]
	v_mov_b64_e32 v[44:45], v[60:61]
	v_mov_b64_e32 v[46:47], v[62:63]
	v_mov_b64_e32 v[48:49], v[64:65]
	v_mov_b64_e32 v[20:21], v[52:53]
	v_mov_b64_e32 v[22:23], v[54:55]
	v_mov_b64_e32 v[24:25], v[56:57]
	v_mov_b64_e32 v[26:27], v[58:59]
	v_mov_b64_e32 v[28:29], v[60:61]
	v_mov_b64_e32 v[30:31], v[62:63]
	v_mov_b64_e32 v[32:33], v[64:65]
	v_mov_b64_e32 v[4:5], v[52:53]
	v_mov_b64_e32 v[6:7], v[54:55]
	v_mov_b64_e32 v[8:9], v[56:57]
	v_mov_b64_e32 v[10:11], v[58:59]
	v_mov_b64_e32 v[12:13], v[60:61]
	v_mov_b64_e32 v[14:15], v[62:63]
	v_mov_b64_e32 v[16:17], v[64:65]
	s_waitcnt lgkmcnt(0)
	s_barrier
	s_branch .LBB0_616
	.p2align	6

.LBB0_693:
	s_and_b32 s61, s35, 3
	s_lshl_b32 s5, s4, 13
	s_lshl_b32 s7, s61, 12
	s_add_u32 s48, s28, 0x80
	s_addc_u32 s49, s29, 0
	s_add_i32 s18, 0, 0x18000
	s_mov_b64 s[8:9], s[48:49]
	s_add_i32 s67, s18, s6
	v_mov_b32_e32 v2, v171
	s_waitcnt vmcnt(2)
	s_barrier
	s_mov_b32 m0, s67
	s_add_i32 s69, s67, 0x2000
	global_load_lds_dwordx4 v2, s[8:9]
	v_mov_b32_e32 v2, v173
	s_add_u32 s50, s28, 0x40080
	s_mov_b32 m0, s69
	s_addc_u32 s51, s29, 0
	s_add_i32 s19, 0, 0x1c000
	global_load_lds_dwordx4 v2, s[8:9]
	s_mov_b64 s[8:9], s[50:51]
	s_add_i32 s70, s19, s6
	v_mov_b32_e32 v2, v171
	s_mov_b32 m0, s70
	s_add_i32 s71, s70, 0x2000
	global_load_lds_dwordx4 v2, s[8:9]
	v_mov_b32_e32 v2, v173
	s_mov_b32 m0, s71
	v_lshlrev_b32_e32 v5, 6, v0
	global_load_lds_dwordx4 v2, s[8:9]
	v_and_b32_e32 v2, 48, v0
	v_and_b32_e32 v5, 0x3c0, v5
	v_and_b32_e32 v175, 15, v0
	v_and_b32_e32 v3, 32, v200
	v_or_b32_e32 v6, v5, v2
	v_lshl_or_b32 v176, v175, 6, v2
	v_bitop3_b32 v177, v5, v3, v2 bitop3:0x36
	v_bitop3_b32 v2, s7, v6, v3 bitop3:0xf6
	s_add_i32 s17, 0, 0x10000
	v_bitop3_b32 v4, v176, s5, v3 bitop3:0xde
	v_add_u32_e32 v162, s17, v2
	s_add_i32 s16, 0, 0x14000
	s_waitcnt vmcnt(6)
	s_barrier
	v_add_u32_e32 v163, s16, v2
	v_add_u32_e32 v164, 0, v4
	v_add_u32_e32 v165, s18, v2
	v_add_u32_e32 v166, s19, v2
	ds_read_b128 v[2:5], v162
	s_waitcnt lgkmcnt(0)
	ds_read_b128 v[6:9], v162 offset:1024
	s_waitcnt vmcnt(0)
	ds_read_b128 v[10:13], v162 offset:2048
	ds_read_b128 v[14:17], v162 offset:3072
	ds_read_b128 v[18:21], v163
	ds_read_b128 v[22:25], v163 offset:1024
	ds_read_b128 v[26:29], v163 offset:2048
	ds_read_b128 v[30:33], v163 offset:3072
	v_lshl_or_b32 v179, s4, 6, v175
	s_add_u32 s4, s0, 0x100
	s_addc_u32 s5, s1, 0
	s_add_u32 s44, s28, 0x100
	s_addc_u32 s45, s29, 0
	s_add_u32 s8, s0, 0x80
	s_addc_u32 s9, s1, 0
	v_mov_b32_e32 v66, v170
	s_add_i32 s72, s21, 0x8000
	ds_read_b128 v[34:37], v164
	ds_read_b128 v[38:41], v164 offset:1024
	ds_read_b128 v[42:45], v164 offset:2048
	ds_read_b128 v[46:49], v164 offset:3072
	ds_read_b128 v[50:53], v164 offset:4096
	ds_read_b128 v[54:57], v164 offset:5120
	ds_read_b128 v[58:61], v164 offset:6144
	ds_read_b128 v[62:65], v164 offset:7168
	s_mov_b32 m0, s72
	s_add_i32 s73, s21, 0xa000
	global_load_lds_dwordx4 v66, s[8:9]
	v_mov_b32_e32 v66, v172
	s_mov_b32 m0, s73
	s_nop 0
	global_load_lds_dwordx4 v66, s[8:9]
	s_add_u32 s8, s0, 0x40080
	s_addc_u32 s9, s1, 0
	v_mov_b32_e32 v66, v170
	s_add_i32 s74, s21, 0xc000
	s_mov_b32 m0, s74
	s_add_i32 s75, s21, 0xe000
	global_load_lds_dwordx4 v66, s[8:9]
	v_mov_b32_e32 v66, v172
	s_mov_b32 m0, s75
	s_add_u32 s42, s28, 0x180
	global_load_lds_dwordx4 v66, s[8:9]
	s_waitcnt vmcnt(8)
	s_waitcnt lgkmcnt(0)
	s_addc_u32 s43, s29, 0
	s_barrier
	s_setprio 1
	s_waitcnt lgkmcnt(0)
	v_mfma_f32_16x16x128_f8f6f4 v[158:161], v[2:9], v[34:41], 0
	v_mfma_f32_16x16x128_f8f6f4 v[154:157], v[10:17], v[34:41], 0
	v_mfma_f32_16x16x128_f8f6f4 v[150:153], v[18:25], v[34:41], 0
	v_mfma_f32_16x16x128_f8f6f4 v[146:149], v[26:33], v[34:41], 0
	v_mfma_f32_16x16x128_f8f6f4 v[122:125], v[26:33], v[42:49], 0
	v_mfma_f32_16x16x128_f8f6f4 v[102:105], v[18:25], v[42:49], 0
	v_mfma_f32_16x16x128_f8f6f4 v[114:117], v[10:17], v[42:49], 0
	v_mfma_f32_16x16x128_f8f6f4 v[110:113], v[2:9], v[42:49], 0
	v_mfma_f32_16x16x128_f8f6f4 v[134:137], v[2:9], v[50:57], 0
	v_mfma_f32_16x16x128_f8f6f4 v[138:141], v[10:17], v[50:57], 0
	v_mfma_f32_16x16x128_f8f6f4 v[130:133], v[18:25], v[50:57], 0
	v_mfma_f32_16x16x128_f8f6f4 v[142:145], v[26:33], v[50:57], 0
	v_mfma_f32_16x16x128_f8f6f4 v[98:101], v[26:33], v[58:65], 0
	v_mfma_f32_16x16x128_f8f6f4 v[106:109], v[18:25], v[58:65], 0
	v_mfma_f32_16x16x128_f8f6f4 v[118:121], v[10:17], v[58:65], 0
	v_mfma_f32_16x16x128_f8f6f4 v[126:129], v[2:9], v[58:65], 0
	s_setprio 0
	s_barrier
	s_mov_b64 s[8:9], s[44:45]
	v_mov_b32_e32 v50, v171
	s_add_i32 s76, s17, s6
	ds_read_b128 v[34:37], v164 offset:16384
	ds_read_b128 v[38:41], v164 offset:17408
	ds_read_b128 v[42:45], v164 offset:18432
	ds_read_b128 v[46:49], v164 offset:19456
	ds_read_b128 v[180:183], v164 offset:20480
	ds_read_b128 v[184:187], v164 offset:21504
	ds_read_b128 v[188:191], v164 offset:22528
	ds_read_b128 v[192:195], v164 offset:23552
	s_mov_b32 m0, s76
	s_add_i32 s77, s76, 0x2000
	global_load_lds_dwordx4 v50, s[8:9]
	v_mov_b32_e32 v50, v173
	s_add_u32 s52, s28, 0x40100
	s_mov_b32 m0, s77
	s_addc_u32 s53, s29, 0
	global_load_lds_dwordx4 v50, s[8:9]
	s_mov_b64 s[8:9], s[52:53]
	v_mov_b32_e32 v50, v171
	s_add_i32 s78, s16, s6
	s_mov_b32 m0, s78
	s_add_i32 s79, s78, 0x2000
	global_load_lds_dwordx4 v50, s[8:9]
	v_mov_b32_e32 v50, v173
	s_mov_b32 m0, s79
	s_nop 0
	global_load_lds_dwordx4 v50, s[8:9]
	s_waitcnt vmcnt(6)
	s_waitcnt lgkmcnt(0)
	s_barrier
	s_setprio 1
	s_waitcnt lgkmcnt(0)
	v_mfma_f32_16x16x128_f8f6f4 v[94:97], v[2:9], v[34:41], 0
	v_mfma_f32_16x16x128_f8f6f4 v[90:93], v[10:17], v[34:41], 0
	v_mfma_f32_16x16x128_f8f6f4 v[86:89], v[18:25], v[34:41], 0
	v_mfma_f32_16x16x128_f8f6f4 v[82:85], v[26:33], v[34:41], 0
	v_mfma_f32_16x16x128_f8f6f4 v[66:69], v[26:33], v[42:49], 0
	v_mfma_f32_16x16x128_f8f6f4 v[70:73], v[18:25], v[42:49], 0
	v_mfma_f32_16x16x128_f8f6f4 v[74:77], v[10:17], v[42:49], 0
	v_mfma_f32_16x16x128_f8f6f4 v[78:81], v[2:9], v[42:49], 0
	v_mfma_f32_16x16x128_f8f6f4 v[62:65], v[2:9], v[180:187], 0
	v_mfma_f32_16x16x128_f8f6f4 v[58:61], v[10:17], v[180:187], 0
	v_mfma_f32_16x16x128_f8f6f4 v[54:57], v[18:25], v[180:187], 0
	v_mfma_f32_16x16x128_f8f6f4 v[50:53], v[26:33], v[180:187], 0
	v_mfma_f32_16x16x128_f8f6f4 v[34:37], v[26:33], v[188:195], 0
	v_mfma_f32_16x16x128_f8f6f4 v[38:41], v[18:25], v[188:195], 0
	v_mfma_f32_16x16x128_f8f6f4 v[42:45], v[10:17], v[188:195], 0
	v_mfma_f32_16x16x128_f8f6f4 v[46:49], v[2:9], v[188:195], 0
	s_setprio 0
	s_barrier
	ds_read_b128 v[26:29], v165
	ds_read_b128 v[30:33], v165 offset:1024
	ds_read_b128 v[18:21], v165 offset:2048
	ds_read_b128 v[22:25], v165 offset:3072
	ds_read_b128 v[10:13], v166
	ds_read_b128 v[14:17], v166 offset:1024
	ds_read_b128 v[2:5], v166 offset:2048
	ds_read_b128 v[6:9], v166 offset:3072
	v_mov_b32_e32 v167, v170
	s_mov_b32 m0, s21
	ds_read_b128 v[180:183], v164 offset:32768
	ds_read_b128 v[184:187], v164 offset:33792
	ds_read_b128 v[188:191], v164 offset:34816
	ds_read_b128 v[192:195], v164 offset:35840
	ds_read_b128 v[202:205], v164 offset:36864
	ds_read_b128 v[206:209], v164 offset:37888
	ds_read_b128 v[210:213], v164 offset:38912
	ds_read_b128 v[214:217], v164 offset:39936
	s_nop 0
	global_load_lds_dwordx4 v167, s[4:5]
	v_mov_b32_e32 v167, v172
	s_mov_b32 m0, s60
	s_nop 0
	global_load_lds_dwordx4 v167, s[4:5]
	s_add_u32 s4, s0, 0x40100
	s_addc_u32 s5, s1, 0
	v_mov_b32_e32 v167, v170
	s_mov_b32 m0, s62
	s_nop 0
	global_load_lds_dwordx4 v167, s[4:5]
	v_mov_b32_e32 v167, v172
	s_mov_b32 m0, s63
	s_nop 0
	global_load_lds_dwordx4 v167, s[4:5]
	s_waitcnt vmcnt(8)
	s_waitcnt lgkmcnt(0)
	s_barrier
	s_setprio 1
	s_waitcnt lgkmcnt(0)
	v_mfma_f32_16x16x128_f8f6f4 v[158:161], v[26:33], v[180:187], v[158:161]
	v_mfma_f32_16x16x128_f8f6f4 v[154:157], v[18:25], v[180:187], v[154:157]
	v_mfma_f32_16x16x128_f8f6f4 v[150:153], v[10:17], v[180:187], v[150:153]
	v_mfma_f32_16x16x128_f8f6f4 v[146:149], v[2:9], v[180:187], v[146:149]
	v_mfma_f32_16x16x128_f8f6f4 v[122:125], v[2:9], v[188:195], v[122:125]
	v_mfma_f32_16x16x128_f8f6f4 v[102:105], v[10:17], v[188:195], v[102:105]
	v_mfma_f32_16x16x128_f8f6f4 v[114:117], v[18:25], v[188:195], v[114:117]
	v_mfma_f32_16x16x128_f8f6f4 v[110:113], v[26:33], v[188:195], v[110:113]
	v_mfma_f32_16x16x128_f8f6f4 v[134:137], v[26:33], v[202:209], v[134:137]
	v_mfma_f32_16x16x128_f8f6f4 v[138:141], v[18:25], v[202:209], v[138:141]
	v_mfma_f32_16x16x128_f8f6f4 v[130:133], v[10:17], v[202:209], v[130:133]
	v_mfma_f32_16x16x128_f8f6f4 v[142:145], v[2:9], v[202:209], v[142:145]
	v_mfma_f32_16x16x128_f8f6f4 v[98:101], v[2:9], v[210:217], v[98:101]
	v_mfma_f32_16x16x128_f8f6f4 v[106:109], v[10:17], v[210:217], v[106:109]
	v_mfma_f32_16x16x128_f8f6f4 v[118:121], v[18:25], v[210:217], v[118:121]
	v_mfma_f32_16x16x128_f8f6f4 v[126:129], v[26:33], v[210:217], v[126:129]
	s_setprio 0
	s_barrier
	s_mov_b64 s[4:5], s[42:43]
	v_mov_b32_e32 v167, v171
	s_mov_b32 m0, s67
	ds_read_b128 v[180:183], v164 offset:49152
	ds_read_b128 v[184:187], v164 offset:50176
	ds_read_b128 v[188:191], v164 offset:51200
	ds_read_b128 v[192:195], v164 offset:52224
	ds_read_b128 v[202:205], v164 offset:53248
	ds_read_b128 v[206:209], v164 offset:54272
	ds_read_b128 v[210:213], v164 offset:55296
	ds_read_b128 v[214:217], v164 offset:56320
	s_add_u32 s64, s28, 0x40180
	global_load_lds_dwordx4 v167, s[4:5]
	v_mov_b32_e32 v167, v173
	s_mov_b32 m0, s69
	s_addc_u32 s65, s29, 0
	global_load_lds_dwordx4 v167, s[4:5]
	s_mov_b64 s[4:5], s[64:65]
	v_mov_b32_e32 v167, v171
	s_mov_b32 m0, s70
	s_nop 0
	global_load_lds_dwordx4 v167, s[4:5]
	v_mov_b32_e32 v167, v173
	s_mov_b32 m0, s71
	s_nop 0
	global_load_lds_dwordx4 v167, s[4:5]
	s_waitcnt vmcnt(6)
	s_waitcnt lgkmcnt(0)
	s_barrier
	s_setprio 1
	s_waitcnt lgkmcnt(0)
	v_mfma_f32_16x16x128_f8f6f4 v[94:97], v[26:33], v[180:187], v[94:97]
	v_mfma_f32_16x16x128_f8f6f4 v[90:93], v[18:25], v[180:187], v[90:93]
	v_mfma_f32_16x16x128_f8f6f4 v[86:89], v[10:17], v[180:187], v[86:89]
	v_mfma_f32_16x16x128_f8f6f4 v[82:85], v[2:9], v[180:187], v[82:85]
	v_mfma_f32_16x16x128_f8f6f4 v[66:69], v[2:9], v[188:195], v[66:69]
	v_mfma_f32_16x16x128_f8f6f4 v[70:73], v[10:17], v[188:195], v[70:73]
	v_mfma_f32_16x16x128_f8f6f4 v[74:77], v[18:25], v[188:195], v[74:77]
	v_mfma_f32_16x16x128_f8f6f4 v[78:81], v[26:33], v[188:195], v[78:81]
	v_mfma_f32_16x16x128_f8f6f4 v[62:65], v[26:33], v[202:209], v[62:65]
	v_mfma_f32_16x16x128_f8f6f4 v[58:61], v[18:25], v[202:209], v[58:61]
	v_mfma_f32_16x16x128_f8f6f4 v[54:57], v[10:17], v[202:209], v[54:57]
	v_mfma_f32_16x16x128_f8f6f4 v[50:53], v[2:9], v[202:209], v[50:53]
	v_mfma_f32_16x16x128_f8f6f4 v[34:37], v[2:9], v[210:217], v[34:37]
	v_mfma_f32_16x16x128_f8f6f4 v[38:41], v[10:17], v[210:217], v[38:41]
	v_mfma_f32_16x16x128_f8f6f4 v[42:45], v[18:25], v[210:217], v[42:45]
	v_mfma_f32_16x16x128_f8f6f4 v[46:49], v[26:33], v[210:217], v[46:49]
	s_setprio 0
	s_barrier
	s_and_b32 s4, s12, 7
	s_lshl_b32 s4, s4, 22
	s_lshl_b32 s5, s11, 19
	s_or_b32 s4, s4, s5
	s_add_u32 s4, s56, s4
	s_addc_u32 s5, s57, 0
	s_add_u32 s8, s4, 0x3ab00100
	s_addc_u32 s9, s5, 0
	s_add_u32 s2, s56, s2
	s_addc_u32 s3, s57, s3
	s_add_u32 s30, s2, 0xf00200
	s_addc_u32 s31, s3, 0
	s_mov_b64 s[2:3], s[30:31]
	.p2align	6

.LBB0_740:
	s_add_i32 s66, s18, s70
	v_mov_b32_e32 v2, v171
	s_waitcnt vmcnt(2)
	s_barrier
	s_mov_b32 m0, s66
	s_add_i32 s67, s66, 0x2000
	global_load_lds_dwordx4 v2, s[48:49]
	v_mov_b32_e32 v2, v173
	s_mov_b32 m0, s67
	s_and_b32 s20, s35, 3
	global_load_lds_dwordx4 v2, s[48:49]
	s_add_i32 s48, s19, s70
	v_mov_b32_e32 v2, v171
	s_mov_b32 m0, s48
	s_add_i32 s49, s48, 0x2000
	global_load_lds_dwordx4 v2, s[50:51]
	v_mov_b32_e32 v2, v173
	s_mov_b32 m0, s49
	v_lshl_or_b32 v179, s14, 6, v175
	global_load_lds_dwordx4 v2, s[50:51]
	v_lshlrev_b32_e32 v2, 2, v175
	s_lshl_b32 s14, s14, 13
	v_and_b32_e32 v2, 32, v2
	v_lshl_or_b32 v3, s20, 12, v177
	v_bitop3_b32 v2, v176, s14, v2 bitop3:0xde
	v_add_u32_e32 v162, s17, v3
	s_waitcnt vmcnt(6)
	s_barrier
	v_add_u32_e32 v163, s16, v3
	v_add_u32_e32 v164, 0, v2
	v_add_u32_e32 v165, s18, v3
	v_add_u32_e32 v166, s19, v3
	ds_read_b128 v[2:5], v162
	ds_read_b128 v[6:9], v162 offset:1024
	ds_read_b128 v[10:13], v162 offset:2048
	ds_read_b128 v[14:17], v162 offset:3072
	ds_read_b128 v[18:21], v163
	ds_read_b128 v[22:25], v163 offset:1024
	ds_read_b128 v[26:29], v163 offset:2048
	ds_read_b128 v[30:33], v163 offset:3072
	s_add_u32 s14, s0, 0x100
	s_addc_u32 s15, s1, 0
	s_add_u32 s40, s0, 0x80
	s_addc_u32 s41, s1, 0
	v_mov_b32_e32 v66, v170
	s_add_i32 s18, s61, 0x8000
	ds_read_b128 v[34:37], v164
	ds_read_b128 v[38:41], v164 offset:1024
	ds_read_b128 v[42:45], v164 offset:2048
	ds_read_b128 v[46:49], v164 offset:3072
	ds_read_b128 v[50:53], v164 offset:4096
	ds_read_b128 v[54:57], v164 offset:5120
	ds_read_b128 v[58:61], v164 offset:6144
	ds_read_b128 v[62:65], v164 offset:7168
	s_mov_b32 m0, s18
	s_add_i32 s19, s61, 0xa000
	global_load_lds_dwordx4 v66, s[40:41]
	v_mov_b32_e32 v66, v172
	s_mov_b32 m0, s19
	s_nop 0
	global_load_lds_dwordx4 v66, s[40:41]
	s_add_u32 s40, s0, 0x40080
	s_addc_u32 s41, s1, 0
	v_mov_b32_e32 v66, v170
	s_add_i32 s50, s61, 0xc000
	s_mov_b32 m0, s50
	s_add_i32 s51, s61, 0xe000
	global_load_lds_dwordx4 v66, s[40:41]
	v_mov_b32_e32 v66, v172
	s_mov_b32 m0, s51
	s_nop 0
	global_load_lds_dwordx4 v66, s[40:41]
	s_waitcnt vmcnt(8)
	s_waitcnt lgkmcnt(0)
	s_barrier
	s_setprio 1
	s_waitcnt lgkmcnt(0)
	v_mfma_f32_16x16x128_f8f6f4 v[158:161], v[2:9], v[34:41], 0
	v_mfma_f32_16x16x128_f8f6f4 v[154:157], v[10:17], v[34:41], 0
	v_mfma_f32_16x16x128_f8f6f4 v[150:153], v[18:25], v[34:41], 0
	v_mfma_f32_16x16x128_f8f6f4 v[146:149], v[26:33], v[34:41], 0
	v_mfma_f32_16x16x128_f8f6f4 v[118:121], v[26:33], v[42:49], 0
	v_mfma_f32_16x16x128_f8f6f4 v[102:105], v[18:25], v[42:49], 0
	v_mfma_f32_16x16x128_f8f6f4 v[110:113], v[10:17], v[42:49], 0
	v_mfma_f32_16x16x128_f8f6f4 v[106:109], v[2:9], v[42:49], 0
	v_mfma_f32_16x16x128_f8f6f4 v[134:137], v[2:9], v[50:57], 0
	v_mfma_f32_16x16x128_f8f6f4 v[138:141], v[10:17], v[50:57], 0
	v_mfma_f32_16x16x128_f8f6f4 v[126:129], v[18:25], v[50:57], 0
	v_mfma_f32_16x16x128_f8f6f4 v[142:145], v[26:33], v[50:57], 0
	v_mfma_f32_16x16x128_f8f6f4 v[98:101], v[26:33], v[58:65], 0
	v_mfma_f32_16x16x128_f8f6f4 v[114:117], v[18:25], v[58:65], 0
	v_mfma_f32_16x16x128_f8f6f4 v[122:125], v[10:17], v[58:65], 0
	v_mfma_f32_16x16x128_f8f6f4 v[130:133], v[2:9], v[58:65], 0
	s_setprio 0
	s_barrier
	v_mov_b32_e32 v50, v171
	s_add_i32 s17, s17, s70
	ds_read_b128 v[34:37], v164 offset:16384
	ds_read_b128 v[38:41], v164 offset:17408
	ds_read_b128 v[42:45], v164 offset:18432
	ds_read_b128 v[46:49], v164 offset:19456
	ds_read_b128 v[180:183], v164 offset:20480
	ds_read_b128 v[184:187], v164 offset:21504
	ds_read_b128 v[188:191], v164 offset:22528
	ds_read_b128 v[192:195], v164 offset:23552
	s_mov_b32 m0, s17
	s_add_i32 s69, s17, 0x2000
	global_load_lds_dwordx4 v50, s[44:45]
	v_mov_b32_e32 v50, v173
	s_mov_b32 m0, s69
	s_add_i32 s16, s16, s70
	global_load_lds_dwordx4 v50, s[44:45]
	v_mov_b32_e32 v50, v171
	s_mov_b32 m0, s16
	s_add_i32 s70, s16, 0x2000
	global_load_lds_dwordx4 v50, s[52:53]
	v_mov_b32_e32 v50, v173
	s_mov_b32 m0, s70
	s_nop 0
	global_load_lds_dwordx4 v50, s[52:53]
	s_waitcnt vmcnt(6)
	s_waitcnt lgkmcnt(0)
	s_barrier
	s_setprio 1
	s_waitcnt lgkmcnt(0)
	v_mfma_f32_16x16x128_f8f6f4 v[94:97], v[2:9], v[34:41], 0
	v_mfma_f32_16x16x128_f8f6f4 v[90:93], v[10:17], v[34:41], 0
	v_mfma_f32_16x16x128_f8f6f4 v[86:89], v[18:25], v[34:41], 0
	v_mfma_f32_16x16x128_f8f6f4 v[82:85], v[26:33], v[34:41], 0
	v_mfma_f32_16x16x128_f8f6f4 v[66:69], v[26:33], v[42:49], 0
	v_mfma_f32_16x16x128_f8f6f4 v[70:73], v[18:25], v[42:49], 0
	v_mfma_f32_16x16x128_f8f6f4 v[74:77], v[10:17], v[42:49], 0
	v_mfma_f32_16x16x128_f8f6f4 v[78:81], v[2:9], v[42:49], 0
	v_mfma_f32_16x16x128_f8f6f4 v[62:65], v[2:9], v[180:187], 0
	v_mfma_f32_16x16x128_f8f6f4 v[58:61], v[10:17], v[180:187], 0
	v_mfma_f32_16x16x128_f8f6f4 v[54:57], v[18:25], v[180:187], 0
	v_mfma_f32_16x16x128_f8f6f4 v[50:53], v[26:33], v[180:187], 0
	v_mfma_f32_16x16x128_f8f6f4 v[34:37], v[26:33], v[188:195], 0
	v_mfma_f32_16x16x128_f8f6f4 v[38:41], v[18:25], v[188:195], 0
	v_mfma_f32_16x16x128_f8f6f4 v[42:45], v[10:17], v[188:195], 0
	v_mfma_f32_16x16x128_f8f6f4 v[46:49], v[2:9], v[188:195], 0
	s_setprio 0
	s_barrier
	ds_read_b128 v[26:29], v165
	ds_read_b128 v[30:33], v165 offset:1024
	ds_read_b128 v[18:21], v165 offset:2048
	ds_read_b128 v[22:25], v165 offset:3072
	ds_read_b128 v[10:13], v166
	ds_read_b128 v[14:17], v166 offset:1024
	ds_read_b128 v[2:5], v166 offset:2048
	ds_read_b128 v[6:9], v166 offset:3072
	v_mov_b32_e32 v167, v170
	s_mov_b32 m0, s61
	ds_read_b128 v[180:183], v164 offset:32768
	ds_read_b128 v[184:187], v164 offset:33792
	ds_read_b128 v[188:191], v164 offset:34816
	ds_read_b128 v[192:195], v164 offset:35840
	ds_read_b128 v[202:205], v164 offset:36864
	ds_read_b128 v[206:209], v164 offset:37888
	ds_read_b128 v[210:213], v164 offset:38912
	ds_read_b128 v[214:217], v164 offset:39936
	s_nop 0
	global_load_lds_dwordx4 v167, s[14:15]
	v_mov_b32_e32 v167, v172
	s_mov_b32 m0, s46
	s_nop 0
	global_load_lds_dwordx4 v167, s[14:15]
	s_add_u32 s14, s0, 0x40100
	s_addc_u32 s15, s1, 0
	v_mov_b32_e32 v167, v170
	s_mov_b32 m0, s47
	s_nop 0
	global_load_lds_dwordx4 v167, s[14:15]
	v_mov_b32_e32 v167, v172
	s_mov_b32 m0, s62
	s_nop 0
	global_load_lds_dwordx4 v167, s[14:15]
	s_waitcnt vmcnt(8)
	s_waitcnt lgkmcnt(0)
	s_barrier
	s_setprio 1
	s_waitcnt lgkmcnt(0)
	v_mfma_f32_16x16x128_f8f6f4 v[158:161], v[26:33], v[180:187], v[158:161]
	v_mfma_f32_16x16x128_f8f6f4 v[154:157], v[18:25], v[180:187], v[154:157]
	v_mfma_f32_16x16x128_f8f6f4 v[150:153], v[10:17], v[180:187], v[150:153]
	v_mfma_f32_16x16x128_f8f6f4 v[146:149], v[2:9], v[180:187], v[146:149]
	v_mfma_f32_16x16x128_f8f6f4 v[118:121], v[2:9], v[188:195], v[118:121]
	v_mfma_f32_16x16x128_f8f6f4 v[102:105], v[10:17], v[188:195], v[102:105]
	v_mfma_f32_16x16x128_f8f6f4 v[110:113], v[18:25], v[188:195], v[110:113]
	v_mfma_f32_16x16x128_f8f6f4 v[106:109], v[26:33], v[188:195], v[106:109]
	v_mfma_f32_16x16x128_f8f6f4 v[134:137], v[26:33], v[202:209], v[134:137]
	v_mfma_f32_16x16x128_f8f6f4 v[138:141], v[18:25], v[202:209], v[138:141]
	v_mfma_f32_16x16x128_f8f6f4 v[126:129], v[10:17], v[202:209], v[126:129]
	v_mfma_f32_16x16x128_f8f6f4 v[142:145], v[2:9], v[202:209], v[142:145]
	v_mfma_f32_16x16x128_f8f6f4 v[98:101], v[2:9], v[210:217], v[98:101]
	v_mfma_f32_16x16x128_f8f6f4 v[114:117], v[10:17], v[210:217], v[114:117]
	v_mfma_f32_16x16x128_f8f6f4 v[122:125], v[18:25], v[210:217], v[122:125]
	v_mfma_f32_16x16x128_f8f6f4 v[130:133], v[26:33], v[210:217], v[130:133]
	s_setprio 0
	s_barrier
	v_mov_b32_e32 v167, v171
	s_mov_b32 m0, s66
	ds_read_b128 v[180:183], v164 offset:49152
	ds_read_b128 v[184:187], v164 offset:50176
	ds_read_b128 v[188:191], v164 offset:51200
	ds_read_b128 v[192:195], v164 offset:52224
	ds_read_b128 v[202:205], v164 offset:53248
	ds_read_b128 v[206:209], v164 offset:54272
	ds_read_b128 v[210:213], v164 offset:55296
	ds_read_b128 v[214:217], v164 offset:56320
	s_nop 0
	global_load_lds_dwordx4 v167, s[42:43]
	v_mov_b32_e32 v167, v173
	s_mov_b32 m0, s67
	s_nop 0
	global_load_lds_dwordx4 v167, s[42:43]
	v_mov_b32_e32 v167, v171
	s_mov_b32 m0, s48
	s_nop 0
	global_load_lds_dwordx4 v167, s[64:65]
	v_mov_b32_e32 v167, v173
	s_mov_b32 m0, s49
	s_nop 0
	global_load_lds_dwordx4 v167, s[64:65]
	s_waitcnt vmcnt(6)
	s_waitcnt lgkmcnt(0)
	s_barrier
	s_setprio 1
	s_waitcnt lgkmcnt(0)
	v_mfma_f32_16x16x128_f8f6f4 v[94:97], v[26:33], v[180:187], v[94:97]
	v_mfma_f32_16x16x128_f8f6f4 v[90:93], v[18:25], v[180:187], v[90:93]
	v_mfma_f32_16x16x128_f8f6f4 v[86:89], v[10:17], v[180:187], v[86:89]
	v_mfma_f32_16x16x128_f8f6f4 v[82:85], v[2:9], v[180:187], v[82:85]
	v_mfma_f32_16x16x128_f8f6f4 v[66:69], v[2:9], v[188:195], v[66:69]
	v_mfma_f32_16x16x128_f8f6f4 v[70:73], v[10:17], v[188:195], v[70:73]
	v_mfma_f32_16x16x128_f8f6f4 v[74:77], v[18:25], v[188:195], v[74:77]
	v_mfma_f32_16x16x128_f8f6f4 v[78:81], v[26:33], v[188:195], v[78:81]
	v_mfma_f32_16x16x128_f8f6f4 v[62:65], v[26:33], v[202:209], v[62:65]
	v_mfma_f32_16x16x128_f8f6f4 v[58:61], v[18:25], v[202:209], v[58:61]
	v_mfma_f32_16x16x128_f8f6f4 v[54:57], v[10:17], v[202:209], v[54:57]
	v_mfma_f32_16x16x128_f8f6f4 v[50:53], v[2:9], v[202:209], v[50:53]
	v_mfma_f32_16x16x128_f8f6f4 v[34:37], v[2:9], v[210:217], v[34:37]
	v_mfma_f32_16x16x128_f8f6f4 v[38:41], v[10:17], v[210:217], v[38:41]
	v_mfma_f32_16x16x128_f8f6f4 v[42:45], v[18:25], v[210:217], v[42:45]
	v_mfma_f32_16x16x128_f8f6f4 v[46:49], v[26:33], v[210:217], v[46:49]
	s_setprio 0
	s_barrier
	s_add_i32 s10, s10, s11
	s_lshl_b32 s10, s10, 19
	s_add_i32 s10, s10, 0x200000
	s_add_u32 s10, s56, s10
	s_addc_u32 s11, s57, 0
	s_add_u32 s42, s10, 0x3ab00100
	s_addc_u32 s43, s11, 0
	.p2align	6

.LBB0_851:
	s_waitcnt vmcnt(8)
	s_waitcnt lgkmcnt(0)
	s_barrier
	s_setprio 1
	v_mfma_i32_16x16x64_i8 v[18:21], v[158:161], v[190:193], 0
	s_nop 0
	v_mfma_i32_16x16x64_i8 v[18:21], v[154:157], v[186:189], v[18:21]
	v_mfma_i32_16x16x64_i8 v[22:25], v[150:153], v[190:193], 0
	s_nop 0
	v_mfma_i32_16x16x64_i8 v[22:25], v[142:145], v[186:189], v[22:25]
	v_mfma_i32_16x16x64_i8 v[26:29], v[146:149], v[190:193], 0
	s_nop 0
	v_mfma_i32_16x16x64_i8 v[26:29], v[138:141], v[186:189], v[26:29]
	v_mfma_i32_16x16x64_i8 v[34:37], v[134:137], v[190:193], 0
	s_nop 0
	v_mfma_i32_16x16x64_i8 v[34:37], v[130:133], v[186:189], v[34:37]
	v_mfma_i32_16x16x64_i8 v[50:53], v[158:161], v[182:185], 0
	s_nop 0
	v_mfma_i32_16x16x64_i8 v[50:53], v[154:157], v[178:181], v[50:53]
	v_mfma_i32_16x16x64_i8 v[62:65], v[150:153], v[182:185], 0
	s_nop 0
	v_mfma_i32_16x16x64_i8 v[62:65], v[142:145], v[178:181], v[62:65]
	v_mfma_i32_16x16x64_i8 v[54:57], v[146:149], v[182:185], 0
	s_nop 0
	v_mfma_i32_16x16x64_i8 v[54:57], v[138:141], v[178:181], v[54:57]
	v_mfma_i32_16x16x64_i8 v[66:69], v[134:137], v[182:185], 0
	s_nop 0
	v_mfma_i32_16x16x64_i8 v[66:69], v[130:133], v[178:181], v[66:69]
	v_mfma_i32_16x16x64_i8 v[82:85], v[158:161], v[174:177], 0
	s_nop 0
	v_mfma_i32_16x16x64_i8 v[82:85], v[154:157], v[170:173], v[82:85]
	v_mfma_i32_16x16x64_i8 v[94:97], v[150:153], v[174:177], 0
	s_nop 0
	v_mfma_i32_16x16x64_i8 v[94:97], v[142:145], v[170:173], v[94:97]
	v_mfma_i32_16x16x64_i8 v[86:89], v[146:149], v[174:177], 0
	s_nop 0
	v_mfma_i32_16x16x64_i8 v[86:89], v[138:141], v[170:173], v[86:89]
	v_mfma_i32_16x16x64_i8 v[98:101], v[134:137], v[174:177], 0
	s_nop 0
	v_mfma_i32_16x16x64_i8 v[98:101], v[130:133], v[170:173], v[98:101]
	v_mfma_i32_16x16x64_i8 v[114:117], v[158:161], v[166:169], 0
	s_nop 0
	v_mfma_i32_16x16x64_i8 v[114:117], v[154:157], v[162:165], v[114:117]
	v_mfma_i32_16x16x64_i8 v[122:125], v[150:153], v[166:169], 0
	s_nop 0
	v_mfma_i32_16x16x64_i8 v[122:125], v[142:145], v[162:165], v[122:125]
	v_mfma_i32_16x16x64_i8 v[118:121], v[146:149], v[166:169], 0
	s_nop 0
	v_mfma_i32_16x16x64_i8 v[118:121], v[138:141], v[162:165], v[118:121]
	v_mfma_i32_16x16x64_i8 v[126:129], v[134:137], v[166:169], 0
	s_nop 0
	v_mfma_i32_16x16x64_i8 v[126:129], v[130:133], v[162:165], v[126:129]
	s_setprio 0
	s_barrier
	s_add_u32 s81, s74, s50
	s_addc_u32 s82, s75, s51
	s_cmp_eq_u32 s43, 12
	s_cselect_b64 s[76:77], -1, 0
	s_and_b64 s[78:79], s[76:77], exec
	s_cselect_b32 s65, s65, s82
	s_cselect_b32 s64, s64, s81
	s_mov_b64 s[78:79], s[64:65]
	v_mov_b32_e32 v209, v202
	s_mov_b32 m0, s21
	s_waitcnt lgkmcnt(0)
	ds_read_b128 v[190:193], v207 offset:16384
	ds_read_b128 v[186:189], v207 offset:17408
	ds_read_b128 v[182:185], v207 offset:18432
	ds_read_b128 v[178:181], v207 offset:19456
	ds_read_b128 v[174:177], v207 offset:20480
	ds_read_b128 v[170:173], v207 offset:21504
	ds_read_b128 v[166:169], v207 offset:22528
	ds_read_b128 v[162:165], v207 offset:23552
	s_nop 0
	global_load_lds_dwordx4 v209, s[78:79]
	v_mov_b32_e32 v209, v204
	s_mov_b32 m0, s33
	s_nop 0
	global_load_lds_dwordx4 v209, s[78:79]
	s_add_u32 s78, s64, 0x40000
	s_addc_u32 s79, s65, 0
	v_mov_b32_e32 v209, v202
	s_mov_b32 m0, s35
	s_nop 0
	global_load_lds_dwordx4 v209, s[78:79]
	v_mov_b32_e32 v209, v204
	s_mov_b32 m0, s60
	s_nop 0
	global_load_lds_dwordx4 v209, s[78:79]
	s_waitcnt vmcnt(6)
	s_waitcnt lgkmcnt(0)
	s_barrier
	s_setprio 1
	v_mfma_i32_16x16x64_i8 v[2:5], v[158:161], v[190:193], 0
	s_nop 0
	v_mfma_i32_16x16x64_i8 v[2:5], v[154:157], v[186:189], v[2:5]
	v_mfma_i32_16x16x64_i8 v[6:9], v[150:153], v[190:193], 0
	s_nop 0
	v_mfma_i32_16x16x64_i8 v[6:9], v[142:145], v[186:189], v[6:9]
	v_mfma_i32_16x16x64_i8 v[10:13], v[146:149], v[190:193], 0
	s_nop 0
	v_mfma_i32_16x16x64_i8 v[10:13], v[138:141], v[186:189], v[10:13]
	v_mfma_i32_16x16x64_i8 v[14:17], v[134:137], v[190:193], 0
	s_nop 0
	v_mfma_i32_16x16x64_i8 v[14:17], v[130:133], v[186:189], v[14:17]
	v_mfma_i32_16x16x64_i8 v[30:33], v[158:161], v[182:185], 0
	s_nop 0
	v_mfma_i32_16x16x64_i8 v[30:33], v[154:157], v[178:181], v[30:33]
	v_mfma_i32_16x16x64_i8 v[42:45], v[150:153], v[182:185], 0
	s_nop 0
	v_mfma_i32_16x16x64_i8 v[42:45], v[142:145], v[178:181], v[42:45]
	v_mfma_i32_16x16x64_i8 v[38:41], v[146:149], v[182:185], 0
	s_nop 0
	v_mfma_i32_16x16x64_i8 v[38:41], v[138:141], v[178:181], v[38:41]
	v_mfma_i32_16x16x64_i8 v[46:49], v[134:137], v[182:185], 0
	s_nop 0
	v_mfma_i32_16x16x64_i8 v[46:49], v[130:133], v[178:181], v[46:49]
	v_mfma_i32_16x16x64_i8 v[58:61], v[158:161], v[174:177], 0
	s_nop 0
	v_mfma_i32_16x16x64_i8 v[58:61], v[154:157], v[170:173], v[58:61]
	v_mfma_i32_16x16x64_i8 v[74:77], v[150:153], v[174:177], 0
	s_nop 0
	v_mfma_i32_16x16x64_i8 v[74:77], v[142:145], v[170:173], v[74:77]
	v_mfma_i32_16x16x64_i8 v[70:73], v[146:149], v[174:177], 0
	s_nop 0
	v_mfma_i32_16x16x64_i8 v[70:73], v[138:141], v[170:173], v[70:73]
	v_mfma_i32_16x16x64_i8 v[78:81], v[134:137], v[174:177], 0
	s_nop 0
	v_mfma_i32_16x16x64_i8 v[78:81], v[130:133], v[170:173], v[78:81]
	v_mfma_i32_16x16x64_i8 v[90:93], v[158:161], v[166:169], 0
	s_nop 0
	v_mfma_i32_16x16x64_i8 v[90:93], v[154:157], v[162:165], v[90:93]
	v_mfma_i32_16x16x64_i8 v[106:109], v[150:153], v[166:169], 0
	s_nop 0
	v_mfma_i32_16x16x64_i8 v[106:109], v[142:145], v[162:165], v[106:109]
	v_mfma_i32_16x16x64_i8 v[102:105], v[146:149], v[166:169], 0
	s_nop 0
	v_mfma_i32_16x16x64_i8 v[102:105], v[138:141], v[162:165], v[102:105]
	v_mfma_i32_16x16x64_i8 v[110:113], v[134:137], v[166:169], 0
	s_nop 0
	v_mfma_i32_16x16x64_i8 v[110:113], v[130:133], v[162:165], v[110:113]
	s_setprio 0
	s_barrier
	s_add_u32 s45, s45, 0x100
	s_addc_u32 s78, s80, 0
	s_and_b64 s[66:67], s[76:77], exec
	s_cselect_b32 s67, s53, s78
	s_cselect_b32 s66, s52, s45
	s_add_u32 s52, s64, 0x80
	s_addc_u32 s53, s65, 0
	s_add_i32 s45, 0, 0x18000
	s_add_i32 s78, 0, 0x1c000
	v_add_u32_e32 v130, s45, v206
	v_add_u32_e32 v131, s78, v206
	ds_read_b128 v[158:161], v130
	ds_read_b128 v[154:157], v130 offset:1024
	ds_read_b128 v[150:153], v130 offset:2048
	ds_read_b128 v[146:149], v130 offset:3072
	ds_read_b128 v[142:145], v131
	ds_read_b128 v[138:141], v131 offset:1024
	ds_read_b128 v[134:137], v131 offset:2048
	ds_read_b128 v[130:133], v131 offset:3072
	s_mov_b64 s[76:77], s[66:67]
	v_mov_b32_e32 v209, v201
	s_mov_b32 m0, s1
	s_waitcnt lgkmcnt(0)
	ds_read_b128 v[162:165], v207 offset:32768
	ds_read_b128 v[166:169], v207 offset:33792
	ds_read_b128 v[170:173], v207 offset:34816
	ds_read_b128 v[174:177], v207 offset:35840
	ds_read_b128 v[178:181], v207 offset:36864
	ds_read_b128 v[182:185], v207 offset:37888
	ds_read_b128 v[186:189], v207 offset:38912
	ds_read_b128 v[190:193], v207 offset:39936
	s_add_u32 s66, s66, 0x40000
	global_load_lds_dwordx4 v209, s[76:77]
	v_mov_b32_e32 v209, v203
	s_mov_b32 m0, s61
	s_addc_u32 s67, s67, 0
	global_load_lds_dwordx4 v209, s[76:77]
	v_mov_b32_e32 v209, v201
	s_mov_b32 m0, s62
	s_nop 0
	global_load_lds_dwordx4 v209, s[66:67]
	v_mov_b32_e32 v209, v203
	s_mov_b32 m0, s63
	s_nop 0
	global_load_lds_dwordx4 v209, s[66:67]
	s_waitcnt vmcnt(8)
	s_waitcnt lgkmcnt(0)
	s_barrier
	s_setprio 1
	s_waitcnt lgkmcnt(0)
	v_mfma_i32_16x16x64_i8 v[18:21], v[158:161], v[162:165], v[18:21]
	s_nop 0
	v_mfma_i32_16x16x64_i8 v[18:21], v[154:157], v[166:169], v[18:21]
	v_mfma_i32_16x16x64_i8 v[22:25], v[150:153], v[162:165], v[22:25]
	s_nop 0
	v_mfma_i32_16x16x64_i8 v[22:25], v[146:149], v[166:169], v[22:25]
	v_mfma_i32_16x16x64_i8 v[26:29], v[142:145], v[162:165], v[26:29]
	s_nop 0
	v_mfma_i32_16x16x64_i8 v[26:29], v[138:141], v[166:169], v[26:29]
	v_mfma_i32_16x16x64_i8 v[34:37], v[134:137], v[162:165], v[34:37]
	s_nop 0
	v_mfma_i32_16x16x64_i8 v[34:37], v[130:133], v[166:169], v[34:37]
	v_mfma_i32_16x16x64_i8 v[50:53], v[158:161], v[170:173], v[50:53]
	s_nop 0
	v_mfma_i32_16x16x64_i8 v[50:53], v[154:157], v[174:177], v[50:53]
	v_mfma_i32_16x16x64_i8 v[62:65], v[150:153], v[170:173], v[62:65]
	s_nop 0
	v_mfma_i32_16x16x64_i8 v[62:65], v[146:149], v[174:177], v[62:65]
	v_mfma_i32_16x16x64_i8 v[54:57], v[142:145], v[170:173], v[54:57]
	s_nop 0
	v_mfma_i32_16x16x64_i8 v[54:57], v[138:141], v[174:177], v[54:57]
	v_mfma_i32_16x16x64_i8 v[66:69], v[134:137], v[170:173], v[66:69]
	s_nop 0
	v_mfma_i32_16x16x64_i8 v[66:69], v[130:133], v[174:177], v[66:69]
	v_mfma_i32_16x16x64_i8 v[82:85], v[158:161], v[178:181], v[82:85]
	s_nop 0
	v_mfma_i32_16x16x64_i8 v[82:85], v[154:157], v[182:185], v[82:85]
	v_mfma_i32_16x16x64_i8 v[94:97], v[150:153], v[178:181], v[94:97]
	s_nop 0
	v_mfma_i32_16x16x64_i8 v[94:97], v[146:149], v[182:185], v[94:97]
	v_mfma_i32_16x16x64_i8 v[86:89], v[142:145], v[178:181], v[86:89]
	s_nop 0
	v_mfma_i32_16x16x64_i8 v[86:89], v[138:141], v[182:185], v[86:89]
	v_mfma_i32_16x16x64_i8 v[98:101], v[134:137], v[178:181], v[98:101]
	s_nop 0
	v_mfma_i32_16x16x64_i8 v[98:101], v[130:133], v[182:185], v[98:101]
	v_mfma_i32_16x16x64_i8 v[114:117], v[158:161], v[186:189], v[114:117]
	s_nop 0
	v_mfma_i32_16x16x64_i8 v[114:117], v[154:157], v[190:193], v[114:117]
	v_mfma_i32_16x16x64_i8 v[122:125], v[150:153], v[186:189], v[122:125]
	s_nop 0
	v_mfma_i32_16x16x64_i8 v[122:125], v[146:149], v[190:193], v[122:125]
	v_mfma_i32_16x16x64_i8 v[118:121], v[142:145], v[186:189], v[118:121]
	s_nop 0
	v_mfma_i32_16x16x64_i8 v[118:121], v[138:141], v[190:193], v[118:121]
	v_mfma_i32_16x16x64_i8 v[126:129], v[134:137], v[186:189], v[126:129]
	s_nop 0
	v_mfma_i32_16x16x64_i8 v[126:129], v[130:133], v[190:193], v[126:129]
	s_setprio 0
	s_barrier
	v_mov_b32_e32 v209, v202
	s_add_i32 s45, s45, s10
	ds_read_b128 v[162:165], v207 offset:49152
	ds_read_b128 v[166:169], v207 offset:50176
	ds_read_b128 v[170:173], v207 offset:51200
	ds_read_b128 v[174:177], v207 offset:52224
	ds_read_b128 v[178:181], v207 offset:53248
	ds_read_b128 v[182:185], v207 offset:54272
	ds_read_b128 v[186:189], v207 offset:55296
	ds_read_b128 v[190:193], v207 offset:56320
	s_mov_b32 m0, s45
	s_nop 0
	global_load_lds_dwordx4 v209, s[52:53]
	v_mov_b32_e32 v209, v204
	s_add_i32 m0, s45, 0x2000
	s_nop 0
	global_load_lds_dwordx4 v209, s[52:53]
	s_add_u32 s52, s64, 0x40080
	s_addc_u32 s53, s65, 0
	v_mov_b32_e32 v209, v202
	s_add_i32 s45, s78, s10
	s_mov_b32 m0, s45
	s_nop 0
	global_load_lds_dwordx4 v209, s[52:53]
	v_mov_b32_e32 v209, v204
	s_add_i32 m0, s45, 0x2000
	s_nop 0
	global_load_lds_dwordx4 v209, s[52:53]
	s_waitcnt vmcnt(6)
	s_waitcnt lgkmcnt(0)
	s_barrier
	s_setprio 1
	s_waitcnt lgkmcnt(0)
	v_mfma_i32_16x16x64_i8 v[2:5], v[158:161], v[162:165], v[2:5]
	s_nop 0
	v_mfma_i32_16x16x64_i8 v[2:5], v[154:157], v[166:169], v[2:5]
	v_mfma_i32_16x16x64_i8 v[6:9], v[150:153], v[162:165], v[6:9]
	s_nop 0
	v_mfma_i32_16x16x64_i8 v[6:9], v[146:149], v[166:169], v[6:9]
	v_mfma_i32_16x16x64_i8 v[10:13], v[142:145], v[162:165], v[10:13]
	s_nop 0
	v_mfma_i32_16x16x64_i8 v[10:13], v[138:141], v[166:169], v[10:13]
	v_mfma_i32_16x16x64_i8 v[14:17], v[134:137], v[162:165], v[14:17]
	s_nop 0
	v_mfma_i32_16x16x64_i8 v[14:17], v[130:133], v[166:169], v[14:17]
	v_mfma_i32_16x16x64_i8 v[30:33], v[158:161], v[170:173], v[30:33]
	s_nop 0
	v_mfma_i32_16x16x64_i8 v[30:33], v[154:157], v[174:177], v[30:33]
	v_mfma_i32_16x16x64_i8 v[42:45], v[150:153], v[170:173], v[42:45]
	s_nop 0
	v_mfma_i32_16x16x64_i8 v[42:45], v[146:149], v[174:177], v[42:45]
	v_mfma_i32_16x16x64_i8 v[38:41], v[142:145], v[170:173], v[38:41]
	s_nop 0
	v_mfma_i32_16x16x64_i8 v[38:41], v[138:141], v[174:177], v[38:41]
	v_mfma_i32_16x16x64_i8 v[46:49], v[134:137], v[170:173], v[46:49]
	s_nop 0
	v_mfma_i32_16x16x64_i8 v[46:49], v[130:133], v[174:177], v[46:49]
	v_mfma_i32_16x16x64_i8 v[58:61], v[158:161], v[178:181], v[58:61]
	s_nop 0
	v_mfma_i32_16x16x64_i8 v[58:61], v[154:157], v[182:185], v[58:61]
	v_mfma_i32_16x16x64_i8 v[74:77], v[150:153], v[178:181], v[74:77]
	s_nop 0
	v_mfma_i32_16x16x64_i8 v[74:77], v[146:149], v[182:185], v[74:77]
	v_mfma_i32_16x16x64_i8 v[70:73], v[142:145], v[178:181], v[70:73]
	s_nop 0
	v_mfma_i32_16x16x64_i8 v[70:73], v[138:141], v[182:185], v[70:73]
	v_mfma_i32_16x16x64_i8 v[78:81], v[134:137], v[178:181], v[78:81]
	s_nop 0
	v_mfma_i32_16x16x64_i8 v[78:81], v[130:133], v[182:185], v[78:81]
	v_mfma_i32_16x16x64_i8 v[90:93], v[158:161], v[186:189], v[90:93]
	s_nop 0
	v_mfma_i32_16x16x64_i8 v[90:93], v[154:157], v[190:193], v[90:93]
	v_mfma_i32_16x16x64_i8 v[106:109], v[150:153], v[186:189], v[106:109]
	s_nop 0
	v_mfma_i32_16x16x64_i8 v[106:109], v[146:149], v[190:193], v[106:109]
	v_mfma_i32_16x16x64_i8 v[102:105], v[142:145], v[186:189], v[102:105]
	s_nop 0
	v_mfma_i32_16x16x64_i8 v[102:105], v[138:141], v[190:193], v[102:105]
	v_mfma_i32_16x16x64_i8 v[110:113], v[134:137], v[186:189], v[110:113]
	s_nop 0
	v_mfma_i32_16x16x64_i8 v[110:113], v[130:133], v[190:193], v[110:113]
	s_setprio 0
	s_barrier
	s_add_i32 s43, s43, 2
	s_add_u32 s50, s50, 0x100
	s_addc_u32 s51, s51, 0
	s_cmp_gt_u32 s43, 13
	s_cbranch_scc1 .LBB0_861
	s_mov_b64 s[64:65], s[8:9]
	s_mov_b64 s[52:53], s[26:27]
	.p2align	6

.LBB0_930:
	s_and_b32 s64, s63, 3
	s_lshl_b32 s3, s2, 13
	s_lshl_b32 s7, s64, 12
	s_add_u32 s46, s28, 0x4000
	s_addc_u32 s47, s29, 0
	s_add_i32 s33, 0, 0x18000
	s_mov_b64 s[8:9], s[46:47]
	s_add_i32 s67, s33, s6
	v_mov_b32_e32 v2, v170
	s_waitcnt vmcnt(2)
	s_barrier
	s_mov_b32 m0, s67
	s_add_i32 s69, s67, 0x2000
	global_load_lds_dwordx4 v2, s[8:9]
	v_mov_b32_e32 v2, v171
	s_add_u32 s48, s28, 0xb4000
	s_mov_b32 m0, s69
	s_addc_u32 s49, s29, 0
	s_add_i32 s60, 0, 0x1c000
	global_load_lds_dwordx4 v2, s[8:9]
	s_mov_b64 s[8:9], s[48:49]
	s_add_i32 s70, s60, s6
	v_mov_b32_e32 v2, v170
	s_mov_b32 m0, s70
	s_add_i32 s71, s70, 0x2000
	global_load_lds_dwordx4 v2, s[8:9]
	v_mov_b32_e32 v2, v171
	s_mov_b32 m0, s71
	v_lshlrev_b32_e32 v5, 6, v0
	global_load_lds_dwordx4 v2, s[8:9]
	v_and_b32_e32 v2, 48, v0
	v_and_b32_e32 v5, 0x3c0, v5
	v_and_b32_e32 v172, 15, v0
	v_and_b32_e32 v3, 32, v200
	s_waitcnt vmcnt(0)
	v_or_b32_e32 v6, v5, v2
	v_lshl_or_b32 v173, v172, 6, v2
	v_bitop3_b32 v174, v5, v3, v2 bitop3:0x36
	v_bitop3_b32 v2, s7, v6, v3 bitop3:0xf6
	s_add_i32 s21, 0, 0x10000
	v_bitop3_b32 v4, v173, s3, v3 bitop3:0xde
	v_add_u32_e32 v162, s21, v2
	s_add_i32 s20, 0, 0x14000
	s_waitcnt vmcnt(6)
	s_barrier
	v_add_u32_e32 v163, s20, v2
	v_add_u32_e32 v164, 0, v4
	v_add_u32_e32 v165, s33, v2
	v_add_u32_e32 v166, s60, v2
	ds_read_b128 v[2:5], v162
	s_waitcnt lgkmcnt(0)
	ds_read_b128 v[6:9], v162 offset:1024
	ds_read_b128 v[10:13], v162 offset:2048
	ds_read_b128 v[14:17], v162 offset:3072
	ds_read_b128 v[18:21], v163
	ds_read_b128 v[22:25], v163 offset:1024
	ds_read_b128 v[26:29], v163 offset:2048
	ds_read_b128 v[30:33], v163 offset:3072
	v_lshl_or_b32 v177, s2, 6, v172
	s_add_u32 s2, s0, 0x8000
	s_addc_u32 s3, s1, 0
	s_add_u32 s42, s28, 0x8000
	s_addc_u32 s43, s29, 0
	s_add_u32 s8, s0, 0x4000
	s_addc_u32 s9, s1, 0
	v_mov_b32_e32 v66, v170
	s_add_i32 s72, s18, 0x8000
	ds_read_b128 v[34:37], v164
	ds_read_b128 v[38:41], v164 offset:1024
	ds_read_b128 v[42:45], v164 offset:2048
	ds_read_b128 v[46:49], v164 offset:3072
	ds_read_b128 v[50:53], v164 offset:4096
	ds_read_b128 v[54:57], v164 offset:5120
	ds_read_b128 v[58:61], v164 offset:6144
	ds_read_b128 v[62:65], v164 offset:7168
	s_mov_b32 m0, s72
	s_add_i32 s73, s18, 0xa000
	global_load_lds_dwordx4 v66, s[8:9]
	v_mov_b32_e32 v66, v171
	s_mov_b32 m0, s73
	s_nop 0
	global_load_lds_dwordx4 v66, s[8:9]
	s_add_u32 s8, s0, 0xb4000
	s_addc_u32 s9, s1, 0
	v_mov_b32_e32 v66, v170
	s_add_i32 s74, s18, 0xc000
	s_mov_b32 m0, s74
	s_add_i32 s75, s18, 0xe000
	global_load_lds_dwordx4 v66, s[8:9]
	v_mov_b32_e32 v66, v171
	s_mov_b32 m0, s75
	s_add_u32 s40, s28, 0xc000
	global_load_lds_dwordx4 v66, s[8:9]
	s_waitcnt vmcnt(8)
	s_waitcnt lgkmcnt(0)
	s_addc_u32 s41, s29, 0
	s_barrier
	s_setprio 1
	s_waitcnt lgkmcnt(0)
	v_mfma_f32_16x16x128_f8f6f4 v[150:153], v[2:9], v[34:41], 0
	v_mfma_f32_16x16x128_f8f6f4 v[154:157], v[10:17], v[34:41], 0
	v_mfma_f32_16x16x128_f8f6f4 v[158:161], v[18:25], v[34:41], 0
	v_mfma_f32_16x16x128_f8f6f4 v[146:149], v[26:33], v[34:41], 0
	v_mfma_f32_16x16x128_f8f6f4 v[98:101], v[26:33], v[42:49], 0
	v_mfma_f32_16x16x128_f8f6f4 v[102:105], v[18:25], v[42:49], 0
	v_mfma_f32_16x16x128_f8f6f4 v[122:125], v[10:17], v[42:49], 0
	v_mfma_f32_16x16x128_f8f6f4 v[126:129], v[2:9], v[42:49], 0
	v_mfma_f32_16x16x128_f8f6f4 v[142:145], v[2:9], v[50:57], 0
	v_mfma_f32_16x16x128_f8f6f4 v[138:141], v[10:17], v[50:57], 0
	v_mfma_f32_16x16x128_f8f6f4 v[134:137], v[18:25], v[50:57], 0
	v_mfma_f32_16x16x128_f8f6f4 v[130:133], v[26:33], v[50:57], 0
	v_mfma_f32_16x16x128_f8f6f4 v[106:109], v[26:33], v[58:65], 0
	v_mfma_f32_16x16x128_f8f6f4 v[110:113], v[18:25], v[58:65], 0
	v_mfma_f32_16x16x128_f8f6f4 v[114:117], v[10:17], v[58:65], 0
	v_mfma_f32_16x16x128_f8f6f4 v[118:121], v[2:9], v[58:65], 0
	s_setprio 0
	s_barrier
	s_mov_b64 s[8:9], s[42:43]
	v_mov_b32_e32 v50, v170
	s_add_i32 s76, s21, s6
	ds_read_b128 v[34:37], v164 offset:16384
	ds_read_b128 v[38:41], v164 offset:17408
	ds_read_b128 v[42:45], v164 offset:18432
	ds_read_b128 v[46:49], v164 offset:19456
	ds_read_b128 v[178:181], v164 offset:20480
	ds_read_b128 v[182:185], v164 offset:21504
	ds_read_b128 v[186:189], v164 offset:22528
	ds_read_b128 v[190:193], v164 offset:23552
	s_mov_b32 m0, s76
	s_add_i32 s77, s76, 0x2000
	global_load_lds_dwordx4 v50, s[8:9]
	v_mov_b32_e32 v50, v171
	s_add_u32 s50, s28, 0xb8000
	s_mov_b32 m0, s77
	s_addc_u32 s51, s29, 0
	global_load_lds_dwordx4 v50, s[8:9]
	s_mov_b64 s[8:9], s[50:51]
	v_mov_b32_e32 v50, v170
	s_add_i32 s78, s20, s6
	s_mov_b32 m0, s78
	s_add_i32 s79, s78, 0x2000
	global_load_lds_dwordx4 v50, s[8:9]
	v_mov_b32_e32 v50, v171
	s_mov_b32 m0, s79
	s_nop 0
	global_load_lds_dwordx4 v50, s[8:9]
	s_waitcnt vmcnt(6)
	s_waitcnt lgkmcnt(0)
	s_barrier
	s_setprio 1
	s_waitcnt lgkmcnt(0)
	v_mfma_f32_16x16x128_f8f6f4 v[94:97], v[2:9], v[34:41], 0
	v_mfma_f32_16x16x128_f8f6f4 v[90:93], v[10:17], v[34:41], 0
	v_mfma_f32_16x16x128_f8f6f4 v[86:89], v[18:25], v[34:41], 0
	v_mfma_f32_16x16x128_f8f6f4 v[82:85], v[26:33], v[34:41], 0
	v_mfma_f32_16x16x128_f8f6f4 v[66:69], v[26:33], v[42:49], 0
	v_mfma_f32_16x16x128_f8f6f4 v[70:73], v[18:25], v[42:49], 0
	v_mfma_f32_16x16x128_f8f6f4 v[74:77], v[10:17], v[42:49], 0
	v_mfma_f32_16x16x128_f8f6f4 v[78:81], v[2:9], v[42:49], 0
	v_mfma_f32_16x16x128_f8f6f4 v[62:65], v[2:9], v[178:185], 0
	v_mfma_f32_16x16x128_f8f6f4 v[58:61], v[10:17], v[178:185], 0
	v_mfma_f32_16x16x128_f8f6f4 v[54:57], v[18:25], v[178:185], 0
	v_mfma_f32_16x16x128_f8f6f4 v[50:53], v[26:33], v[178:185], 0
	v_mfma_f32_16x16x128_f8f6f4 v[34:37], v[26:33], v[186:193], 0
	v_mfma_f32_16x16x128_f8f6f4 v[38:41], v[18:25], v[186:193], 0
	v_mfma_f32_16x16x128_f8f6f4 v[42:45], v[10:17], v[186:193], 0
	v_mfma_f32_16x16x128_f8f6f4 v[46:49], v[2:9], v[186:193], 0
	s_setprio 0
	s_barrier
	ds_read_b128 v[26:29], v165
	ds_read_b128 v[30:33], v165 offset:1024
	ds_read_b128 v[18:21], v165 offset:2048
	ds_read_b128 v[22:25], v165 offset:3072
	ds_read_b128 v[10:13], v166
	ds_read_b128 v[14:17], v166 offset:1024
	ds_read_b128 v[2:5], v166 offset:2048
	ds_read_b128 v[6:9], v166 offset:3072
	v_mov_b32_e32 v167, v170
	s_mov_b32 m0, s18
	ds_read_b128 v[178:181], v164 offset:32768
	ds_read_b128 v[182:185], v164 offset:33792
	ds_read_b128 v[186:189], v164 offset:34816
	ds_read_b128 v[190:193], v164 offset:35840
	ds_read_b128 v[202:205], v164 offset:36864
	ds_read_b128 v[206:209], v164 offset:37888
	ds_read_b128 v[210:213], v164 offset:38912
	ds_read_b128 v[214:217], v164 offset:39936
	s_nop 0
	global_load_lds_dwordx4 v167, s[2:3]
	v_mov_b32_e32 v167, v171
	s_mov_b32 m0, s19
	s_nop 0
	global_load_lds_dwordx4 v167, s[2:3]
	s_add_u32 s2, s0, 0xb8000
	s_addc_u32 s3, s1, 0
	v_mov_b32_e32 v167, v170
	s_mov_b32 m0, s61
	s_nop 0
	global_load_lds_dwordx4 v167, s[2:3]
	v_mov_b32_e32 v167, v171
	s_mov_b32 m0, s65
	s_nop 0
	global_load_lds_dwordx4 v167, s[2:3]
	s_waitcnt vmcnt(8)
	s_waitcnt lgkmcnt(0)
	s_barrier
	s_setprio 1
	s_waitcnt lgkmcnt(0)
	v_mfma_f32_16x16x128_f8f6f4 v[150:153], v[26:33], v[178:185], v[150:153]
	v_mfma_f32_16x16x128_f8f6f4 v[154:157], v[18:25], v[178:185], v[154:157]
	v_mfma_f32_16x16x128_f8f6f4 v[158:161], v[10:17], v[178:185], v[158:161]
	v_mfma_f32_16x16x128_f8f6f4 v[146:149], v[2:9], v[178:185], v[146:149]
	v_mfma_f32_16x16x128_f8f6f4 v[98:101], v[2:9], v[186:193], v[98:101]
	v_mfma_f32_16x16x128_f8f6f4 v[102:105], v[10:17], v[186:193], v[102:105]
	v_mfma_f32_16x16x128_f8f6f4 v[122:125], v[18:25], v[186:193], v[122:125]
	v_mfma_f32_16x16x128_f8f6f4 v[126:129], v[26:33], v[186:193], v[126:129]
	v_mfma_f32_16x16x128_f8f6f4 v[142:145], v[26:33], v[202:209], v[142:145]
	v_mfma_f32_16x16x128_f8f6f4 v[138:141], v[18:25], v[202:209], v[138:141]
	v_mfma_f32_16x16x128_f8f6f4 v[134:137], v[10:17], v[202:209], v[134:137]
	v_mfma_f32_16x16x128_f8f6f4 v[130:133], v[2:9], v[202:209], v[130:133]
	v_mfma_f32_16x16x128_f8f6f4 v[106:109], v[2:9], v[210:217], v[106:109]
	v_mfma_f32_16x16x128_f8f6f4 v[110:113], v[10:17], v[210:217], v[110:113]
	v_mfma_f32_16x16x128_f8f6f4 v[114:117], v[18:25], v[210:217], v[114:117]
	v_mfma_f32_16x16x128_f8f6f4 v[118:121], v[26:33], v[210:217], v[118:121]
	s_setprio 0
	s_barrier
	s_mov_b64 s[2:3], s[40:41]
	v_mov_b32_e32 v167, v170
	s_mov_b32 m0, s67
	ds_read_b128 v[178:181], v164 offset:49152
	ds_read_b128 v[182:185], v164 offset:50176
	ds_read_b128 v[186:189], v164 offset:51200
	ds_read_b128 v[190:193], v164 offset:52224
	ds_read_b128 v[202:205], v164 offset:53248
	ds_read_b128 v[206:209], v164 offset:54272
	ds_read_b128 v[210:213], v164 offset:55296
	ds_read_b128 v[214:217], v164 offset:56320
	s_add_u32 s52, s28, 0xbc000
	global_load_lds_dwordx4 v167, s[2:3]
	v_mov_b32_e32 v167, v171
	s_mov_b32 m0, s69
	s_addc_u32 s53, s29, 0
	global_load_lds_dwordx4 v167, s[2:3]
	s_mov_b64 s[2:3], s[52:53]
	v_mov_b32_e32 v167, v170
	s_mov_b32 m0, s70
	s_nop 0
	global_load_lds_dwordx4 v167, s[2:3]
	v_mov_b32_e32 v167, v171
	s_mov_b32 m0, s71
	s_nop 0
	global_load_lds_dwordx4 v167, s[2:3]
	s_waitcnt vmcnt(6)
	s_waitcnt lgkmcnt(0)
	s_barrier
	s_setprio 1
	s_waitcnt lgkmcnt(0)
	v_mfma_f32_16x16x128_f8f6f4 v[94:97], v[26:33], v[178:185], v[94:97]
	v_mfma_f32_16x16x128_f8f6f4 v[90:93], v[18:25], v[178:185], v[90:93]
	v_mfma_f32_16x16x128_f8f6f4 v[86:89], v[10:17], v[178:185], v[86:89]
	v_mfma_f32_16x16x128_f8f6f4 v[82:85], v[2:9], v[178:185], v[82:85]
	v_mfma_f32_16x16x128_f8f6f4 v[66:69], v[2:9], v[186:193], v[66:69]
	v_mfma_f32_16x16x128_f8f6f4 v[70:73], v[10:17], v[186:193], v[70:73]
	v_mfma_f32_16x16x128_f8f6f4 v[74:77], v[18:25], v[186:193], v[74:77]
	v_mfma_f32_16x16x128_f8f6f4 v[78:81], v[26:33], v[186:193], v[78:81]
	v_mfma_f32_16x16x128_f8f6f4 v[62:65], v[26:33], v[202:209], v[62:65]
	v_mfma_f32_16x16x128_f8f6f4 v[58:61], v[18:25], v[202:209], v[58:61]
	v_mfma_f32_16x16x128_f8f6f4 v[54:57], v[10:17], v[202:209], v[54:57]
	v_mfma_f32_16x16x128_f8f6f4 v[50:53], v[2:9], v[202:209], v[50:53]
	v_mfma_f32_16x16x128_f8f6f4 v[34:37], v[2:9], v[210:217], v[34:37]
	v_mfma_f32_16x16x128_f8f6f4 v[38:41], v[10:17], v[210:217], v[38:41]
	v_mfma_f32_16x16x128_f8f6f4 v[42:45], v[18:25], v[210:217], v[42:45]
	v_mfma_f32_16x16x128_f8f6f4 v[46:49], v[26:33], v[210:217], v[46:49]
	s_setprio 0
	s_barrier
	s_and_b32 s2, s12, 7
	s_mul_i32 s2, s2, 0xb00000
	s_mul_i32 s3, s11, 0x160000
	s_add_i32 s2, s2, s3
	s_add_u32 s2, s56, s2
	s_addc_u32 s3, s57, 0
	s_add_u32 s8, s2, 0x3eb08000
	s_addc_u32 s9, s3, 0
	s_add_u32 s2, s56, s5
	s_addc_u32 s3, s57, s4
	s_add_u32 s30, s2, 0x4310000
	s_addc_u32 s31, s3, 0
	s_mov_b64 s[2:3], s[30:31]
	.p2align	6

.LBB0_977:
	s_add_i32 s69, s33, s72
	v_mov_b32_e32 v2, v170
	s_waitcnt vmcnt(2)
	s_barrier
	s_mov_b32 m0, s69
	s_add_i32 s70, s69, 0x2000
	global_load_lds_dwordx4 v2, s[46:47]
	v_mov_b32_e32 v2, v171
	s_mov_b32 m0, s70
	s_and_b32 s44, s63, 3
	global_load_lds_dwordx4 v2, s[46:47]
	s_add_i32 s46, s60, s72
	v_mov_b32_e32 v2, v170
	s_mov_b32 m0, s46
	s_add_i32 s47, s46, 0x2000
	global_load_lds_dwordx4 v2, s[48:49]
	v_mov_b32_e32 v2, v171
	s_mov_b32 m0, s47
	v_lshl_or_b32 v177, s14, 6, v172
	global_load_lds_dwordx4 v2, s[48:49]
	v_lshlrev_b32_e32 v2, 2, v172
	s_lshl_b32 s14, s14, 13
	v_and_b32_e32 v2, 32, v2
	v_lshl_or_b32 v3, s44, 12, v174
	v_bitop3_b32 v2, v173, s14, v2 bitop3:0xde
	v_add_u32_e32 v162, s21, v3
	s_waitcnt vmcnt(6)
	s_barrier
	v_add_u32_e32 v163, s20, v3
	v_add_u32_e32 v164, 0, v2
	v_add_u32_e32 v165, s33, v3
	v_add_u32_e32 v166, s60, v3
	ds_read_b128 v[2:5], v162
	ds_read_b128 v[6:9], v162 offset:1024
	ds_read_b128 v[10:13], v162 offset:2048
	ds_read_b128 v[14:17], v162 offset:3072
	ds_read_b128 v[18:21], v163
	ds_read_b128 v[22:25], v163 offset:1024
	ds_read_b128 v[26:29], v163 offset:2048
	ds_read_b128 v[30:33], v163 offset:3072
	s_add_u32 s14, s0, 0x8000
	s_addc_u32 s15, s1, 0
	s_add_u32 s16, s0, 0x4000
	s_addc_u32 s17, s1, 0
	v_mov_b32_e32 v66, v170
	s_add_i32 s33, s64, 0x8000
	ds_read_b128 v[34:37], v164
	ds_read_b128 v[38:41], v164 offset:1024
	ds_read_b128 v[42:45], v164 offset:2048
	ds_read_b128 v[46:49], v164 offset:3072
	ds_read_b128 v[50:53], v164 offset:4096
	ds_read_b128 v[54:57], v164 offset:5120
	ds_read_b128 v[58:61], v164 offset:6144
	ds_read_b128 v[62:65], v164 offset:7168
	s_mov_b32 m0, s33
	s_add_i32 s48, s64, 0xa000
	global_load_lds_dwordx4 v66, s[16:17]
	v_mov_b32_e32 v66, v171
	s_mov_b32 m0, s48
	s_nop 0
	global_load_lds_dwordx4 v66, s[16:17]
	s_add_u32 s16, s0, 0xb4000
	s_addc_u32 s17, s1, 0
	v_mov_b32_e32 v66, v170
	s_add_i32 s49, s64, 0xc000
	s_mov_b32 m0, s49
	s_add_i32 s60, s64, 0xe000
	global_load_lds_dwordx4 v66, s[16:17]
	v_mov_b32_e32 v66, v171
	s_mov_b32 m0, s60
	s_nop 0
	global_load_lds_dwordx4 v66, s[16:17]
	s_waitcnt vmcnt(8)
	s_waitcnt lgkmcnt(0)
	s_barrier
	s_setprio 1
	s_waitcnt lgkmcnt(0)
	v_mfma_f32_16x16x128_f8f6f4 v[146:149], v[2:9], v[34:41], 0
	v_mfma_f32_16x16x128_f8f6f4 v[150:153], v[10:17], v[34:41], 0
	v_mfma_f32_16x16x128_f8f6f4 v[154:157], v[18:25], v[34:41], 0
	v_mfma_f32_16x16x128_f8f6f4 v[158:161], v[26:33], v[34:41], 0
	v_mfma_f32_16x16x128_f8f6f4 v[98:101], v[26:33], v[42:49], 0
	v_mfma_f32_16x16x128_f8f6f4 v[102:105], v[18:25], v[42:49], 0
	v_mfma_f32_16x16x128_f8f6f4 v[106:109], v[10:17], v[42:49], 0
	v_mfma_f32_16x16x128_f8f6f4 v[110:113], v[2:9], v[42:49], 0
	v_mfma_f32_16x16x128_f8f6f4 v[142:145], v[2:9], v[50:57], 0
	v_mfma_f32_16x16x128_f8f6f4 v[138:141], v[10:17], v[50:57], 0
	v_mfma_f32_16x16x128_f8f6f4 v[134:137], v[18:25], v[50:57], 0
	v_mfma_f32_16x16x128_f8f6f4 v[130:133], v[26:33], v[50:57], 0
	v_mfma_f32_16x16x128_f8f6f4 v[114:117], v[26:33], v[58:65], 0
	v_mfma_f32_16x16x128_f8f6f4 v[118:121], v[18:25], v[58:65], 0
	v_mfma_f32_16x16x128_f8f6f4 v[122:125], v[10:17], v[58:65], 0
	v_mfma_f32_16x16x128_f8f6f4 v[126:129], v[2:9], v[58:65], 0
	s_setprio 0
	s_barrier
	v_mov_b32_e32 v50, v170
	s_add_i32 s21, s21, s72
	ds_read_b128 v[34:37], v164 offset:16384
	ds_read_b128 v[38:41], v164 offset:17408
	ds_read_b128 v[42:45], v164 offset:18432
	ds_read_b128 v[46:49], v164 offset:19456
	ds_read_b128 v[178:181], v164 offset:20480
	ds_read_b128 v[182:185], v164 offset:21504
	ds_read_b128 v[186:189], v164 offset:22528
	ds_read_b128 v[190:193], v164 offset:23552
	s_mov_b32 m0, s21
	s_add_i32 s71, s21, 0x2000
	global_load_lds_dwordx4 v50, s[42:43]
	v_mov_b32_e32 v50, v171
	s_mov_b32 m0, s71
	s_add_i32 s20, s20, s72
	global_load_lds_dwordx4 v50, s[42:43]
	v_mov_b32_e32 v50, v170
	s_mov_b32 m0, s20
	s_add_i32 s72, s20, 0x2000
	global_load_lds_dwordx4 v50, s[50:51]
	v_mov_b32_e32 v50, v171
	s_mov_b32 m0, s72
	s_nop 0
	global_load_lds_dwordx4 v50, s[50:51]
	s_waitcnt vmcnt(6)
	s_waitcnt lgkmcnt(0)
	s_barrier
	s_setprio 1
	s_waitcnt lgkmcnt(0)
	v_mfma_f32_16x16x128_f8f6f4 v[94:97], v[2:9], v[34:41], 0
	v_mfma_f32_16x16x128_f8f6f4 v[90:93], v[10:17], v[34:41], 0
	v_mfma_f32_16x16x128_f8f6f4 v[86:89], v[18:25], v[34:41], 0
	v_mfma_f32_16x16x128_f8f6f4 v[82:85], v[26:33], v[34:41], 0
	v_mfma_f32_16x16x128_f8f6f4 v[66:69], v[26:33], v[42:49], 0
	v_mfma_f32_16x16x128_f8f6f4 v[70:73], v[18:25], v[42:49], 0
	v_mfma_f32_16x16x128_f8f6f4 v[74:77], v[10:17], v[42:49], 0
	v_mfma_f32_16x16x128_f8f6f4 v[78:81], v[2:9], v[42:49], 0
	v_mfma_f32_16x16x128_f8f6f4 v[62:65], v[2:9], v[178:185], 0
	v_mfma_f32_16x16x128_f8f6f4 v[58:61], v[10:17], v[178:185], 0
	v_mfma_f32_16x16x128_f8f6f4 v[54:57], v[18:25], v[178:185], 0
	v_mfma_f32_16x16x128_f8f6f4 v[50:53], v[26:33], v[178:185], 0
	v_mfma_f32_16x16x128_f8f6f4 v[34:37], v[26:33], v[186:193], 0
	v_mfma_f32_16x16x128_f8f6f4 v[38:41], v[18:25], v[186:193], 0
	v_mfma_f32_16x16x128_f8f6f4 v[42:45], v[10:17], v[186:193], 0
	v_mfma_f32_16x16x128_f8f6f4 v[46:49], v[2:9], v[186:193], 0
	s_setprio 0
	s_barrier
	ds_read_b128 v[26:29], v165
	ds_read_b128 v[30:33], v165 offset:1024
	ds_read_b128 v[18:21], v165 offset:2048
	ds_read_b128 v[22:25], v165 offset:3072
	ds_read_b128 v[10:13], v166
	ds_read_b128 v[14:17], v166 offset:1024
	ds_read_b128 v[2:5], v166 offset:2048
	ds_read_b128 v[6:9], v166 offset:3072
	v_mov_b32_e32 v167, v170
	s_mov_b32 m0, s64
	ds_read_b128 v[178:181], v164 offset:32768
	ds_read_b128 v[182:185], v164 offset:33792
	ds_read_b128 v[186:189], v164 offset:34816
	ds_read_b128 v[190:193], v164 offset:35840
	ds_read_b128 v[202:205], v164 offset:36864
	ds_read_b128 v[206:209], v164 offset:37888
	ds_read_b128 v[210:213], v164 offset:38912
	ds_read_b128 v[214:217], v164 offset:39936
	s_nop 0
	global_load_lds_dwordx4 v167, s[14:15]
	v_mov_b32_e32 v167, v171
	s_mov_b32 m0, s45
	s_nop 0
	global_load_lds_dwordx4 v167, s[14:15]
	s_add_u32 s14, s0, 0xb8000
	s_addc_u32 s15, s1, 0
	v_mov_b32_e32 v167, v170
	s_mov_b32 m0, s65
	s_nop 0
	global_load_lds_dwordx4 v167, s[14:15]
	v_mov_b32_e32 v167, v171
	s_mov_b32 m0, s66
	s_nop 0
	global_load_lds_dwordx4 v167, s[14:15]
	s_waitcnt vmcnt(8)
	s_waitcnt lgkmcnt(0)
	s_barrier
	s_setprio 1
	s_waitcnt lgkmcnt(0)
	v_mfma_f32_16x16x128_f8f6f4 v[146:149], v[26:33], v[178:185], v[146:149]
	v_mfma_f32_16x16x128_f8f6f4 v[150:153], v[18:25], v[178:185], v[150:153]
	v_mfma_f32_16x16x128_f8f6f4 v[154:157], v[10:17], v[178:185], v[154:157]
	v_mfma_f32_16x16x128_f8f6f4 v[158:161], v[2:9], v[178:185], v[158:161]
	v_mfma_f32_16x16x128_f8f6f4 v[98:101], v[2:9], v[186:193], v[98:101]
	v_mfma_f32_16x16x128_f8f6f4 v[102:105], v[10:17], v[186:193], v[102:105]
	v_mfma_f32_16x16x128_f8f6f4 v[106:109], v[18:25], v[186:193], v[106:109]
	v_mfma_f32_16x16x128_f8f6f4 v[110:113], v[26:33], v[186:193], v[110:113]
	v_mfma_f32_16x16x128_f8f6f4 v[142:145], v[26:33], v[202:209], v[142:145]
	v_mfma_f32_16x16x128_f8f6f4 v[138:141], v[18:25], v[202:209], v[138:141]
	v_mfma_f32_16x16x128_f8f6f4 v[134:137], v[10:17], v[202:209], v[134:137]
	v_mfma_f32_16x16x128_f8f6f4 v[130:133], v[2:9], v[202:209], v[130:133]
	v_mfma_f32_16x16x128_f8f6f4 v[114:117], v[2:9], v[210:217], v[114:117]
	v_mfma_f32_16x16x128_f8f6f4 v[118:121], v[10:17], v[210:217], v[118:121]
	v_mfma_f32_16x16x128_f8f6f4 v[122:125], v[18:25], v[210:217], v[122:125]
	v_mfma_f32_16x16x128_f8f6f4 v[126:129], v[26:33], v[210:217], v[126:129]
	s_setprio 0
	s_barrier
	v_mov_b32_e32 v167, v170
	s_mov_b32 m0, s69
	ds_read_b128 v[178:181], v164 offset:49152
	ds_read_b128 v[182:185], v164 offset:50176
	ds_read_b128 v[186:189], v164 offset:51200
	ds_read_b128 v[190:193], v164 offset:52224
	ds_read_b128 v[202:205], v164 offset:53248
	ds_read_b128 v[206:209], v164 offset:54272
	ds_read_b128 v[210:213], v164 offset:55296
	ds_read_b128 v[214:217], v164 offset:56320
	s_nop 0
	global_load_lds_dwordx4 v167, s[40:41]
	v_mov_b32_e32 v167, v171
	s_mov_b32 m0, s70
	s_nop 0
	global_load_lds_dwordx4 v167, s[40:41]
	v_mov_b32_e32 v167, v170
	s_mov_b32 m0, s46
	s_nop 0
	global_load_lds_dwordx4 v167, s[52:53]
	v_mov_b32_e32 v167, v171
	s_mov_b32 m0, s47
	s_nop 0
	global_load_lds_dwordx4 v167, s[52:53]
	s_waitcnt vmcnt(6)
	s_waitcnt lgkmcnt(0)
	s_barrier
	s_setprio 1
	s_waitcnt lgkmcnt(0)
	v_mfma_f32_16x16x128_f8f6f4 v[94:97], v[26:33], v[178:185], v[94:97]
	v_mfma_f32_16x16x128_f8f6f4 v[90:93], v[18:25], v[178:185], v[90:93]
	v_mfma_f32_16x16x128_f8f6f4 v[86:89], v[10:17], v[178:185], v[86:89]
	v_mfma_f32_16x16x128_f8f6f4 v[82:85], v[2:9], v[178:185], v[82:85]
	v_mfma_f32_16x16x128_f8f6f4 v[66:69], v[2:9], v[186:193], v[66:69]
	v_mfma_f32_16x16x128_f8f6f4 v[70:73], v[10:17], v[186:193], v[70:73]
	v_mfma_f32_16x16x128_f8f6f4 v[74:77], v[18:25], v[186:193], v[74:77]
	v_mfma_f32_16x16x128_f8f6f4 v[78:81], v[26:33], v[186:193], v[78:81]
	v_mfma_f32_16x16x128_f8f6f4 v[62:65], v[26:33], v[202:209], v[62:65]
	v_mfma_f32_16x16x128_f8f6f4 v[58:61], v[18:25], v[202:209], v[58:61]
	v_mfma_f32_16x16x128_f8f6f4 v[54:57], v[10:17], v[202:209], v[54:57]
	v_mfma_f32_16x16x128_f8f6f4 v[50:53], v[2:9], v[202:209], v[50:53]
	v_mfma_f32_16x16x128_f8f6f4 v[34:37], v[2:9], v[210:217], v[34:37]
	v_mfma_f32_16x16x128_f8f6f4 v[38:41], v[10:17], v[210:217], v[38:41]
	v_mfma_f32_16x16x128_f8f6f4 v[42:45], v[18:25], v[210:217], v[42:45]
	v_mfma_f32_16x16x128_f8f6f4 v[46:49], v[26:33], v[210:217], v[46:49]
	s_setprio 0
	s_barrier
	s_add_i32 s10, s10, s11
	s_mul_i32 s10, s10, 0x160000
	s_add_i32 s10, s10, 0x580000
	s_add_u32 s10, s56, s10
	s_addc_u32 s11, s57, 0
	s_add_u32 s40, s10, 0x3eb08000
	s_addc_u32 s41, s11, 0
	.p2align	6

.LBB0_1088:
	s_waitcnt vmcnt(8)
	s_waitcnt lgkmcnt(0)
	s_barrier
	s_setprio 1
	v_mfma_i32_16x16x64_i8 v[18:21], v[158:161], v[190:193], 0
	s_nop 0
	v_mfma_i32_16x16x64_i8 v[18:21], v[154:157], v[186:189], v[18:21]
	v_mfma_i32_16x16x64_i8 v[22:25], v[150:153], v[190:193], 0
	s_nop 0
	v_mfma_i32_16x16x64_i8 v[22:25], v[142:145], v[186:189], v[22:25]
	v_mfma_i32_16x16x64_i8 v[26:29], v[146:149], v[190:193], 0
	s_nop 0
	v_mfma_i32_16x16x64_i8 v[26:29], v[138:141], v[186:189], v[26:29]
	v_mfma_i32_16x16x64_i8 v[34:37], v[134:137], v[190:193], 0
	s_nop 0
	v_mfma_i32_16x16x64_i8 v[34:37], v[130:133], v[186:189], v[34:37]
	v_mfma_i32_16x16x64_i8 v[50:53], v[158:161], v[182:185], 0
	s_nop 0
	v_mfma_i32_16x16x64_i8 v[50:53], v[154:157], v[178:181], v[50:53]
	v_mfma_i32_16x16x64_i8 v[62:65], v[150:153], v[182:185], 0
	s_nop 0
	v_mfma_i32_16x16x64_i8 v[62:65], v[142:145], v[178:181], v[62:65]
	v_mfma_i32_16x16x64_i8 v[54:57], v[146:149], v[182:185], 0
	s_nop 0
	v_mfma_i32_16x16x64_i8 v[54:57], v[138:141], v[178:181], v[54:57]
	v_mfma_i32_16x16x64_i8 v[66:69], v[134:137], v[182:185], 0
	s_nop 0
	v_mfma_i32_16x16x64_i8 v[66:69], v[130:133], v[178:181], v[66:69]
	v_mfma_i32_16x16x64_i8 v[82:85], v[158:161], v[174:177], 0
	s_nop 0
	v_mfma_i32_16x16x64_i8 v[82:85], v[154:157], v[170:173], v[82:85]
	v_mfma_i32_16x16x64_i8 v[94:97], v[150:153], v[174:177], 0
	s_nop 0
	v_mfma_i32_16x16x64_i8 v[94:97], v[142:145], v[170:173], v[94:97]
	v_mfma_i32_16x16x64_i8 v[86:89], v[146:149], v[174:177], 0
	s_nop 0
	v_mfma_i32_16x16x64_i8 v[86:89], v[138:141], v[170:173], v[86:89]
	v_mfma_i32_16x16x64_i8 v[98:101], v[134:137], v[174:177], 0
	s_nop 0
	v_mfma_i32_16x16x64_i8 v[98:101], v[130:133], v[170:173], v[98:101]
	v_mfma_i32_16x16x64_i8 v[114:117], v[158:161], v[166:169], 0
	s_nop 0
	v_mfma_i32_16x16x64_i8 v[114:117], v[154:157], v[162:165], v[114:117]
	v_mfma_i32_16x16x64_i8 v[122:125], v[150:153], v[166:169], 0
	s_nop 0
	v_mfma_i32_16x16x64_i8 v[122:125], v[142:145], v[162:165], v[122:125]
	v_mfma_i32_16x16x64_i8 v[118:121], v[146:149], v[166:169], 0
	s_nop 0
	v_mfma_i32_16x16x64_i8 v[118:121], v[138:141], v[162:165], v[118:121]
	v_mfma_i32_16x16x64_i8 v[126:129], v[134:137], v[166:169], 0
	s_nop 0
	v_mfma_i32_16x16x64_i8 v[126:129], v[130:133], v[162:165], v[126:129]
	s_setprio 0
	s_barrier
	s_add_u32 s81, s77, s48
	s_addc_u32 s82, s78, s49
	s_cmp_eq_u32 s41, 12
	s_cselect_b64 s[66:67], -1, 0
	s_and_b64 s[74:75], s[66:67], exec
	s_cselect_b32 s53, s53, s82
	s_cselect_b32 s52, s52, s81
	s_mov_b64 s[74:75], s[52:53]
	v_mov_b32_e32 v205, v197
	s_mov_b32 m0, s33
	s_waitcnt lgkmcnt(0)
	ds_read_b128 v[190:193], v204 offset:16384
	ds_read_b128 v[186:189], v204 offset:17408
	ds_read_b128 v[182:185], v204 offset:18432
	ds_read_b128 v[178:181], v204 offset:19456
	ds_read_b128 v[174:177], v204 offset:20480
	ds_read_b128 v[170:173], v204 offset:21504
	ds_read_b128 v[166:169], v204 offset:22528
	ds_read_b128 v[162:165], v204 offset:23552
	s_nop 0
	global_load_lds_dwordx4 v205, s[74:75]
	v_mov_b32_e32 v205, v199
	s_mov_b32 m0, s35
	s_nop 0
	global_load_lds_dwordx4 v205, s[74:75]
	s_add_u32 s74, s52, 0x40000
	s_addc_u32 s75, s53, 0
	v_mov_b32_e32 v205, v197
	s_mov_b32 m0, s60
	s_nop 0
	global_load_lds_dwordx4 v205, s[74:75]
	v_mov_b32_e32 v205, v199
	s_mov_b32 m0, s61
	s_nop 0
	global_load_lds_dwordx4 v205, s[74:75]
	s_waitcnt vmcnt(6)
	s_waitcnt lgkmcnt(0)
	s_barrier
	s_setprio 1
	v_mfma_i32_16x16x64_i8 v[2:5], v[158:161], v[190:193], 0
	s_nop 0
	v_mfma_i32_16x16x64_i8 v[2:5], v[154:157], v[186:189], v[2:5]
	v_mfma_i32_16x16x64_i8 v[6:9], v[150:153], v[190:193], 0
	s_nop 0
	v_mfma_i32_16x16x64_i8 v[6:9], v[142:145], v[186:189], v[6:9]
	v_mfma_i32_16x16x64_i8 v[10:13], v[146:149], v[190:193], 0
	s_nop 0
	v_mfma_i32_16x16x64_i8 v[10:13], v[138:141], v[186:189], v[10:13]
	v_mfma_i32_16x16x64_i8 v[14:17], v[134:137], v[190:193], 0
	s_nop 0
	v_mfma_i32_16x16x64_i8 v[14:17], v[130:133], v[186:189], v[14:17]
	v_mfma_i32_16x16x64_i8 v[30:33], v[158:161], v[182:185], 0
	s_nop 0
	v_mfma_i32_16x16x64_i8 v[30:33], v[154:157], v[178:181], v[30:33]
	v_mfma_i32_16x16x64_i8 v[42:45], v[150:153], v[182:185], 0
	s_nop 0
	v_mfma_i32_16x16x64_i8 v[42:45], v[142:145], v[178:181], v[42:45]
	v_mfma_i32_16x16x64_i8 v[38:41], v[146:149], v[182:185], 0
	s_nop 0
	v_mfma_i32_16x16x64_i8 v[38:41], v[138:141], v[178:181], v[38:41]
	v_mfma_i32_16x16x64_i8 v[46:49], v[134:137], v[182:185], 0
	s_nop 0
	v_mfma_i32_16x16x64_i8 v[46:49], v[130:133], v[178:181], v[46:49]
	v_mfma_i32_16x16x64_i8 v[58:61], v[158:161], v[174:177], 0
	s_nop 0
	v_mfma_i32_16x16x64_i8 v[58:61], v[154:157], v[170:173], v[58:61]
	v_mfma_i32_16x16x64_i8 v[74:77], v[150:153], v[174:177], 0
	s_nop 0
	v_mfma_i32_16x16x64_i8 v[74:77], v[142:145], v[170:173], v[74:77]
	v_mfma_i32_16x16x64_i8 v[70:73], v[146:149], v[174:177], 0
	s_nop 0
	v_mfma_i32_16x16x64_i8 v[70:73], v[138:141], v[170:173], v[70:73]
	v_mfma_i32_16x16x64_i8 v[78:81], v[134:137], v[174:177], 0
	s_nop 0
	v_mfma_i32_16x16x64_i8 v[78:81], v[130:133], v[170:173], v[78:81]
	v_mfma_i32_16x16x64_i8 v[90:93], v[158:161], v[166:169], 0
	s_nop 0
	v_mfma_i32_16x16x64_i8 v[90:93], v[154:157], v[162:165], v[90:93]
	v_mfma_i32_16x16x64_i8 v[106:109], v[150:153], v[166:169], 0
	s_nop 0
	v_mfma_i32_16x16x64_i8 v[106:109], v[142:145], v[162:165], v[106:109]
	v_mfma_i32_16x16x64_i8 v[102:105], v[146:149], v[166:169], 0
	s_nop 0
	v_mfma_i32_16x16x64_i8 v[102:105], v[138:141], v[162:165], v[102:105]
	v_mfma_i32_16x16x64_i8 v[110:113], v[134:137], v[166:169], 0
	s_nop 0
	v_mfma_i32_16x16x64_i8 v[110:113], v[130:133], v[162:165], v[110:113]
	s_setprio 0
	s_barrier
	s_add_u32 s43, s43, 0x100
	s_addc_u32 s74, s80, 0
	s_and_b64 s[64:65], s[66:67], exec
	s_cselect_b32 s65, s51, s74
	s_cselect_b32 s64, s50, s43
	s_add_u32 s50, s52, 0x80
	s_addc_u32 s51, s53, 0
	s_add_i32 s43, 0, 0x18000
	s_add_i32 s74, 0, 0x1c000
	v_add_u32_e32 v130, s43, v202
	v_add_u32_e32 v131, s74, v202
	ds_read_b128 v[158:161], v130
	ds_read_b128 v[154:157], v130 offset:1024
	ds_read_b128 v[150:153], v130 offset:2048
	ds_read_b128 v[146:149], v130 offset:3072
	ds_read_b128 v[142:145], v131
	ds_read_b128 v[138:141], v131 offset:1024
	ds_read_b128 v[134:137], v131 offset:2048
	ds_read_b128 v[130:133], v131 offset:3072
	s_mov_b64 s[66:67], s[64:65]
	v_mov_b32_e32 v205, v196
	s_mov_b32 m0, s5
	s_waitcnt lgkmcnt(0)
	ds_read_b128 v[162:165], v204 offset:32768
	ds_read_b128 v[166:169], v204 offset:33792
	ds_read_b128 v[170:173], v204 offset:34816
	ds_read_b128 v[174:177], v204 offset:35840
	ds_read_b128 v[178:181], v204 offset:36864
	ds_read_b128 v[182:185], v204 offset:37888
	ds_read_b128 v[186:189], v204 offset:38912
	ds_read_b128 v[190:193], v204 offset:39936
	s_add_u32 s64, s64, 0x40000
	global_load_lds_dwordx4 v205, s[66:67]
	v_mov_b32_e32 v205, v198
	s_mov_b32 m0, s62
	s_addc_u32 s65, s65, 0
	global_load_lds_dwordx4 v205, s[66:67]
	v_mov_b32_e32 v205, v196
	s_mov_b32 m0, s63
	s_nop 0
	global_load_lds_dwordx4 v205, s[64:65]
	v_mov_b32_e32 v205, v198
	s_mov_b32 m0, s69
	s_nop 0
	global_load_lds_dwordx4 v205, s[64:65]
	s_waitcnt vmcnt(8)
	s_waitcnt lgkmcnt(0)
	s_barrier
	s_setprio 1
	s_waitcnt lgkmcnt(0)
	v_mfma_i32_16x16x64_i8 v[18:21], v[158:161], v[162:165], v[18:21]
	s_nop 0
	v_mfma_i32_16x16x64_i8 v[18:21], v[154:157], v[166:169], v[18:21]
	v_mfma_i32_16x16x64_i8 v[22:25], v[150:153], v[162:165], v[22:25]
	s_nop 0
	v_mfma_i32_16x16x64_i8 v[22:25], v[146:149], v[166:169], v[22:25]
	v_mfma_i32_16x16x64_i8 v[26:29], v[142:145], v[162:165], v[26:29]
	s_nop 0
	v_mfma_i32_16x16x64_i8 v[26:29], v[138:141], v[166:169], v[26:29]
	v_mfma_i32_16x16x64_i8 v[34:37], v[134:137], v[162:165], v[34:37]
	s_nop 0
	v_mfma_i32_16x16x64_i8 v[34:37], v[130:133], v[166:169], v[34:37]
	v_mfma_i32_16x16x64_i8 v[50:53], v[158:161], v[170:173], v[50:53]
	s_nop 0
	v_mfma_i32_16x16x64_i8 v[50:53], v[154:157], v[174:177], v[50:53]
	v_mfma_i32_16x16x64_i8 v[62:65], v[150:153], v[170:173], v[62:65]
	s_nop 0
	v_mfma_i32_16x16x64_i8 v[62:65], v[146:149], v[174:177], v[62:65]
	v_mfma_i32_16x16x64_i8 v[54:57], v[142:145], v[170:173], v[54:57]
	s_nop 0
	v_mfma_i32_16x16x64_i8 v[54:57], v[138:141], v[174:177], v[54:57]
	v_mfma_i32_16x16x64_i8 v[66:69], v[134:137], v[170:173], v[66:69]
	s_nop 0
	v_mfma_i32_16x16x64_i8 v[66:69], v[130:133], v[174:177], v[66:69]
	v_mfma_i32_16x16x64_i8 v[82:85], v[158:161], v[178:181], v[82:85]
	s_nop 0
	v_mfma_i32_16x16x64_i8 v[82:85], v[154:157], v[182:185], v[82:85]
	v_mfma_i32_16x16x64_i8 v[94:97], v[150:153], v[178:181], v[94:97]
	s_nop 0
	v_mfma_i32_16x16x64_i8 v[94:97], v[146:149], v[182:185], v[94:97]
	v_mfma_i32_16x16x64_i8 v[86:89], v[142:145], v[178:181], v[86:89]
	s_nop 0
	v_mfma_i32_16x16x64_i8 v[86:89], v[138:141], v[182:185], v[86:89]
	v_mfma_i32_16x16x64_i8 v[98:101], v[134:137], v[178:181], v[98:101]
	s_nop 0
	v_mfma_i32_16x16x64_i8 v[98:101], v[130:133], v[182:185], v[98:101]
	v_mfma_i32_16x16x64_i8 v[114:117], v[158:161], v[186:189], v[114:117]
	s_nop 0
	v_mfma_i32_16x16x64_i8 v[114:117], v[154:157], v[190:193], v[114:117]
	v_mfma_i32_16x16x64_i8 v[122:125], v[150:153], v[186:189], v[122:125]
	s_nop 0
	v_mfma_i32_16x16x64_i8 v[122:125], v[146:149], v[190:193], v[122:125]
	v_mfma_i32_16x16x64_i8 v[118:121], v[142:145], v[186:189], v[118:121]
	s_nop 0
	v_mfma_i32_16x16x64_i8 v[118:121], v[138:141], v[190:193], v[118:121]
	v_mfma_i32_16x16x64_i8 v[126:129], v[134:137], v[186:189], v[126:129]
	s_nop 0
	v_mfma_i32_16x16x64_i8 v[126:129], v[130:133], v[190:193], v[126:129]
	s_setprio 0
	s_barrier
	v_mov_b32_e32 v205, v197
	s_add_i32 s43, s43, s10
	ds_read_b128 v[162:165], v204 offset:49152
	ds_read_b128 v[166:169], v204 offset:50176
	ds_read_b128 v[170:173], v204 offset:51200
	ds_read_b128 v[174:177], v204 offset:52224
	ds_read_b128 v[178:181], v204 offset:53248
	ds_read_b128 v[182:185], v204 offset:54272
	ds_read_b128 v[186:189], v204 offset:55296
	ds_read_b128 v[190:193], v204 offset:56320
	s_mov_b32 m0, s43
	s_nop 0
	global_load_lds_dwordx4 v205, s[50:51]
	v_mov_b32_e32 v205, v199
	s_add_i32 m0, s43, 0x2000
	s_nop 0
	global_load_lds_dwordx4 v205, s[50:51]
	s_add_u32 s50, s52, 0x40080
	s_addc_u32 s51, s53, 0
	v_mov_b32_e32 v205, v197
	s_add_i32 s43, s74, s10
	s_mov_b32 m0, s43
	s_nop 0
	global_load_lds_dwordx4 v205, s[50:51]
	v_mov_b32_e32 v205, v199
	s_add_i32 m0, s43, 0x2000
	s_nop 0
	global_load_lds_dwordx4 v205, s[50:51]
	s_waitcnt vmcnt(6)
	s_waitcnt lgkmcnt(0)
	s_barrier
	s_setprio 1
	s_waitcnt lgkmcnt(0)
	v_mfma_i32_16x16x64_i8 v[2:5], v[158:161], v[162:165], v[2:5]
	s_nop 0
	v_mfma_i32_16x16x64_i8 v[2:5], v[154:157], v[166:169], v[2:5]
	v_mfma_i32_16x16x64_i8 v[6:9], v[150:153], v[162:165], v[6:9]
	s_nop 0
	v_mfma_i32_16x16x64_i8 v[6:9], v[146:149], v[166:169], v[6:9]
	v_mfma_i32_16x16x64_i8 v[10:13], v[142:145], v[162:165], v[10:13]
	s_nop 0
	v_mfma_i32_16x16x64_i8 v[10:13], v[138:141], v[166:169], v[10:13]
	v_mfma_i32_16x16x64_i8 v[14:17], v[134:137], v[162:165], v[14:17]
	s_nop 0
	v_mfma_i32_16x16x64_i8 v[14:17], v[130:133], v[166:169], v[14:17]
	v_mfma_i32_16x16x64_i8 v[30:33], v[158:161], v[170:173], v[30:33]
	s_nop 0
	v_mfma_i32_16x16x64_i8 v[30:33], v[154:157], v[174:177], v[30:33]
	v_mfma_i32_16x16x64_i8 v[42:45], v[150:153], v[170:173], v[42:45]
	s_nop 0
	v_mfma_i32_16x16x64_i8 v[42:45], v[146:149], v[174:177], v[42:45]
	v_mfma_i32_16x16x64_i8 v[38:41], v[142:145], v[170:173], v[38:41]
	s_nop 0
	v_mfma_i32_16x16x64_i8 v[38:41], v[138:141], v[174:177], v[38:41]
	v_mfma_i32_16x16x64_i8 v[46:49], v[134:137], v[170:173], v[46:49]
	s_nop 0
	v_mfma_i32_16x16x64_i8 v[46:49], v[130:133], v[174:177], v[46:49]
	v_mfma_i32_16x16x64_i8 v[58:61], v[158:161], v[178:181], v[58:61]
	s_nop 0
	v_mfma_i32_16x16x64_i8 v[58:61], v[154:157], v[182:185], v[58:61]
	v_mfma_i32_16x16x64_i8 v[74:77], v[150:153], v[178:181], v[74:77]
	s_nop 0
	v_mfma_i32_16x16x64_i8 v[74:77], v[146:149], v[182:185], v[74:77]
	v_mfma_i32_16x16x64_i8 v[70:73], v[142:145], v[178:181], v[70:73]
	s_nop 0
	v_mfma_i32_16x16x64_i8 v[70:73], v[138:141], v[182:185], v[70:73]
	v_mfma_i32_16x16x64_i8 v[78:81], v[134:137], v[178:181], v[78:81]
	s_nop 0
	v_mfma_i32_16x16x64_i8 v[78:81], v[130:133], v[182:185], v[78:81]
	v_mfma_i32_16x16x64_i8 v[90:93], v[158:161], v[186:189], v[90:93]
	s_nop 0
	v_mfma_i32_16x16x64_i8 v[90:93], v[154:157], v[190:193], v[90:93]
	v_mfma_i32_16x16x64_i8 v[106:109], v[150:153], v[186:189], v[106:109]
	s_nop 0
	v_mfma_i32_16x16x64_i8 v[106:109], v[146:149], v[190:193], v[106:109]
	v_mfma_i32_16x16x64_i8 v[102:105], v[142:145], v[186:189], v[102:105]
	s_nop 0
	v_mfma_i32_16x16x64_i8 v[102:105], v[138:141], v[190:193], v[102:105]
	v_mfma_i32_16x16x64_i8 v[110:113], v[134:137], v[186:189], v[110:113]
	s_nop 0
	v_mfma_i32_16x16x64_i8 v[110:113], v[130:133], v[190:193], v[110:113]
	s_setprio 0
	s_barrier
	s_add_i32 s41, s41, 2
	s_add_u32 s48, s48, 0x100
	s_addc_u32 s49, s49, 0
	s_cmp_gt_u32 s41, 13
	s_cbranch_scc1 .LBB0_1098
	s_mov_b64 s[52:53], s[14:15]
	s_mov_b64 s[50:51], s[26:27]
	.p2align	6

.LBB0_1298:
	s_waitcnt vmcnt(8)
	s_waitcnt lgkmcnt(0)
	s_barrier
	s_setprio 1
	v_mfma_i32_16x16x64_i8 v[18:21], v[158:161], v[190:193], 0
	s_nop 0
	v_mfma_i32_16x16x64_i8 v[18:21], v[154:157], v[186:189], v[18:21]
	v_mfma_i32_16x16x64_i8 v[22:25], v[150:153], v[190:193], 0
	s_nop 0
	v_mfma_i32_16x16x64_i8 v[22:25], v[142:145], v[186:189], v[22:25]
	v_mfma_i32_16x16x64_i8 v[26:29], v[146:149], v[190:193], 0
	s_nop 0
	v_mfma_i32_16x16x64_i8 v[26:29], v[138:141], v[186:189], v[26:29]
	v_mfma_i32_16x16x64_i8 v[34:37], v[134:137], v[190:193], 0
	s_nop 0
	v_mfma_i32_16x16x64_i8 v[34:37], v[130:133], v[186:189], v[34:37]
	v_mfma_i32_16x16x64_i8 v[50:53], v[158:161], v[182:185], 0
	s_nop 0
	v_mfma_i32_16x16x64_i8 v[50:53], v[154:157], v[178:181], v[50:53]
	v_mfma_i32_16x16x64_i8 v[62:65], v[150:153], v[182:185], 0
	s_nop 0
	v_mfma_i32_16x16x64_i8 v[62:65], v[142:145], v[178:181], v[62:65]
	v_mfma_i32_16x16x64_i8 v[54:57], v[146:149], v[182:185], 0
	s_nop 0
	v_mfma_i32_16x16x64_i8 v[54:57], v[138:141], v[178:181], v[54:57]
	v_mfma_i32_16x16x64_i8 v[66:69], v[134:137], v[182:185], 0
	s_nop 0
	v_mfma_i32_16x16x64_i8 v[66:69], v[130:133], v[178:181], v[66:69]
	v_mfma_i32_16x16x64_i8 v[82:85], v[158:161], v[174:177], 0
	s_nop 0
	v_mfma_i32_16x16x64_i8 v[82:85], v[154:157], v[170:173], v[82:85]
	v_mfma_i32_16x16x64_i8 v[94:97], v[150:153], v[174:177], 0
	s_nop 0
	v_mfma_i32_16x16x64_i8 v[94:97], v[142:145], v[170:173], v[94:97]
	v_mfma_i32_16x16x64_i8 v[86:89], v[146:149], v[174:177], 0
	s_nop 0
	v_mfma_i32_16x16x64_i8 v[86:89], v[138:141], v[170:173], v[86:89]
	v_mfma_i32_16x16x64_i8 v[98:101], v[134:137], v[174:177], 0
	s_nop 0
	v_mfma_i32_16x16x64_i8 v[98:101], v[130:133], v[170:173], v[98:101]
	v_mfma_i32_16x16x64_i8 v[114:117], v[158:161], v[166:169], 0
	s_nop 0
	v_mfma_i32_16x16x64_i8 v[114:117], v[154:157], v[162:165], v[114:117]
	v_mfma_i32_16x16x64_i8 v[122:125], v[150:153], v[166:169], 0
	s_nop 0
	v_mfma_i32_16x16x64_i8 v[122:125], v[142:145], v[162:165], v[122:125]
	v_mfma_i32_16x16x64_i8 v[118:121], v[146:149], v[166:169], 0
	s_nop 0
	v_mfma_i32_16x16x64_i8 v[118:121], v[138:141], v[162:165], v[118:121]
	v_mfma_i32_16x16x64_i8 v[126:129], v[134:137], v[166:169], 0
	s_nop 0
	v_mfma_i32_16x16x64_i8 v[126:129], v[130:133], v[162:165], v[126:129]
	s_setprio 0
	s_barrier
	s_add_u32 s81, s77, s48
	s_addc_u32 s82, s78, s49
	s_cmp_eq_u32 s41, 12
	s_cselect_b64 s[66:67], -1, 0
	s_and_b64 s[74:75], s[66:67], exec
	s_cselect_b32 s53, s53, s82
	s_cselect_b32 s52, s52, s81
	s_mov_b64 s[74:75], s[52:53]
	v_mov_b32_e32 v203, v196
	s_mov_b32 m0, s33
	s_waitcnt lgkmcnt(0)
	ds_read_b128 v[190:193], v202 offset:16384
	ds_read_b128 v[186:189], v202 offset:17408
	ds_read_b128 v[182:185], v202 offset:18432
	ds_read_b128 v[178:181], v202 offset:19456
	ds_read_b128 v[174:177], v202 offset:20480
	ds_read_b128 v[170:173], v202 offset:21504
	ds_read_b128 v[166:169], v202 offset:22528
	ds_read_b128 v[162:165], v202 offset:23552
	s_nop 0
	global_load_lds_dwordx4 v203, s[74:75]
	v_mov_b32_e32 v203, v197
	s_mov_b32 m0, s35
	s_nop 0
	global_load_lds_dwordx4 v203, s[74:75]
	s_add_u32 s74, s52, 0x40000
	s_addc_u32 s75, s53, 0
	v_mov_b32_e32 v203, v196
	s_mov_b32 m0, s60
	s_nop 0
	global_load_lds_dwordx4 v203, s[74:75]
	v_mov_b32_e32 v203, v197
	s_mov_b32 m0, s61
	s_nop 0
	global_load_lds_dwordx4 v203, s[74:75]
	s_waitcnt vmcnt(6)
	s_waitcnt lgkmcnt(0)
	s_barrier
	s_setprio 1
	v_mfma_i32_16x16x64_i8 v[2:5], v[158:161], v[190:193], 0
	s_nop 0
	v_mfma_i32_16x16x64_i8 v[2:5], v[154:157], v[186:189], v[2:5]
	v_mfma_i32_16x16x64_i8 v[6:9], v[150:153], v[190:193], 0
	s_nop 0
	v_mfma_i32_16x16x64_i8 v[6:9], v[142:145], v[186:189], v[6:9]
	v_mfma_i32_16x16x64_i8 v[10:13], v[146:149], v[190:193], 0
	s_nop 0
	v_mfma_i32_16x16x64_i8 v[10:13], v[138:141], v[186:189], v[10:13]
	v_mfma_i32_16x16x64_i8 v[14:17], v[134:137], v[190:193], 0
	s_nop 0
	v_mfma_i32_16x16x64_i8 v[14:17], v[130:133], v[186:189], v[14:17]
	v_mfma_i32_16x16x64_i8 v[30:33], v[158:161], v[182:185], 0
	s_nop 0
	v_mfma_i32_16x16x64_i8 v[30:33], v[154:157], v[178:181], v[30:33]
	v_mfma_i32_16x16x64_i8 v[42:45], v[150:153], v[182:185], 0
	s_nop 0
	v_mfma_i32_16x16x64_i8 v[42:45], v[142:145], v[178:181], v[42:45]
	v_mfma_i32_16x16x64_i8 v[38:41], v[146:149], v[182:185], 0
	s_nop 0
	v_mfma_i32_16x16x64_i8 v[38:41], v[138:141], v[178:181], v[38:41]
	v_mfma_i32_16x16x64_i8 v[46:49], v[134:137], v[182:185], 0
	s_nop 0
	v_mfma_i32_16x16x64_i8 v[46:49], v[130:133], v[178:181], v[46:49]
	v_mfma_i32_16x16x64_i8 v[58:61], v[158:161], v[174:177], 0
	s_nop 0
	v_mfma_i32_16x16x64_i8 v[58:61], v[154:157], v[170:173], v[58:61]
	v_mfma_i32_16x16x64_i8 v[74:77], v[150:153], v[174:177], 0
	s_nop 0
	v_mfma_i32_16x16x64_i8 v[74:77], v[142:145], v[170:173], v[74:77]
	v_mfma_i32_16x16x64_i8 v[70:73], v[146:149], v[174:177], 0
	s_nop 0
	v_mfma_i32_16x16x64_i8 v[70:73], v[138:141], v[170:173], v[70:73]
	v_mfma_i32_16x16x64_i8 v[78:81], v[134:137], v[174:177], 0
	s_nop 0
	v_mfma_i32_16x16x64_i8 v[78:81], v[130:133], v[170:173], v[78:81]
	v_mfma_i32_16x16x64_i8 v[90:93], v[158:161], v[166:169], 0
	s_nop 0
	v_mfma_i32_16x16x64_i8 v[90:93], v[154:157], v[162:165], v[90:93]
	v_mfma_i32_16x16x64_i8 v[106:109], v[150:153], v[166:169], 0
	s_nop 0
	v_mfma_i32_16x16x64_i8 v[106:109], v[142:145], v[162:165], v[106:109]
	v_mfma_i32_16x16x64_i8 v[102:105], v[146:149], v[166:169], 0
	s_nop 0
	v_mfma_i32_16x16x64_i8 v[102:105], v[138:141], v[162:165], v[102:105]
	v_mfma_i32_16x16x64_i8 v[110:113], v[134:137], v[166:169], 0
	s_nop 0
	v_mfma_i32_16x16x64_i8 v[110:113], v[130:133], v[162:165], v[110:113]
	s_setprio 0
	s_barrier
	s_add_u32 s43, s43, 0x100
	s_addc_u32 s74, s80, 0
	s_and_b64 s[64:65], s[66:67], exec
	s_cselect_b32 s65, s51, s74
	s_cselect_b32 s64, s50, s43
	s_add_u32 s50, s52, 0x80
	s_addc_u32 s51, s53, 0
	s_add_i32 s43, 0, 0x18000
	s_add_i32 s74, 0, 0x1c000
	v_add_u32_e32 v130, s43, v199
	v_add_u32_e32 v131, s74, v199
	ds_read_b128 v[158:161], v130
	ds_read_b128 v[154:157], v130 offset:1024
	ds_read_b128 v[150:153], v130 offset:2048
	ds_read_b128 v[146:149], v130 offset:3072
	ds_read_b128 v[142:145], v131
	ds_read_b128 v[138:141], v131 offset:1024
	ds_read_b128 v[134:137], v131 offset:2048
	ds_read_b128 v[130:133], v131 offset:3072
	s_mov_b64 s[66:67], s[64:65]
	v_mov_b32_e32 v203, v196
	s_mov_b32 m0, s5
	s_waitcnt lgkmcnt(0)
	ds_read_b128 v[162:165], v202 offset:32768
	ds_read_b128 v[166:169], v202 offset:33792
	ds_read_b128 v[170:173], v202 offset:34816
	ds_read_b128 v[174:177], v202 offset:35840
	ds_read_b128 v[178:181], v202 offset:36864
	ds_read_b128 v[182:185], v202 offset:37888
	ds_read_b128 v[186:189], v202 offset:38912
	ds_read_b128 v[190:193], v202 offset:39936
	s_add_u32 s64, s64, 0x40000
	global_load_lds_dwordx4 v203, s[66:67]
	v_mov_b32_e32 v203, v197
	s_mov_b32 m0, s62
	s_addc_u32 s65, s65, 0
	global_load_lds_dwordx4 v203, s[66:67]
	v_mov_b32_e32 v203, v196
	s_mov_b32 m0, s63
	s_nop 0
	global_load_lds_dwordx4 v203, s[64:65]
	v_mov_b32_e32 v203, v197
	s_mov_b32 m0, s69
	s_nop 0
	global_load_lds_dwordx4 v203, s[64:65]
	s_waitcnt vmcnt(8)
	s_waitcnt lgkmcnt(0)
	s_barrier
	s_setprio 1
	s_waitcnt lgkmcnt(0)
	v_mfma_i32_16x16x64_i8 v[18:21], v[158:161], v[162:165], v[18:21]
	s_nop 0
	v_mfma_i32_16x16x64_i8 v[18:21], v[154:157], v[166:169], v[18:21]
	v_mfma_i32_16x16x64_i8 v[22:25], v[150:153], v[162:165], v[22:25]
	s_nop 0
	v_mfma_i32_16x16x64_i8 v[22:25], v[146:149], v[166:169], v[22:25]
	v_mfma_i32_16x16x64_i8 v[26:29], v[142:145], v[162:165], v[26:29]
	s_nop 0
	v_mfma_i32_16x16x64_i8 v[26:29], v[138:141], v[166:169], v[26:29]
	v_mfma_i32_16x16x64_i8 v[34:37], v[134:137], v[162:165], v[34:37]
	s_nop 0
	v_mfma_i32_16x16x64_i8 v[34:37], v[130:133], v[166:169], v[34:37]
	v_mfma_i32_16x16x64_i8 v[50:53], v[158:161], v[170:173], v[50:53]
	s_nop 0
	v_mfma_i32_16x16x64_i8 v[50:53], v[154:157], v[174:177], v[50:53]
	v_mfma_i32_16x16x64_i8 v[62:65], v[150:153], v[170:173], v[62:65]
	s_nop 0
	v_mfma_i32_16x16x64_i8 v[62:65], v[146:149], v[174:177], v[62:65]
	v_mfma_i32_16x16x64_i8 v[54:57], v[142:145], v[170:173], v[54:57]
	s_nop 0
	v_mfma_i32_16x16x64_i8 v[54:57], v[138:141], v[174:177], v[54:57]
	v_mfma_i32_16x16x64_i8 v[66:69], v[134:137], v[170:173], v[66:69]
	s_nop 0
	v_mfma_i32_16x16x64_i8 v[66:69], v[130:133], v[174:177], v[66:69]
	v_mfma_i32_16x16x64_i8 v[82:85], v[158:161], v[178:181], v[82:85]
	s_nop 0
	v_mfma_i32_16x16x64_i8 v[82:85], v[154:157], v[182:185], v[82:85]
	v_mfma_i32_16x16x64_i8 v[94:97], v[150:153], v[178:181], v[94:97]
	s_nop 0
	v_mfma_i32_16x16x64_i8 v[94:97], v[146:149], v[182:185], v[94:97]
	v_mfma_i32_16x16x64_i8 v[86:89], v[142:145], v[178:181], v[86:89]
	s_nop 0
	v_mfma_i32_16x16x64_i8 v[86:89], v[138:141], v[182:185], v[86:89]
	v_mfma_i32_16x16x64_i8 v[98:101], v[134:137], v[178:181], v[98:101]
	s_nop 0
	v_mfma_i32_16x16x64_i8 v[98:101], v[130:133], v[182:185], v[98:101]
	v_mfma_i32_16x16x64_i8 v[114:117], v[158:161], v[186:189], v[114:117]
	s_nop 0
	v_mfma_i32_16x16x64_i8 v[114:117], v[154:157], v[190:193], v[114:117]
	v_mfma_i32_16x16x64_i8 v[122:125], v[150:153], v[186:189], v[122:125]
	s_nop 0
	v_mfma_i32_16x16x64_i8 v[122:125], v[146:149], v[190:193], v[122:125]
	v_mfma_i32_16x16x64_i8 v[118:121], v[142:145], v[186:189], v[118:121]
	s_nop 0
	v_mfma_i32_16x16x64_i8 v[118:121], v[138:141], v[190:193], v[118:121]
	v_mfma_i32_16x16x64_i8 v[126:129], v[134:137], v[186:189], v[126:129]
	s_nop 0
	v_mfma_i32_16x16x64_i8 v[126:129], v[130:133], v[190:193], v[126:129]
	s_setprio 0
	s_barrier
	v_mov_b32_e32 v203, v196
	s_add_i32 s43, s43, s10
	ds_read_b128 v[162:165], v202 offset:49152
	ds_read_b128 v[166:169], v202 offset:50176
	ds_read_b128 v[170:173], v202 offset:51200
	ds_read_b128 v[174:177], v202 offset:52224
	ds_read_b128 v[178:181], v202 offset:53248
	ds_read_b128 v[182:185], v202 offset:54272
	ds_read_b128 v[186:189], v202 offset:55296
	ds_read_b128 v[190:193], v202 offset:56320
	s_mov_b32 m0, s43
	s_nop 0
	global_load_lds_dwordx4 v203, s[50:51]
	v_mov_b32_e32 v203, v197
	s_add_i32 m0, s43, 0x2000
	s_nop 0
	global_load_lds_dwordx4 v203, s[50:51]
	s_add_u32 s50, s52, 0x40080
	s_addc_u32 s51, s53, 0
	v_mov_b32_e32 v203, v196
	s_add_i32 s43, s74, s10
	s_mov_b32 m0, s43
	s_nop 0
	global_load_lds_dwordx4 v203, s[50:51]
	v_mov_b32_e32 v203, v197
	s_add_i32 m0, s43, 0x2000
	s_nop 0
	global_load_lds_dwordx4 v203, s[50:51]
	s_waitcnt vmcnt(6)
	s_waitcnt lgkmcnt(0)
	s_barrier
	s_setprio 1
	s_waitcnt lgkmcnt(0)
	v_mfma_i32_16x16x64_i8 v[2:5], v[158:161], v[162:165], v[2:5]
	s_nop 0
	v_mfma_i32_16x16x64_i8 v[2:5], v[154:157], v[166:169], v[2:5]
	v_mfma_i32_16x16x64_i8 v[6:9], v[150:153], v[162:165], v[6:9]
	s_nop 0
	v_mfma_i32_16x16x64_i8 v[6:9], v[146:149], v[166:169], v[6:9]
	v_mfma_i32_16x16x64_i8 v[10:13], v[142:145], v[162:165], v[10:13]
	s_nop 0
	v_mfma_i32_16x16x64_i8 v[10:13], v[138:141], v[166:169], v[10:13]
	v_mfma_i32_16x16x64_i8 v[14:17], v[134:137], v[162:165], v[14:17]
	s_nop 0
	v_mfma_i32_16x16x64_i8 v[14:17], v[130:133], v[166:169], v[14:17]
	v_mfma_i32_16x16x64_i8 v[30:33], v[158:161], v[170:173], v[30:33]
	s_nop 0
	v_mfma_i32_16x16x64_i8 v[30:33], v[154:157], v[174:177], v[30:33]
	v_mfma_i32_16x16x64_i8 v[42:45], v[150:153], v[170:173], v[42:45]
	s_nop 0
	v_mfma_i32_16x16x64_i8 v[42:45], v[146:149], v[174:177], v[42:45]
	v_mfma_i32_16x16x64_i8 v[38:41], v[142:145], v[170:173], v[38:41]
	s_nop 0
	v_mfma_i32_16x16x64_i8 v[38:41], v[138:141], v[174:177], v[38:41]
	v_mfma_i32_16x16x64_i8 v[46:49], v[134:137], v[170:173], v[46:49]
	s_nop 0
	v_mfma_i32_16x16x64_i8 v[46:49], v[130:133], v[174:177], v[46:49]
	v_mfma_i32_16x16x64_i8 v[58:61], v[158:161], v[178:181], v[58:61]
	s_nop 0
	v_mfma_i32_16x16x64_i8 v[58:61], v[154:157], v[182:185], v[58:61]
	v_mfma_i32_16x16x64_i8 v[74:77], v[150:153], v[178:181], v[74:77]
	s_nop 0
	v_mfma_i32_16x16x64_i8 v[74:77], v[146:149], v[182:185], v[74:77]
	v_mfma_i32_16x16x64_i8 v[70:73], v[142:145], v[178:181], v[70:73]
	s_nop 0
	v_mfma_i32_16x16x64_i8 v[70:73], v[138:141], v[182:185], v[70:73]
	v_mfma_i32_16x16x64_i8 v[78:81], v[134:137], v[178:181], v[78:81]
	s_nop 0
	v_mfma_i32_16x16x64_i8 v[78:81], v[130:133], v[182:185], v[78:81]
	v_mfma_i32_16x16x64_i8 v[90:93], v[158:161], v[186:189], v[90:93]
	s_nop 0
	v_mfma_i32_16x16x64_i8 v[90:93], v[154:157], v[190:193], v[90:93]
	v_mfma_i32_16x16x64_i8 v[106:109], v[150:153], v[186:189], v[106:109]
	s_nop 0
	v_mfma_i32_16x16x64_i8 v[106:109], v[146:149], v[190:193], v[106:109]
	v_mfma_i32_16x16x64_i8 v[102:105], v[142:145], v[186:189], v[102:105]
	s_nop 0
	v_mfma_i32_16x16x64_i8 v[102:105], v[138:141], v[190:193], v[102:105]
	v_mfma_i32_16x16x64_i8 v[110:113], v[134:137], v[186:189], v[110:113]
	s_nop 0
	v_mfma_i32_16x16x64_i8 v[110:113], v[130:133], v[190:193], v[110:113]
	s_setprio 0
	s_barrier
	s_add_i32 s41, s41, 2
	s_add_u32 s48, s48, 0x100
	s_addc_u32 s49, s49, 0
	s_cmp_gt_u32 s41, 13
	s_cbranch_scc1 .LBB0_1308
	s_mov_b64 s[52:53], s[14:15]
	s_mov_b64 s[50:51], s[18:19]
	.p2align	6

.LBB0_1520:
	s_and_b32 s7, s3, 3
	s_lshl_b32 s8, s1, 13
	s_lshl_b32 s16, s3, 5
	s_lshl_b32 s1, s7, 12
	s_ashr_i32 s62, s13, 31
	s_add_u32 s14, s42, 0x80
	s_addc_u32 s15, s43, 0
	v_mov_b32_e32 v3, v167
	s_waitcnt vmcnt(2)
	s_barrier
	s_add_i32 m0, s33, 0x18000
	s_sext_i32_i16 s31, s2
	global_load_lds_dwordx4 v3, s[14:15]
	v_mov_b32_e32 v3, v169
	s_add_i32 m0, s33, 0x1a000
	v_and_b32_e32 v5, 32, v200
	global_load_lds_dwordx4 v3, s[14:15]
	s_add_u32 s14, s42, 0x40080
	s_addc_u32 s15, s43, 0
	v_mov_b32_e32 v3, v167
	s_add_i32 m0, s33, 0x1c000
	s_mul_i32 s63, s9, 7
	global_load_lds_dwordx4 v3, s[14:15]
	v_mov_b32_e32 v3, v169
	s_add_i32 m0, s33, 0x1e000
	s_cmpk_lt_u32 s6, 0x100
	global_load_lds_dwordx4 v3, s[14:15]
	v_lshlrev_b32_e32 v3, 6, v0
	v_and_b32_e32 v3, 0x3c0, v3
	v_lshl_or_b32 v4, v2, 1, v3
	s_cselect_b64 s[6:7], -1, 0
	v_and_or_b32 v3, s16, 32, v3
	s_lshl_b32 s2, s3, 9
	s_and_b32 s2, s2, 0x400
	v_bitop3_b32 v2, v3, v5, v2 bitop3:0x36
	v_or_b32_e32 v2, s2, v2
	v_bitop3_b32 v170, s1, v4, v5 bitop3:0xf6
	s_waitcnt vmcnt(6)
	v_or_b32_e32 v2, s8, v2
	v_mov_b32_e32 v3, 0
	v_bitop3_b32 v6, s8, v4, v5 bitop3:0xf6
	s_mov_b32 s1, 0
	v_lshl_add_u64 v[162:163], s[36:37], 0, v[2:3]
	v_add_u32_e32 v2, 0, v170
	v_add_u32_e32 v171, 0x10000, v2
	v_add_u32_e32 v172, 0x14000, v2
	v_add_u32_e32 v173, 0, v6
	s_add_i32 s64, s33, 0x8000
	s_add_i32 s65, s33, 0xa000
	s_add_i32 s66, s33, 0xc000
	s_add_i32 s67, s33, 0xe000
	v_mov_b64_e32 v[164:165], s[0:1]
	s_mov_b32 s0, 0xbc38aa3b
	s_mov_b32 s8, 0x46800000
	s_mov_b32 s69, 0xc3e00000
	s_movk_i32 s70, 0x1000
	v_mov_b32_e32 v174, 0x43e00000
	s_mov_b64 s[18:19], s[40:41]
	s_mov_b64 s[24:25], s[42:43]
	s_barrier
	s_waitcnt vmcnt(0)
	s_branch .LBB0_1523
	.p2align	6
.LBB0_1521:
	s_mov_b64 s[2:3], 0
	.p2align	6

.LBB0_1525:
	s_add_u32 s46, s40, 0x100
	s_addc_u32 s47, s41, 0
	s_add_u32 s48, s42, 0x100
	s_waitcnt vmcnt(8)
	s_addc_u32 s49, s43, 0
	s_waitcnt lgkmcnt(0)
	s_add_u32 s44, s42, 0x180
	s_addc_u32 s45, s43, 0
	s_barrier
	s_setprio 1
	s_waitcnt lgkmcnt(0)
	v_mfma_f32_16x16x128_f8f6f4 v[154:157], v[2:9], v[58:65], 0
	v_mfma_f32_16x16x128_f8f6f4 v[146:149], v[10:17], v[58:65], 0
	v_mfma_f32_16x16x128_f8f6f4 v[158:161], v[18:25], v[58:65], 0
	v_mfma_f32_16x16x128_f8f6f4 v[150:153], v[26:33], v[58:65], 0
	v_mfma_f32_16x16x128_f8f6f4 v[134:137], v[26:33], v[50:57], 0
	v_mfma_f32_16x16x128_f8f6f4 v[142:145], v[18:25], v[50:57], 0
	v_mfma_f32_16x16x128_f8f6f4 v[130:133], v[10:17], v[50:57], 0
	v_mfma_f32_16x16x128_f8f6f4 v[138:141], v[2:9], v[50:57], 0
	v_mfma_f32_16x16x128_f8f6f4 v[122:125], v[2:9], v[42:49], 0
	v_mfma_f32_16x16x128_f8f6f4 v[114:117], v[10:17], v[42:49], 0
	v_mfma_f32_16x16x128_f8f6f4 v[126:129], v[18:25], v[42:49], 0
	v_mfma_f32_16x16x128_f8f6f4 v[118:121], v[26:33], v[42:49], 0
	v_mfma_f32_16x16x128_f8f6f4 v[102:105], v[26:33], v[34:41], 0
	v_mfma_f32_16x16x128_f8f6f4 v[110:113], v[18:25], v[34:41], 0
	v_mfma_f32_16x16x128_f8f6f4 v[98:101], v[10:17], v[34:41], 0
	v_mfma_f32_16x16x128_f8f6f4 v[106:109], v[2:9], v[34:41], 0
	s_setprio 0
	s_barrier
	v_mov_b32_e32 v50, v167
	s_mov_b32 m0, s35
	ds_read_b128 v[34:37], v173 offset:16384
	ds_read_b128 v[38:41], v173 offset:17408
	ds_read_b128 v[42:45], v173 offset:18432
	ds_read_b128 v[46:49], v173 offset:19456
	ds_read_b128 v[176:179], v173 offset:20480
	ds_read_b128 v[180:183], v173 offset:21504
	ds_read_b128 v[184:187], v173 offset:22528
	ds_read_b128 v[188:191], v173 offset:23552
	s_nop 0
	global_load_lds_dwordx4 v50, s[48:49]
	v_mov_b32_e32 v50, v169
	s_mov_b32 m0, s50
	s_nop 0
	global_load_lds_dwordx4 v50, s[48:49]
	s_add_u32 s48, s42, 0x40100
	s_addc_u32 s49, s43, 0
	v_mov_b32_e32 v50, v167
	s_mov_b32 m0, s51
	s_nop 0
	global_load_lds_dwordx4 v50, s[48:49]
	v_mov_b32_e32 v50, v169
	s_mov_b32 m0, s52
	s_nop 0
	global_load_lds_dwordx4 v50, s[48:49]
	s_waitcnt vmcnt(6)
	s_waitcnt lgkmcnt(0)
	s_barrier
	s_setprio 1
	s_waitcnt lgkmcnt(0)
	v_mfma_f32_16x16x128_f8f6f4 v[90:93], v[2:9], v[34:41], 0
	v_mfma_f32_16x16x128_f8f6f4 v[82:85], v[10:17], v[34:41], 0
	v_mfma_f32_16x16x128_f8f6f4 v[94:97], v[18:25], v[34:41], 0
	v_mfma_f32_16x16x128_f8f6f4 v[86:89], v[26:33], v[34:41], 0
	v_mfma_f32_16x16x128_f8f6f4 v[70:73], v[26:33], v[42:49], 0
	v_mfma_f32_16x16x128_f8f6f4 v[78:81], v[18:25], v[42:49], 0
	v_mfma_f32_16x16x128_f8f6f4 v[66:69], v[10:17], v[42:49], 0
	v_mfma_f32_16x16x128_f8f6f4 v[74:77], v[2:9], v[42:49], 0
	v_mfma_f32_16x16x128_f8f6f4 v[58:61], v[2:9], v[176:183], 0
	v_mfma_f32_16x16x128_f8f6f4 v[50:53], v[10:17], v[176:183], 0
	v_mfma_f32_16x16x128_f8f6f4 v[62:65], v[18:25], v[176:183], 0
	v_mfma_f32_16x16x128_f8f6f4 v[54:57], v[26:33], v[176:183], 0
	v_mfma_f32_16x16x128_f8f6f4 v[38:41], v[26:33], v[184:191], 0
	v_mfma_f32_16x16x128_f8f6f4 v[46:49], v[18:25], v[184:191], 0
	v_mfma_f32_16x16x128_f8f6f4 v[34:37], v[10:17], v[184:191], 0
	v_mfma_f32_16x16x128_f8f6f4 v[42:45], v[2:9], v[184:191], 0
	s_setprio 0
	s_barrier
	s_add_i32 s15, 0, 0x18000
	s_add_i32 s48, 0, 0x1c000
	v_add_u32_e32 v175, s15, v170
	v_add_u32_e32 v176, s48, v170
	ds_read_b128 v[26:29], v175
	ds_read_b128 v[30:33], v175 offset:1024
	ds_read_b128 v[18:21], v175 offset:2048
	ds_read_b128 v[22:25], v175 offset:3072
	ds_read_b128 v[10:13], v176
	ds_read_b128 v[14:17], v176 offset:1024
	ds_read_b128 v[2:5], v176 offset:2048
	ds_read_b128 v[6:9], v176 offset:3072
	v_mov_b32_e32 v177, v166
	s_mov_b32 m0, s33
	ds_read_b128 v[178:181], v173 offset:32768
	ds_read_b128 v[182:185], v173 offset:33792
	ds_read_b128 v[186:189], v173 offset:34816
	ds_read_b128 v[190:193], v173 offset:35840
	ds_read_b128 v[202:205], v173 offset:36864
	ds_read_b128 v[206:209], v173 offset:37888
	ds_read_b128 v[210:213], v173 offset:38912
	ds_read_b128 v[214:217], v173 offset:39936
	s_nop 0
	global_load_lds_dwordx4 v177, s[46:47]
	v_mov_b32_e32 v177, v168
	s_mov_b32 m0, s53
	s_nop 0
	global_load_lds_dwordx4 v177, s[46:47]
	s_add_u32 s46, s40, 0x40100
	s_addc_u32 s47, s41, 0
	v_mov_b32_e32 v177, v166
	s_mov_b32 m0, s60
	s_nop 0
	global_load_lds_dwordx4 v177, s[46:47]
	v_mov_b32_e32 v177, v168
	s_mov_b32 m0, s61
	s_nop 0
	global_load_lds_dwordx4 v177, s[46:47]
	s_waitcnt vmcnt(8)
	s_waitcnt lgkmcnt(0)
	s_barrier
	s_setprio 1
	s_waitcnt lgkmcnt(0)
	v_mfma_f32_16x16x128_f8f6f4 v[154:157], v[26:33], v[178:185], v[154:157]
	v_mfma_f32_16x16x128_f8f6f4 v[146:149], v[18:25], v[178:185], v[146:149]
	v_mfma_f32_16x16x128_f8f6f4 v[158:161], v[10:17], v[178:185], v[158:161]
	v_mfma_f32_16x16x128_f8f6f4 v[150:153], v[2:9], v[178:185], v[150:153]
	v_mfma_f32_16x16x128_f8f6f4 v[134:137], v[2:9], v[186:193], v[134:137]
	v_mfma_f32_16x16x128_f8f6f4 v[142:145], v[10:17], v[186:193], v[142:145]
	v_mfma_f32_16x16x128_f8f6f4 v[130:133], v[18:25], v[186:193], v[130:133]
	v_mfma_f32_16x16x128_f8f6f4 v[138:141], v[26:33], v[186:193], v[138:141]
	v_mfma_f32_16x16x128_f8f6f4 v[122:125], v[26:33], v[202:209], v[122:125]
	v_mfma_f32_16x16x128_f8f6f4 v[114:117], v[18:25], v[202:209], v[114:117]
	v_mfma_f32_16x16x128_f8f6f4 v[126:129], v[10:17], v[202:209], v[126:129]
	v_mfma_f32_16x16x128_f8f6f4 v[118:121], v[2:9], v[202:209], v[118:121]
	v_mfma_f32_16x16x128_f8f6f4 v[102:105], v[2:9], v[210:217], v[102:105]
	v_mfma_f32_16x16x128_f8f6f4 v[110:113], v[10:17], v[210:217], v[110:113]
	v_mfma_f32_16x16x128_f8f6f4 v[98:101], v[18:25], v[210:217], v[98:101]
	v_mfma_f32_16x16x128_f8f6f4 v[106:109], v[26:33], v[210:217], v[106:109]
	s_setprio 0
	s_barrier
	v_mov_b32_e32 v177, v167
	s_add_i32 s15, s15, s10
	ds_read_b128 v[178:181], v173 offset:49152
	ds_read_b128 v[182:185], v173 offset:50176
	ds_read_b128 v[186:189], v173 offset:51200
	ds_read_b128 v[190:193], v173 offset:52224
	ds_read_b128 v[202:205], v173 offset:53248
	ds_read_b128 v[206:209], v173 offset:54272
	ds_read_b128 v[210:213], v173 offset:55296
	ds_read_b128 v[214:217], v173 offset:56320
	s_mov_b32 m0, s15
	s_add_i32 s17, s15, 0x2000
	global_load_lds_dwordx4 v177, s[44:45]
	v_mov_b32_e32 v177, v169
	s_mov_b32 m0, s17
	s_nop 0
	global_load_lds_dwordx4 v177, s[44:45]
	s_add_u32 s44, s42, 0x40180
	s_addc_u32 s45, s43, 0
	v_mov_b32_e32 v177, v167
	s_add_i32 s48, s48, s10
	s_mov_b32 m0, s48
	s_add_i32 s49, s48, 0x2000
	global_load_lds_dwordx4 v177, s[44:45]
	v_mov_b32_e32 v177, v169
	s_mov_b32 m0, s49
	s_nop 0
	global_load_lds_dwordx4 v177, s[44:45]
	s_waitcnt vmcnt(6)
	s_waitcnt lgkmcnt(0)
	s_barrier
	s_setprio 1
	s_waitcnt lgkmcnt(0)
	v_mfma_f32_16x16x128_f8f6f4 v[90:93], v[26:33], v[178:185], v[90:93]
	v_mfma_f32_16x16x128_f8f6f4 v[82:85], v[18:25], v[178:185], v[82:85]
	v_mfma_f32_16x16x128_f8f6f4 v[94:97], v[10:17], v[178:185], v[94:97]
	v_mfma_f32_16x16x128_f8f6f4 v[86:89], v[2:9], v[178:185], v[86:89]
	v_mfma_f32_16x16x128_f8f6f4 v[70:73], v[2:9], v[186:193], v[70:73]
	v_mfma_f32_16x16x128_f8f6f4 v[78:81], v[10:17], v[186:193], v[78:81]
	v_mfma_f32_16x16x128_f8f6f4 v[66:69], v[18:25], v[186:193], v[66:69]
	v_mfma_f32_16x16x128_f8f6f4 v[74:77], v[26:33], v[186:193], v[74:77]
	v_mfma_f32_16x16x128_f8f6f4 v[58:61], v[26:33], v[202:209], v[58:61]
	v_mfma_f32_16x16x128_f8f6f4 v[50:53], v[18:25], v[202:209], v[50:53]
	v_mfma_f32_16x16x128_f8f6f4 v[62:65], v[10:17], v[202:209], v[62:65]
	v_mfma_f32_16x16x128_f8f6f4 v[54:57], v[2:9], v[202:209], v[54:57]
	v_mfma_f32_16x16x128_f8f6f4 v[38:41], v[2:9], v[210:217], v[38:41]
	v_mfma_f32_16x16x128_f8f6f4 v[46:49], v[10:17], v[210:217], v[46:49]
	v_mfma_f32_16x16x128_f8f6f4 v[34:37], v[18:25], v[210:217], v[34:37]
	v_mfma_f32_16x16x128_f8f6f4 v[42:45], v[26:33], v[210:217], v[42:45]
	s_setprio 0
	s_barrier
	s_add_u32 s44, s40, 0x100
	s_addc_u32 s45, s41, 0
	s_add_u32 s71, s42, 0x200
	s_addc_u32 s72, s43, 0
	s_mov_b32 s73, 0
	.p2align	6

.LBB0_1593:
	s_lshl_b32 s8, s8, 5
	s_lshl_b32 s14, s5, 13
	s_and_b32 s15, s8, 0x60
	s_ashr_i32 s63, s13, 31
	s_add_u32 s8, s40, 0x4000
	s_addc_u32 s9, s41, 0
	v_mov_b32_e32 v2, v180
	s_waitcnt vmcnt(2)
	s_barrier
	s_add_i32 m0, s49, 0x18000
	v_lshlrev_b32_e32 v3, 2, v165
	global_load_lds_dwordx4 v2, s[8:9]
	v_mov_b32_e32 v2, v181
	s_add_i32 m0, s49, 0x1a000
	v_and_b32_e32 v3, 32, v3
	global_load_lds_dwordx4 v2, s[8:9]
	s_add_u32 s8, s40, 0xe4000
	s_addc_u32 s9, s41, 0
	v_mov_b32_e32 v2, v180
	s_add_i32 m0, s49, 0x1c000
	v_lshl_or_b32 v169, s15, 7, v167
	global_load_lds_dwordx4 v2, s[8:9]
	v_mov_b32_e32 v2, v181
	s_add_i32 m0, s49, 0x1e000
	v_lshl_or_b32 v168, s5, 6, v165
	global_load_lds_dwordx4 v2, s[8:9]
	v_lshl_or_b32 v2, v165, 6, v166
	s_waitcnt vmcnt(6)
	v_bitop3_b32 v2, v2, s14, v3 bitop3:0xde
	s_mov_b32 s5, 0
	s_cmpk_lt_u32 s3, 0x100
	v_add_u32_e32 v3, 0, v169
	s_sext_i32_i8 s75, s2
	s_cselect_b64 s[8:9], -1, 0
	v_or_b32_e32 v170, s15, v164
	v_add_u32_e32 v171, 0x10000, v3
	v_add_u32_e32 v172, 0x14000, v3
	v_add_u32_e32 v173, 0, v2
	s_add_i32 s64, s49, 0x8000
	s_add_i32 s65, s49, 0xa000
	s_add_i32 s66, s49, 0xc000
	s_add_i32 s67, s49, 0xe000
	v_mov_b64_e32 v[162:163], s[4:5]
	s_mov_b64 s[14:15], 0x80000
	s_mov_b32 s4, 0x80000
	s_mov_b64 s[16:17], 0x90000
	s_mov_b32 s69, 0x90000
	s_mov_b64 s[18:19], 0xa0000
	s_mov_b32 s70, 0xa0000
	s_mov_b64 s[24:25], 0xb0000
	s_mov_b32 s71, 0xb0000
	s_mov_b64 s[30:31], s[0:1]
	s_mov_b64 s[38:39], s[40:41]
	s_barrier
	s_branch .LBB0_1596
	.p2align	6
.LBB0_1594:
	s_mov_b64 s[0:1], 0
	.p2align	6

.LBB0_1598:
	s_add_u32 s44, s0, 0x8000
	s_addc_u32 s45, s1, 0
	s_add_u32 s46, s40, 0x8000
	s_waitcnt vmcnt(8)
	s_addc_u32 s47, s41, 0
	s_waitcnt lgkmcnt(0)
	s_add_u32 s42, s40, 0xc000
	s_addc_u32 s43, s41, 0
	s_barrier
	s_setprio 1
	s_waitcnt lgkmcnt(0)
	v_mfma_f32_16x16x128_f8f6f4 v[146:149], v[2:9], v[58:65], 0
	v_mfma_f32_16x16x128_f8f6f4 v[150:153], v[10:17], v[58:65], 0
	v_mfma_f32_16x16x128_f8f6f4 v[154:157], v[18:25], v[58:65], 0
	v_mfma_f32_16x16x128_f8f6f4 v[158:161], v[26:33], v[58:65], 0
	v_mfma_f32_16x16x128_f8f6f4 v[130:133], v[26:33], v[50:57], 0
	v_mfma_f32_16x16x128_f8f6f4 v[134:137], v[18:25], v[50:57], 0
	v_mfma_f32_16x16x128_f8f6f4 v[138:141], v[10:17], v[50:57], 0
	v_mfma_f32_16x16x128_f8f6f4 v[142:145], v[2:9], v[50:57], 0
	v_mfma_f32_16x16x128_f8f6f4 v[126:129], v[2:9], v[42:49], 0
	v_mfma_f32_16x16x128_f8f6f4 v[122:125], v[10:17], v[42:49], 0
	v_mfma_f32_16x16x128_f8f6f4 v[118:121], v[18:25], v[42:49], 0
	v_mfma_f32_16x16x128_f8f6f4 v[114:117], v[26:33], v[42:49], 0
	v_mfma_f32_16x16x128_f8f6f4 v[82:85], v[26:33], v[34:41], 0
	v_mfma_f32_16x16x128_f8f6f4 v[90:93], v[18:25], v[34:41], 0
	v_mfma_f32_16x16x128_f8f6f4 v[106:109], v[10:17], v[34:41], 0
	v_mfma_f32_16x16x128_f8f6f4 v[110:113], v[2:9], v[34:41], 0
	s_setprio 0
	s_barrier
	v_mov_b32_e32 v50, v180
	s_mov_b32 m0, s50
	ds_read_b128 v[34:37], v173 offset:16384
	ds_read_b128 v[38:41], v173 offset:17408
	ds_read_b128 v[42:45], v173 offset:18432
	ds_read_b128 v[46:49], v173 offset:19456
	ds_read_b128 v[182:185], v173 offset:20480
	ds_read_b128 v[186:189], v173 offset:21504
	ds_read_b128 v[190:193], v173 offset:22528
	ds_read_b128 v[194:197], v173 offset:23552
	s_nop 0
	global_load_lds_dwordx4 v50, s[46:47]
	v_mov_b32_e32 v50, v181
	s_mov_b32 m0, s51
	s_nop 0
	global_load_lds_dwordx4 v50, s[46:47]
	s_add_u32 s46, s40, 0xe8000
	s_addc_u32 s47, s41, 0
	v_mov_b32_e32 v50, v180
	s_mov_b32 m0, s52
	s_nop 0
	global_load_lds_dwordx4 v50, s[46:47]
	v_mov_b32_e32 v50, v181
	s_mov_b32 m0, s53
	s_nop 0
	global_load_lds_dwordx4 v50, s[46:47]
	s_waitcnt vmcnt(6)
	s_waitcnt lgkmcnt(0)
	s_barrier
	s_setprio 1
	s_waitcnt lgkmcnt(0)
	v_mfma_f32_16x16x128_f8f6f4 v[102:105], v[2:9], v[34:41], 0
	v_mfma_f32_16x16x128_f8f6f4 v[98:101], v[10:17], v[34:41], 0
	v_mfma_f32_16x16x128_f8f6f4 v[94:97], v[18:25], v[34:41], 0
	v_mfma_f32_16x16x128_f8f6f4 v[86:89], v[26:33], v[34:41], 0
	v_mfma_f32_16x16x128_f8f6f4 v[66:69], v[26:33], v[42:49], 0
	v_mfma_f32_16x16x128_f8f6f4 v[70:73], v[18:25], v[42:49], 0
	v_mfma_f32_16x16x128_f8f6f4 v[74:77], v[10:17], v[42:49], 0
	v_mfma_f32_16x16x128_f8f6f4 v[78:81], v[2:9], v[42:49], 0
	v_mfma_f32_16x16x128_f8f6f4 v[62:65], v[2:9], v[182:189], 0
	v_mfma_f32_16x16x128_f8f6f4 v[58:61], v[10:17], v[182:189], 0
	v_mfma_f32_16x16x128_f8f6f4 v[54:57], v[18:25], v[182:189], 0
	v_mfma_f32_16x16x128_f8f6f4 v[50:53], v[26:33], v[182:189], 0
	v_mfma_f32_16x16x128_f8f6f4 v[34:37], v[26:33], v[190:197], 0
	v_mfma_f32_16x16x128_f8f6f4 v[38:41], v[18:25], v[190:197], 0
	v_mfma_f32_16x16x128_f8f6f4 v[42:45], v[10:17], v[190:197], 0
	v_mfma_f32_16x16x128_f8f6f4 v[46:49], v[2:9], v[190:197], 0
	s_setprio 0
	s_barrier
	s_add_i32 s46, 0, 0x18000
	s_add_i32 s76, 0, 0x1c000
	v_add_u32_e32 v174, s46, v169
	v_add_u32_e32 v175, s76, v169
	ds_read_b128 v[26:29], v174
	ds_read_b128 v[30:33], v174 offset:1024
	ds_read_b128 v[18:21], v174 offset:2048
	ds_read_b128 v[22:25], v174 offset:3072
	ds_read_b128 v[10:13], v175
	ds_read_b128 v[14:17], v175 offset:1024
	ds_read_b128 v[2:5], v175 offset:2048
	ds_read_b128 v[6:9], v175 offset:3072
	v_mov_b32_e32 v176, v180
	s_mov_b32 m0, s49
	ds_read_b128 v[182:185], v173 offset:32768
	ds_read_b128 v[186:189], v173 offset:33792
	ds_read_b128 v[190:193], v173 offset:34816
	ds_read_b128 v[194:197], v173 offset:35840
	ds_read_b128 v[198:201], v173 offset:36864
	ds_read_b128 v[202:205], v173 offset:37888
	ds_read_b128 v[206:209], v173 offset:38912
	ds_read_b128 v[210:213], v173 offset:39936
	s_nop 0
	global_load_lds_dwordx4 v176, s[44:45]
	v_mov_b32_e32 v176, v181
	s_mov_b32 m0, s60
	s_nop 0
	global_load_lds_dwordx4 v176, s[44:45]
	s_add_u32 s44, s0, 0xe8000
	s_addc_u32 s45, s1, 0
	v_mov_b32_e32 v176, v180
	s_mov_b32 m0, s61
	s_nop 0
	global_load_lds_dwordx4 v176, s[44:45]
	v_mov_b32_e32 v176, v181
	s_mov_b32 m0, s62
	s_nop 0
	global_load_lds_dwordx4 v176, s[44:45]
	s_waitcnt vmcnt(8)
	s_waitcnt lgkmcnt(0)
	s_barrier
	s_setprio 1
	s_waitcnt lgkmcnt(0)
	v_mfma_f32_16x16x128_f8f6f4 v[146:149], v[26:33], v[182:189], v[146:149]
	v_mfma_f32_16x16x128_f8f6f4 v[150:153], v[18:25], v[182:189], v[150:153]
	v_mfma_f32_16x16x128_f8f6f4 v[154:157], v[10:17], v[182:189], v[154:157]
	v_mfma_f32_16x16x128_f8f6f4 v[158:161], v[2:9], v[182:189], v[158:161]
	v_mfma_f32_16x16x128_f8f6f4 v[130:133], v[2:9], v[190:197], v[130:133]
	v_mfma_f32_16x16x128_f8f6f4 v[134:137], v[10:17], v[190:197], v[134:137]
	v_mfma_f32_16x16x128_f8f6f4 v[138:141], v[18:25], v[190:197], v[138:141]
	v_mfma_f32_16x16x128_f8f6f4 v[142:145], v[26:33], v[190:197], v[142:145]
	v_mfma_f32_16x16x128_f8f6f4 v[126:129], v[26:33], v[198:205], v[126:129]
	v_mfma_f32_16x16x128_f8f6f4 v[122:125], v[18:25], v[198:205], v[122:125]
	v_mfma_f32_16x16x128_f8f6f4 v[118:121], v[10:17], v[198:205], v[118:121]
	v_mfma_f32_16x16x128_f8f6f4 v[114:117], v[2:9], v[198:205], v[114:117]
	v_mfma_f32_16x16x128_f8f6f4 v[82:85], v[2:9], v[206:213], v[82:85]
	v_mfma_f32_16x16x128_f8f6f4 v[90:93], v[10:17], v[206:213], v[90:93]
	v_mfma_f32_16x16x128_f8f6f4 v[106:109], v[18:25], v[206:213], v[106:109]
	v_mfma_f32_16x16x128_f8f6f4 v[110:113], v[26:33], v[206:213], v[110:113]
	s_setprio 0
	s_barrier
	v_mov_b32_e32 v176, v180
	s_add_i32 s46, s46, s33
	ds_read_b128 v[182:185], v173 offset:49152
	ds_read_b128 v[186:189], v173 offset:50176
	ds_read_b128 v[190:193], v173 offset:51200
	ds_read_b128 v[194:197], v173 offset:52224
	ds_read_b128 v[198:201], v173 offset:53248
	ds_read_b128 v[202:205], v173 offset:54272
	ds_read_b128 v[206:209], v173 offset:55296
	ds_read_b128 v[210:213], v173 offset:56320
	s_mov_b32 m0, s46
	s_add_i32 s47, s46, 0x2000
	global_load_lds_dwordx4 v176, s[42:43]
	v_mov_b32_e32 v176, v181
	s_mov_b32 m0, s47
	s_nop 0
	global_load_lds_dwordx4 v176, s[42:43]
	s_add_u32 s42, s40, 0xec000
	s_addc_u32 s43, s41, 0
	v_mov_b32_e32 v176, v180
	s_add_i32 s76, s76, s33
	s_mov_b32 m0, s76
	s_add_i32 s77, s76, 0x2000
	global_load_lds_dwordx4 v176, s[42:43]
	v_mov_b32_e32 v176, v181
	s_mov_b32 m0, s77
	s_nop 0
	global_load_lds_dwordx4 v176, s[42:43]
	s_waitcnt vmcnt(6)
	s_waitcnt lgkmcnt(0)
	s_barrier
	s_setprio 1
	s_waitcnt lgkmcnt(0)
	v_mfma_f32_16x16x128_f8f6f4 v[102:105], v[26:33], v[182:189], v[102:105]
	v_mfma_f32_16x16x128_f8f6f4 v[98:101], v[18:25], v[182:189], v[98:101]
	v_mfma_f32_16x16x128_f8f6f4 v[94:97], v[10:17], v[182:189], v[94:97]
	v_mfma_f32_16x16x128_f8f6f4 v[86:89], v[2:9], v[182:189], v[86:89]
	v_mfma_f32_16x16x128_f8f6f4 v[66:69], v[2:9], v[190:197], v[66:69]
	v_mfma_f32_16x16x128_f8f6f4 v[70:73], v[10:17], v[190:197], v[70:73]
	v_mfma_f32_16x16x128_f8f6f4 v[74:77], v[18:25], v[190:197], v[74:77]
	v_mfma_f32_16x16x128_f8f6f4 v[78:81], v[26:33], v[190:197], v[78:81]
	v_mfma_f32_16x16x128_f8f6f4 v[62:65], v[26:33], v[198:205], v[62:65]
	v_mfma_f32_16x16x128_f8f6f4 v[58:61], v[18:25], v[198:205], v[58:61]
	v_mfma_f32_16x16x128_f8f6f4 v[54:57], v[10:17], v[198:205], v[54:57]
	v_mfma_f32_16x16x128_f8f6f4 v[50:53], v[2:9], v[198:205], v[50:53]
	v_mfma_f32_16x16x128_f8f6f4 v[34:37], v[2:9], v[206:213], v[34:37]
	v_mfma_f32_16x16x128_f8f6f4 v[38:41], v[10:17], v[206:213], v[38:41]
	v_mfma_f32_16x16x128_f8f6f4 v[42:45], v[18:25], v[206:213], v[42:45]
	v_mfma_f32_16x16x128_f8f6f4 v[46:49], v[26:33], v[206:213], v[46:49]
	s_setprio 0
	s_barrier
	s_add_u32 s42, s0, 0x8000
	s_addc_u32 s43, s1, 0
	s_add_u32 s78, s40, 0x10000
	s_addc_u32 s79, s41, 0
	s_mov_b32 s80, 0
	.p2align	6

.LBB0_1610:
	s_lshl_b32 s4, s4, 5
	s_and_b32 s51, 0xffff, s33
	s_lshl_b32 s6, s3, 13
	s_and_b32 s7, s4, 0x60
	s_add_u32 s4, s18, 0x4000
	s_addc_u32 s5, s19, 0
	v_mov_b32_e32 v2, v180
	s_waitcnt vmcnt(2)
	s_barrier
	s_add_i32 m0, s42, 0x18000
	v_lshlrev_b32_e32 v3, 2, v165
	global_load_lds_dwordx4 v2, s[4:5]
	v_mov_b32_e32 v2, v181
	s_add_i32 m0, s42, 0x1a000
	v_and_b32_e32 v3, 32, v3
	global_load_lds_dwordx4 v2, s[4:5]
	s_add_u32 s4, s18, 0xe4000
	s_addc_u32 s5, s19, 0
	v_mov_b32_e32 v2, v180
	s_add_i32 m0, s42, 0x1c000
	v_mov_b32_e32 v163, 0
	global_load_lds_dwordx4 v2, s[4:5]
	v_mov_b32_e32 v2, v181
	s_add_i32 m0, s42, 0x1e000
	s_cmpk_lt_u32 s2, 0x100
	global_load_lds_dwordx4 v2, s[4:5]
	v_lshl_or_b32 v2, v165, 6, v166
	v_bitop3_b32 v4, v2, s6, v3 bitop3:0xde
	v_or_b32_e32 v2, s7, v164
	v_lshlrev_b32_e32 v2, 2, v2
	v_mov_b32_e32 v3, v163
	v_lshl_or_b32 v182, s3, 6, v165
	v_lshl_or_b32 v183, s7, 7, v167
	s_waitcnt vmcnt(6)
	s_cselect_b64 s[2:3], -1, 0
	v_lshl_add_u64 v[2:3], s[56:57], 0, v[2:3]
	s_mov_b64 s[4:5], 0x46b00000
	s_add_i32 s62, 0, 0x18000
	s_add_i32 s63, 0, 0x1c000
	v_or_b32_e32 v184, 16, v182
	v_or_b32_e32 v185, 32, v182
	v_or_b32_e32 v186, 48, v182
	v_add_u32_e32 v187, 0x80, v182
	v_add_u32_e32 v188, 0x90, v182
	v_add_u32_e32 v189, 0xa0, v182
	v_add_u32_e32 v190, 0xb0, v182
	v_lshl_add_u64 v[178:179], v[2:3], 0, s[4:5]
	v_add_u32_e32 v2, 0, v183
	s_add_i32 s64, s62, s40
	s_add_i32 s66, s63, s40
	v_lshlrev_b32_e32 v162, 8, v182
	v_lshlrev_b32_e32 v164, 8, v184
	v_mov_b32_e32 v165, v163
	v_lshlrev_b32_e32 v166, 8, v185
	v_mov_b32_e32 v167, v163
	v_lshlrev_b32_e32 v168, 8, v186
	v_mov_b32_e32 v169, v163
	v_lshlrev_b32_e32 v170, 8, v187
	v_mov_b32_e32 v171, v163
	v_lshlrev_b32_e32 v172, 8, v188
	v_mov_b32_e32 v173, v163
	v_lshlrev_b32_e32 v174, 8, v189
	v_mov_b32_e32 v175, v163
	v_lshlrev_b32_e32 v176, 8, v190
	v_mov_b32_e32 v177, v163
	v_add_u32_e32 v191, 0x10000, v2
	v_add_u32_e32 v192, 0x14000, v2
	v_add_u32_e32 v193, 0, v4
	s_add_i32 s52, s42, 0x8000
	s_add_i32 s53, s42, 0xa000
	s_add_i32 s60, s42, 0xc000
	s_add_i32 s61, s42, 0xe000
	s_add_i32 s65, s64, 0x2000
	s_add_i32 s67, s66, 0x2000
	s_mov_b32 s14, s12
	s_mov_b64 s[4:5], s[16:17]
	s_mov_b64 s[6:7], s[18:19]
	s_barrier
	s_branch .LBB0_1613
	.p2align	6
.LBB0_1611:
	s_mov_b64 s[8:9], 0
	.p2align	6

.LBB0_1615:
	s_add_u32 s30, s16, 0x8000
	s_addc_u32 s31, s17, 0
	s_waitcnt vmcnt(8)
	s_add_u32 s38, s18, 0x8000
	s_waitcnt lgkmcnt(0)
	s_addc_u32 s39, s19, 0
	s_add_u32 s24, s18, 0xc000
	s_addc_u32 s25, s19, 0
	s_barrier
	s_setprio 1
	s_waitcnt lgkmcnt(0)
	v_mfma_f32_16x16x128_f8f6f4 v[146:149], v[2:9], v[58:65], 0
	v_mfma_f32_16x16x128_f8f6f4 v[150:153], v[10:17], v[58:65], 0
	v_mfma_f32_16x16x128_f8f6f4 v[154:157], v[18:25], v[58:65], 0
	v_mfma_f32_16x16x128_f8f6f4 v[158:161], v[26:33], v[58:65], 0
	v_mfma_f32_16x16x128_f8f6f4 v[130:133], v[26:33], v[50:57], 0
	v_mfma_f32_16x16x128_f8f6f4 v[134:137], v[18:25], v[50:57], 0
	v_mfma_f32_16x16x128_f8f6f4 v[138:141], v[10:17], v[50:57], 0
	v_mfma_f32_16x16x128_f8f6f4 v[142:145], v[2:9], v[50:57], 0
	v_mfma_f32_16x16x128_f8f6f4 v[126:129], v[2:9], v[42:49], 0
	v_mfma_f32_16x16x128_f8f6f4 v[122:125], v[10:17], v[42:49], 0
	v_mfma_f32_16x16x128_f8f6f4 v[118:121], v[18:25], v[42:49], 0
	v_mfma_f32_16x16x128_f8f6f4 v[114:117], v[26:33], v[42:49], 0
	v_mfma_f32_16x16x128_f8f6f4 v[98:101], v[26:33], v[34:41], 0
	v_mfma_f32_16x16x128_f8f6f4 v[102:105], v[18:25], v[34:41], 0
	v_mfma_f32_16x16x128_f8f6f4 v[106:109], v[10:17], v[34:41], 0
	v_mfma_f32_16x16x128_f8f6f4 v[110:113], v[2:9], v[34:41], 0
	s_setprio 0
	s_barrier
	v_mov_b32_e32 v50, v180
	s_mov_b32 m0, s43
	ds_read_b128 v[34:37], v193 offset:16384
	ds_read_b128 v[38:41], v193 offset:17408
	ds_read_b128 v[42:45], v193 offset:18432
	ds_read_b128 v[46:49], v193 offset:19456
	ds_read_b128 v[194:197], v193 offset:20480
	ds_read_b128 v[198:201], v193 offset:21504
	ds_read_b128 v[202:205], v193 offset:22528
	ds_read_b128 v[206:209], v193 offset:23552
	s_nop 0
	global_load_lds_dwordx4 v50, s[38:39]
	v_mov_b32_e32 v50, v181
	s_mov_b32 m0, s44
	s_nop 0
	global_load_lds_dwordx4 v50, s[38:39]
	s_add_u32 s38, s18, 0xe8000
	s_addc_u32 s39, s19, 0
	v_mov_b32_e32 v50, v180
	s_mov_b32 m0, s45
	s_nop 0
	global_load_lds_dwordx4 v50, s[38:39]
	v_mov_b32_e32 v50, v181
	s_mov_b32 m0, s46
	s_nop 0
	global_load_lds_dwordx4 v50, s[38:39]
	s_waitcnt vmcnt(6)
	s_waitcnt lgkmcnt(0)
	s_barrier
	s_setprio 1
	s_waitcnt lgkmcnt(0)
	v_mfma_f32_16x16x128_f8f6f4 v[94:97], v[2:9], v[34:41], 0
	v_mfma_f32_16x16x128_f8f6f4 v[90:93], v[10:17], v[34:41], 0
	v_mfma_f32_16x16x128_f8f6f4 v[86:89], v[18:25], v[34:41], 0
	v_mfma_f32_16x16x128_f8f6f4 v[82:85], v[26:33], v[34:41], 0
	v_mfma_f32_16x16x128_f8f6f4 v[66:69], v[26:33], v[42:49], 0
	v_mfma_f32_16x16x128_f8f6f4 v[70:73], v[18:25], v[42:49], 0
	v_mfma_f32_16x16x128_f8f6f4 v[74:77], v[10:17], v[42:49], 0
	v_mfma_f32_16x16x128_f8f6f4 v[78:81], v[2:9], v[42:49], 0
	v_mfma_f32_16x16x128_f8f6f4 v[62:65], v[2:9], v[194:201], 0
	v_mfma_f32_16x16x128_f8f6f4 v[58:61], v[10:17], v[194:201], 0
	v_mfma_f32_16x16x128_f8f6f4 v[54:57], v[18:25], v[194:201], 0
	v_mfma_f32_16x16x128_f8f6f4 v[50:53], v[26:33], v[194:201], 0
	v_mfma_f32_16x16x128_f8f6f4 v[34:37], v[26:33], v[202:209], 0
	v_mfma_f32_16x16x128_f8f6f4 v[38:41], v[18:25], v[202:209], 0
	v_mfma_f32_16x16x128_f8f6f4 v[42:45], v[10:17], v[202:209], 0
	v_mfma_f32_16x16x128_f8f6f4 v[46:49], v[2:9], v[202:209], 0
	s_setprio 0
	s_barrier
	v_add_u32_e32 v194, s62, v183
	v_add_u32_e32 v195, s63, v183
	ds_read_b128 v[26:29], v194
	ds_read_b128 v[30:33], v194 offset:1024
	ds_read_b128 v[18:21], v194 offset:2048
	ds_read_b128 v[22:25], v194 offset:3072
	ds_read_b128 v[10:13], v195
	ds_read_b128 v[14:17], v195 offset:1024
	ds_read_b128 v[2:5], v195 offset:2048
	ds_read_b128 v[6:9], v195 offset:3072
	v_mov_b32_e32 v228, v180
	s_mov_b32 m0, s42
	ds_read_b128 v[196:199], v193 offset:32768
	ds_read_b128 v[200:203], v193 offset:33792
	ds_read_b128 v[204:207], v193 offset:34816
	ds_read_b128 v[208:211], v193 offset:35840
	ds_read_b128 v[212:215], v193 offset:36864
	ds_read_b128 v[216:219], v193 offset:37888
	ds_read_b128 v[220:223], v193 offset:38912
	ds_read_b128 v[224:227], v193 offset:39936
	s_nop 0
	global_load_lds_dwordx4 v228, s[30:31]
	v_mov_b32_e32 v228, v181
	s_mov_b32 m0, s47
	s_nop 0
	global_load_lds_dwordx4 v228, s[30:31]
	s_add_u32 s30, s16, 0xe8000
	s_addc_u32 s31, s17, 0
	v_mov_b32_e32 v228, v180
	s_mov_b32 m0, s48
	s_nop 0
	global_load_lds_dwordx4 v228, s[30:31]
	v_mov_b32_e32 v228, v181
	s_mov_b32 m0, s49
	s_nop 0
	global_load_lds_dwordx4 v228, s[30:31]
	s_waitcnt vmcnt(8)
	s_waitcnt lgkmcnt(0)
	s_barrier
	s_setprio 1
	s_waitcnt lgkmcnt(0)
	v_mfma_f32_16x16x128_f8f6f4 v[146:149], v[26:33], v[196:203], v[146:149]
	v_mfma_f32_16x16x128_f8f6f4 v[150:153], v[18:25], v[196:203], v[150:153]
	v_mfma_f32_16x16x128_f8f6f4 v[154:157], v[10:17], v[196:203], v[154:157]
	v_mfma_f32_16x16x128_f8f6f4 v[158:161], v[2:9], v[196:203], v[158:161]
	v_mfma_f32_16x16x128_f8f6f4 v[130:133], v[2:9], v[204:211], v[130:133]
	v_mfma_f32_16x16x128_f8f6f4 v[134:137], v[10:17], v[204:211], v[134:137]
	v_mfma_f32_16x16x128_f8f6f4 v[138:141], v[18:25], v[204:211], v[138:141]
	v_mfma_f32_16x16x128_f8f6f4 v[142:145], v[26:33], v[204:211], v[142:145]
	v_mfma_f32_16x16x128_f8f6f4 v[126:129], v[26:33], v[212:219], v[126:129]
	v_mfma_f32_16x16x128_f8f6f4 v[122:125], v[18:25], v[212:219], v[122:125]
	v_mfma_f32_16x16x128_f8f6f4 v[118:121], v[10:17], v[212:219], v[118:121]
	v_mfma_f32_16x16x128_f8f6f4 v[114:117], v[2:9], v[212:219], v[114:117]
	v_mfma_f32_16x16x128_f8f6f4 v[98:101], v[2:9], v[220:227], v[98:101]
	v_mfma_f32_16x16x128_f8f6f4 v[102:105], v[10:17], v[220:227], v[102:105]
	v_mfma_f32_16x16x128_f8f6f4 v[106:109], v[18:25], v[220:227], v[106:109]
	v_mfma_f32_16x16x128_f8f6f4 v[110:113], v[26:33], v[220:227], v[110:113]
	s_setprio 0
	s_barrier
	v_mov_b32_e32 v228, v180
	s_mov_b32 m0, s64
	ds_read_b128 v[196:199], v193 offset:49152
	ds_read_b128 v[200:203], v193 offset:50176
	ds_read_b128 v[204:207], v193 offset:51200
	ds_read_b128 v[208:211], v193 offset:52224
	ds_read_b128 v[212:215], v193 offset:53248
	ds_read_b128 v[216:219], v193 offset:54272
	ds_read_b128 v[220:223], v193 offset:55296
	ds_read_b128 v[224:227], v193 offset:56320
	s_nop 0
	global_load_lds_dwordx4 v228, s[24:25]
	v_mov_b32_e32 v228, v181
	s_mov_b32 m0, s65
	s_nop 0
	global_load_lds_dwordx4 v228, s[24:25]
	s_add_u32 s24, s18, 0xec000
	s_addc_u32 s25, s19, 0
	v_mov_b32_e32 v228, v180
	s_mov_b32 m0, s66
	s_nop 0
	global_load_lds_dwordx4 v228, s[24:25]
	v_mov_b32_e32 v228, v181
	s_mov_b32 m0, s67
	s_nop 0
	global_load_lds_dwordx4 v228, s[24:25]
	s_waitcnt vmcnt(6)
	s_waitcnt lgkmcnt(0)
	s_barrier
	s_setprio 1
	s_waitcnt lgkmcnt(0)
	v_mfma_f32_16x16x128_f8f6f4 v[94:97], v[26:33], v[196:203], v[94:97]
	v_mfma_f32_16x16x128_f8f6f4 v[90:93], v[18:25], v[196:203], v[90:93]
	v_mfma_f32_16x16x128_f8f6f4 v[86:89], v[10:17], v[196:203], v[86:89]
	v_mfma_f32_16x16x128_f8f6f4 v[82:85], v[2:9], v[196:203], v[82:85]
	v_mfma_f32_16x16x128_f8f6f4 v[66:69], v[2:9], v[204:211], v[66:69]
	v_mfma_f32_16x16x128_f8f6f4 v[70:73], v[10:17], v[204:211], v[70:73]
	v_mfma_f32_16x16x128_f8f6f4 v[74:77], v[18:25], v[204:211], v[74:77]
	v_mfma_f32_16x16x128_f8f6f4 v[78:81], v[26:33], v[204:211], v[78:81]
	v_mfma_f32_16x16x128_f8f6f4 v[62:65], v[26:33], v[212:219], v[62:65]
	v_mfma_f32_16x16x128_f8f6f4 v[58:61], v[18:25], v[212:219], v[58:61]
	v_mfma_f32_16x16x128_f8f6f4 v[54:57], v[10:17], v[212:219], v[54:57]
	v_mfma_f32_16x16x128_f8f6f4 v[50:53], v[2:9], v[212:219], v[50:53]
	v_mfma_f32_16x16x128_f8f6f4 v[34:37], v[2:9], v[220:227], v[34:37]
	v_mfma_f32_16x16x128_f8f6f4 v[38:41], v[10:17], v[220:227], v[38:41]
	v_mfma_f32_16x16x128_f8f6f4 v[42:45], v[18:25], v[220:227], v[42:45]
	v_mfma_f32_16x16x128_f8f6f4 v[46:49], v[26:33], v[220:227], v[46:49]
	s_setprio 0
	s_barrier
	s_add_u32 s30, s18, 0x10000
	s_addc_u32 s31, s19, 0
	s_add_u32 s38, s16, 0x10000
	s_addc_u32 s39, s17, 0
	s_mov_b32 s71, 4
	.p2align	6
